# v104 plus removal of 190 dead zero-initialising moves ahead of packed fp8 conversion pairs
# baseline (speedup 1.0000x reference)
; #define CVT_PK_FP8_SAT(a, b, old, hi) __builtin_amdgcn_cvt_pk_fp8_f32(__builtin_amdgcn_fmed3f((a), -448.0f, 448.0f), __builtin_amdgcn_fmed3f((b), -448.0f, 448.0f), (old), (hi))
;     __device__ __forceinline__ void operator()(const f32x4 (&acc)[2][2][4][2], const Unit& u, int wr, int wc, int fr, int fq) const {
;     ...
;         const int row0 = u.pm * BM + wr * 64 + fr, col0 = u.pn * BM + wc * 32 + 8 * fq;
; #pragma unroll
;         for (int ai = 0; ai < 2; ++ai) {
;             u32x2 p8[4][2];
; #pragma unroll
;             for (int m = 0; m < 4; ++m)
; #pragma unroll
;                 for (int bj = 0; bj < 2; ++bj) {
;                     const f32x4 v0 = acc[ai][bj][m][0] * cs, v1 = acc[ai][bj][m][1] * cs;
;                     int a = CVT_PK_FP8_SAT(v0[0], v0[1], 0, false); a = CVT_PK_FP8_SAT(v0[2], v0[3], a, true);
;                     int b = CVT_PK_FP8_SAT(v1[0], v1[1], 0, false); b = CVT_PK_FP8_SAT(v1[2], v1[3], b, true);
;                     p8[m][bj].x = (unsigned)a; p8[m][bj].y = (unsigned)b;
;                 }
.LBB0_285:
	s_mov_b32 s10, 0x3c800000
	v_pk_mul_f32 v[126:127], v[126:127], s[10:11] op_sel_hi:[1,0]
	v_mov_b32_e32 v219, 0x43e00000
	v_pk_mul_f32 v[128:129], v[128:129], s[10:11] op_sel_hi:[1,0]
	v_pk_mul_f32 v[138:139], v[122:123], s[10:11] op_sel_hi:[1,0]
	v_med3_f32 v123, v126, s97, v219
	v_med3_f32 v126, v127, s97, v219
	v_mov_b32_e32 v122, v65
	v_cvt_pk_fp8_f32 v122, v123, v126
	v_med3_f32 v126, v128, s97, v219
	v_med3_f32 v127, v129, s97, v219
	v_med3_f32 v128, v138, s97, v219
	v_med3_f32 v129, v139, s97, v219
	v_cvt_pk_fp8_f32 v123, v128, v129
	v_pk_mul_f32 v[124:125], v[124:125], s[10:11] op_sel_hi:[1,0]
	v_pk_mul_f32 v[118:119], v[118:119], s[10:11] op_sel_hi:[1,0]
	v_med3_f32 v124, v124, s97, v219
	v_med3_f32 v125, v125, s97, v219
	v_cvt_pk_fp8_f32 v123, v124, v125 op_sel:[0,0,1]
	v_pk_mul_f32 v[120:121], v[120:121], s[10:11] op_sel_hi:[1,0]
	v_pk_mul_f32 v[124:125], v[110:111], s[10:11] op_sel_hi:[1,0]
	v_med3_f32 v111, v118, s97, v219
	v_med3_f32 v118, v119, s97, v219
	v_cvt_pk_fp8_f32 v110, v111, v118
	v_med3_f32 v118, v120, s97, v219
	v_med3_f32 v119, v121, s97, v219
	v_med3_f32 v120, v124, s97, v219
	v_med3_f32 v121, v125, s97, v219
	v_cvt_pk_fp8_f32 v111, v120, v121
	v_pk_mul_f32 v[114:115], v[114:115], s[10:11] op_sel_hi:[1,0]
	v_med3_f32 v114, v114, s97, v219
	v_med3_f32 v115, v115, s97, v219
	v_pk_mul_f32 v[112:113], v[112:113], s[10:11] op_sel_hi:[1,0]
	v_cvt_pk_fp8_f32 v124, v114, v115
	v_med3_f32 v112, v112, s97, v219
	v_med3_f32 v113, v113, s97, v219
	v_cvt_pk_fp8_f32 v111, v112, v113 op_sel:[0,0,1]
	v_pk_mul_f32 v[112:113], v[116:117], s[10:11] op_sel_hi:[1,0]
	v_pk_mul_f32 v[94:95], v[94:95], s[10:11] op_sel_hi:[1,0]
	v_med3_f32 v112, v112, s97, v219
	v_med3_f32 v113, v113, s97, v219
	v_cvt_pk_fp8_f32 v124, v112, v113 op_sel:[0,0,1]
	v_pk_mul_f32 v[96:97], v[96:97], s[10:11] op_sel_hi:[1,0]
	v_med3_f32 v94, v94, s97, v219
	v_med3_f32 v95, v95, s97, v219
	v_cvt_pk_fp8_f32 v113, v94, v95
	v_med3_f32 v94, v96, s97, v219
	v_med3_f32 v95, v97, s97, v219
	v_pk_mul_f32 v[96:97], v[98:99], s[10:11] op_sel_hi:[1,0]
	v_pk_mul_f32 v[98:99], v[90:91], s[10:11] op_sel_hi:[1,0]
	v_med3_f32 v91, v96, s97, v219
	v_med3_f32 v96, v97, s97, v219
	v_cvt_pk_fp8_f32 v90, v91, v96
	v_med3_f32 v96, v98, s97, v219
	v_med3_f32 v97, v99, s97, v219
	v_cvt_pk_fp8_f32 v91, v96, v97
	v_pk_mul_f32 v[92:93], v[92:93], s[10:11] op_sel_hi:[1,0]
	v_pk_mul_f32 v[86:87], v[86:87], s[10:11] op_sel_hi:[1,0]
	v_med3_f32 v92, v92, s97, v219
	v_med3_f32 v93, v93, s97, v219
	v_cvt_pk_fp8_f32 v91, v92, v93 op_sel:[0,0,1]
	v_pk_mul_f32 v[88:89], v[88:89], s[10:11] op_sel_hi:[1,0]
	v_pk_mul_f32 v[92:93], v[78:79], s[10:11] op_sel_hi:[1,0]
	v_med3_f32 v79, v86, s97, v219
	v_med3_f32 v86, v87, s97, v219
	v_cvt_pk_fp8_f32 v78, v79, v86
	v_med3_f32 v86, v88, s97, v219
	v_med3_f32 v87, v89, s97, v219
	v_med3_f32 v88, v92, s97, v219
	v_med3_f32 v89, v93, s97, v219
	v_cvt_pk_fp8_f32 v79, v88, v89
	v_pk_mul_f32 v[82:83], v[82:83], s[10:11] op_sel_hi:[1,0]
	v_med3_f32 v82, v82, s97, v219
	v_med3_f32 v83, v83, s97, v219
	v_pk_mul_f32 v[80:81], v[80:81], s[10:11] op_sel_hi:[1,0]
	v_cvt_pk_fp8_f32 v92, v82, v83
	v_pk_mul_f32 v[106:107], v[106:107], s[10:11] op_sel_hi:[1,0]
	v_pk_mul_f32 v[102:103], v[102:103], s[10:11] op_sel_hi:[1,0]
	v_med3_f32 v80, v80, s97, v219
	v_med3_f32 v81, v81, s97, v219
	v_med3_f32 v106, v106, s97, v219
	v_med3_f32 v107, v107, s97, v219
	v_med3_f32 v102, v102, s97, v219
	v_med3_f32 v103, v103, s97, v219
	v_cvt_pk_fp8_f32 v79, v80, v81 op_sel:[0,0,1]
	v_pk_mul_f32 v[80:81], v[84:85], s[10:11] op_sel_hi:[1,0]
	v_mbcnt_lo_u32_b32 v64, -1, 0
	v_mbcnt_hi_u32_b32 v64, -1, v64
	v_cvt_pk_fp8_f32 v125, v106, v107
	v_cvt_pk_fp8_f32 v112, v102, v103
	v_med3_f32 v80, v80, s97, v219
	v_med3_f32 v81, v81, s97, v219
	v_pk_mul_f32 v[66:67], v[66:67], s[10:11] op_sel_hi:[1,0]
	v_add_u32_e32 v64, s93, v64
	s_lshl_b32 s13, s20, 8
	v_pk_mul_f32 v[74:75], v[74:75], s[10:11] op_sel_hi:[1,0]
	v_cvt_pk_fp8_f32 v92, v80, v81 op_sel:[0,0,1]
	v_pk_mul_f32 v[70:71], v[70:71], s[10:11] op_sel_hi:[1,0]
	v_med3_f32 v66, v66, s97, v219
	v_med3_f32 v67, v67, s97, v219
	s_add_i32 s13, s13, s41
	v_pk_mul_f32 v[108:109], v[108:109], s[10:11] op_sel_hi:[1,0]
	v_pk_mul_f32 v[104:105], v[104:105], s[10:11] op_sel_hi:[1,0]
	v_med3_f32 v74, v74, s97, v219
	v_med3_f32 v75, v75, s97, v219
	v_med3_f32 v70, v70, s97, v219
	v_med3_f32 v71, v71, s97, v219
	v_cvt_pk_fp8_f32 v81, v66, v67
	v_bfe_u32 v137, v64, 4, 2
	v_and_or_b32 v140, v64, 15, s13
	v_bfe_u32 v64, v64, 4, 1
	v_med3_f32 v106, v108, s97, v219
	v_med3_f32 v107, v109, s97, v219
	v_med3_f32 v102, v104, s97, v219
	v_med3_f32 v103, v105, s97, v219
	v_cvt_pk_fp8_f32 v93, v74, v75
	v_cvt_pk_fp8_f32 v80, v70, v71
	s_lshl_b32 s13, s46, 8
	v_lshlrev_b32_e32 v131, 3, v64
	v_cvt_pk_fp8_f32 v122, v126, v127 op_sel:[0,0,1]
	v_cvt_pk_fp8_f32 v110, v118, v119 op_sel:[0,0,1]
	v_cvt_pk_fp8_f32 v125, v106, v107 op_sel:[0,0,1]
	v_cvt_pk_fp8_f32 v112, v102, v103 op_sel:[0,0,1]
	v_cvt_pk_fp8_f32 v113, v94, v95 op_sel:[0,0,1]
	v_pk_mul_f32 v[68:69], v[68:69], s[10:11] op_sel_hi:[1,0]
	v_lshl_or_b32 v130, v137, 3, s13
	v_sub_u32_e32 v131, s42, v131
	v_pk_mul_f32 v[94:95], v[100:101], s[10:11] op_sel_hi:[1,0]
	v_pk_mul_f32 v[76:77], v[76:77], s[10:11] op_sel_hi:[1,0]
	v_pk_mul_f32 v[72:73], v[72:73], s[10:11] op_sel_hi:[1,0]
	v_med3_f32 v66, v68, s97, v219
	v_med3_f32 v67, v69, s97, v219
	v_lshlrev_b32_e32 v64, 4, v64
	v_add_u32_e32 v130, v130, v131
	v_med3_f32 v94, v94, s97, v219
	v_med3_f32 v95, v95, s97, v219
	v_med3_f32 v74, v76, s97, v219
	v_med3_f32 v75, v77, s97, v219
	v_med3_f32 v70, v72, s97, v219
	v_med3_f32 v71, v73, s97, v219
; #define CVT_PK_FP8_SAT(a, b, old, hi) __builtin_amdgcn_cvt_pk_fp8_f32(__builtin_amdgcn_fmed3f((a), -448.0f, 448.0f), __builtin_amdgcn_fmed3f((b), -448.0f, 448.0f), (old), (hi))
;     __device__ __forceinline__ void operator()(const f32x4 (&acc)[2][2][4][2], const Unit& u, int wr, int wc, int fr, int fq) const {
;     ...
;         for (int ai = 0; ai < 2; ++ai) {
;             u32x2 p8[4][2];
; #pragma unroll
;             for (int m = 0; m < 4; ++m)
; #pragma unroll
;                 for (int bj = 0; bj < 2; ++bj) {
;                     const f32x4 v0 = acc[ai][bj][m][0] * cs, v1 = acc[ai][bj][m][1] * cs;
;                     int a = CVT_PK_FP8_SAT(v0[0], v0[1], 0, false); a = CVT_PK_FP8_SAT(v0[2], v0[3], a, true);
;                     int b = CVT_PK_FP8_SAT(v1[0], v1[1], 0, false); b = CVT_PK_FP8_SAT(v1[2], v1[3], b, true);
;                     p8[m][bj].x = (unsigned)a; p8[m][bj].y = (unsigned)b;
;                 }
; #pragma unroll
;             for (int mp = 0; mp < 2; ++mp)
; #pragma unroll
;                 for (int bj = 0; bj < 2; ++bj) {
;                     auto r0 = __builtin_amdgcn_permlane16_swap(p8[2 * mp][bj].x, p8[2 * mp + 1][bj].x, false, false);
;                     auto r1 = __builtin_amdgcn_permlane16_swap(p8[2 * mp][bj].y, p8[2 * mp + 1][bj].y, false, false);
;                     u32x4 w8 = {r0[0], r1[0], r0[1], r1[1]};
;                     const int rowx = row0 + ai * HALF + (2 * mp + (fq & 1)) * 16, colx = col0 - (fq & 1) * 8 + bj * HALF;
;                     *(u32x4*)(O + (size_t)rowx * ldc + colx) = w8; }
	v_cvt_pk_fp8_f32 v81, v66, v67 op_sel:[0,0,1]
	v_or_b32_e32 v68, v64, v140
	v_mov_b64_e32 v[66:67], s[8:9]
	s_movk_i32 s13, 0x2400
	v_cvt_pk_fp8_f32 v90, v94, v95 op_sel:[0,0,1]
	v_cvt_pk_fp8_f32 v78, v86, v87 op_sel:[0,0,1]
	v_cvt_pk_fp8_f32 v93, v74, v75 op_sel:[0,0,1]
	v_cvt_pk_fp8_f32 v80, v70, v71 op_sel:[0,0,1]
	v_mad_i64_i32 v[68:69], s[22:23], v68, s13, v[66:67]
	v_ashrrev_i32_e32 v131, 31, v130
	v_permlane16_swap_b32_e32 v122, v124
	v_permlane16_swap_b32_e32 v123, v125
	v_lshl_add_u64 v[68:69], v[68:69], 0, v[130:131]
	v_permlane16_swap_b32_e32 v110, v112
	v_permlane16_swap_b32_e32 v111, v113
	v_lshl_or_b32 v70, v137, 4, 32
	global_store_dwordx4 v[68:69], v[122:125], off
	global_store_dwordx4 v[68:69], v[110:113], off offset:128
	v_or_b32_e32 v68, v70, v140
	v_mad_i64_i32 v[68:69], s[22:23], v68, s13, v[66:67]
	v_permlane16_swap_b32_e32 v90, v92
	v_permlane16_swap_b32_e32 v91, v93
	v_lshl_add_u64 v[68:69], v[68:69], 0, v[130:131]
	v_permlane16_swap_b32_e32 v78, v80
	v_permlane16_swap_b32_e32 v79, v81
	v_pk_mul_f32 v[60:61], v[60:61], s[10:11] op_sel_hi:[1,0]
	global_store_dwordx4 v[68:69], v[90:93], off
	global_store_dwordx4 v[68:69], v[78:81], off offset:128
	v_pk_mul_f32 v[62:63], v[62:63], s[10:11] op_sel_hi:[1,0]
	v_pk_mul_f32 v[68:69], v[48:49], s[10:11] op_sel_hi:[1,0]
	v_med3_f32 v49, v60, s97, v219
	v_med3_f32 v60, v61, s97, v219
	v_mov_b32_e32 v48, v65
	v_cvt_pk_fp8_f32 v48, v49, v60
	v_med3_f32 v60, v62, s97, v219
	v_med3_f32 v61, v63, s97, v219
	v_med3_f32 v62, v68, s97, v219
	v_med3_f32 v63, v69, s97, v219
	v_cvt_pk_fp8_f32 v49, v62, v63
	v_pk_mul_f32 v[50:51], v[50:51], s[10:11] op_sel_hi:[1,0]
	v_pk_mul_f32 v[36:37], v[36:37], s[10:11] op_sel_hi:[1,0]
	v_med3_f32 v50, v50, s97, v219
	v_med3_f32 v51, v51, s97, v219
	v_cvt_pk_fp8_f32 v49, v50, v51 op_sel:[0,0,1]
	v_pk_mul_f32 v[38:39], v[38:39], s[10:11] op_sel_hi:[1,0]
	v_pk_mul_f32 v[50:51], v[24:25], s[10:11] op_sel_hi:[1,0]
	v_med3_f32 v25, v36, s97, v219
	v_med3_f32 v36, v37, s97, v219
	v_cvt_pk_fp8_f32 v24, v25, v36
	v_med3_f32 v36, v38, s97, v219
	v_med3_f32 v37, v39, s97, v219
	v_med3_f32 v38, v50, s97, v219
	v_med3_f32 v39, v51, s97, v219
	v_cvt_pk_fp8_f32 v25, v38, v39
	v_pk_mul_f32 v[32:33], v[32:33], s[10:11] op_sel_hi:[1,0]
	v_pk_mul_f32 v[28:29], v[28:29], s[10:11] op_sel_hi:[1,0]
	v_med3_f32 v32, v32, s97, v219
	v_med3_f32 v33, v33, s97, v219
	v_pk_mul_f32 v[26:27], v[26:27], s[10:11] op_sel_hi:[1,0]
	v_cvt_pk_fp8_f32 v50, v32, v33
	v_med3_f32 v28, v28, s97, v219
	v_med3_f32 v29, v29, s97, v219
	v_med3_f32 v26, v26, s97, v219
	v_med3_f32 v27, v27, s97, v219
	v_cvt_pk_fp8_f32 v51, v28, v29
	v_cvt_pk_fp8_f32 v25, v26, v27 op_sel:[0,0,1]
	v_pk_mul_f32 v[26:27], v[34:35], s[10:11] op_sel_hi:[1,0]
	v_pk_mul_f32 v[30:31], v[30:31], s[10:11] op_sel_hi:[1,0]
	v_med3_f32 v26, v26, s97, v219
	v_med3_f32 v27, v27, s97, v219
	v_cvt_pk_fp8_f32 v50, v26, v27 op_sel:[0,0,1]
	v_med3_f32 v26, v30, s97, v219
	v_med3_f32 v27, v31, s97, v219
	v_cvt_pk_fp8_f32 v51, v26, v27 op_sel:[0,0,1]
	v_pk_mul_f32 v[26:27], v[52:53], s[10:11] op_sel_hi:[1,0]
	v_pk_mul_f32 v[32:33], v[56:57], s[10:11] op_sel_hi:[1,0]
	v_med3_f32 v34, v26, s97, v219
	v_med3_f32 v27, v27, s97, v219
	v_cvt_pk_fp8_f32 v26, v34, v27
	v_med3_f32 v32, v32, s97, v219
	v_med3_f32 v33, v33, s97, v219
	v_cvt_pk_fp8_f32 v27, v32, v33
	v_pk_mul_f32 v[28:29], v[54:55], s[10:11] op_sel_hi:[1,0]
	v_pk_mul_f32 v[30:31], v[58:59], s[10:11] op_sel_hi:[1,0]
	v_med3_f32 v28, v28, s97, v219
	v_med3_f32 v29, v29, s97, v219
	v_cvt_pk_fp8_f32 v26, v28, v29 op_sel:[0,0,1]
	v_med3_f32 v28, v30, s97, v219
	v_med3_f32 v29, v31, s97, v219
	v_pk_mul_f32 v[12:13], v[12:13], s[10:11] op_sel_hi:[1,0]
; #define CVT_PK_FP8_SAT(a, b, old, hi) __builtin_amdgcn_cvt_pk_fp8_f32(__builtin_amdgcn_fmed3f((a), -448.0f, 448.0f), __builtin_amdgcn_fmed3f((b), -448.0f, 448.0f), (old), (hi))
;     __device__ __forceinline__ void operator()(const f32x4 (&acc)[2][2][4][2], const Unit& u, int wr, int wc, int fr, int fq) const {
;     ...
; #pragma unroll
;         for (int ai = 0; ai < 2; ++ai) {
;             u32x2 p8[4][2];
; #pragma unroll
;             for (int m = 0; m < 4; ++m)
; #pragma unroll
;                 for (int bj = 0; bj < 2; ++bj) {
;                     const f32x4 v0 = acc[ai][bj][m][0] * cs, v1 = acc[ai][bj][m][1] * cs;
;                     int a = CVT_PK_FP8_SAT(v0[0], v0[1], 0, false); a = CVT_PK_FP8_SAT(v0[2], v0[3], a, true);
;                     int b = CVT_PK_FP8_SAT(v1[0], v1[1], 0, false); b = CVT_PK_FP8_SAT(v1[2], v1[3], b, true);
;                     p8[m][bj].x = (unsigned)a; p8[m][bj].y = (unsigned)b;
;                 }
; #pragma unroll
;             for (int mp = 0; mp < 2; ++mp)
; #pragma unroll
;                 for (int bj = 0; bj < 2; ++bj) {
;                     auto r0 = __builtin_amdgcn_permlane16_swap(p8[2 * mp][bj].x, p8[2 * mp + 1][bj].x, false, false);
;                     auto r1 = __builtin_amdgcn_permlane16_swap(p8[2 * mp][bj].y, p8[2 * mp + 1][bj].y, false, false);
;                     u32x4 w8 = {r0[0], r1[0], r0[1], r1[1]};
;                     const int rowx = row0 + ai * HALF + (2 * mp + (fq & 1)) * 16, colx = col0 - (fq & 1) * 8 + bj * HALF;
;                     *(u32x4*)(O + (size_t)rowx * ldc + colx) = w8; }
;         }
	v_cvt_pk_fp8_f32 v27, v28, v29 op_sel:[0,0,1]
	v_pk_mul_f32 v[28:29], v[8:9], s[10:11] op_sel_hi:[1,0]
	v_med3_f32 v9, v12, s97, v219
	v_med3_f32 v12, v13, s97, v219
	v_cvt_pk_fp8_f32 v8, v9, v12
	v_pk_mul_f32 v[14:15], v[14:15], s[10:11] op_sel_hi:[1,0]
	v_med3_f32 v12, v14, s97, v219
	v_med3_f32 v13, v15, s97, v219
	v_med3_f32 v14, v28, s97, v219
	v_med3_f32 v15, v29, s97, v219
	v_cvt_pk_fp8_f32 v9, v14, v15
	v_cvt_pk_fp8_f32 v8, v12, v13 op_sel:[0,0,1]
	v_pk_mul_f32 v[12:13], v[40:41], s[10:11] op_sel_hi:[1,0]
	v_pk_mul_f32 v[28:29], v[44:45], s[10:11] op_sel_hi:[1,0]
	v_med3_f32 v30, v12, s97, v219
	v_med3_f32 v13, v13, s97, v219
	v_pk_mul_f32 v[10:11], v[10:11], s[10:11] op_sel_hi:[1,0]
	v_cvt_pk_fp8_f32 v12, v30, v13
	v_med3_f32 v28, v28, s97, v219
	v_med3_f32 v29, v29, s97, v219
	v_med3_f32 v10, v10, s97, v219
	v_med3_f32 v11, v11, s97, v219
	v_cvt_pk_fp8_f32 v13, v28, v29
	v_cvt_pk_fp8_f32 v9, v10, v11 op_sel:[0,0,1]
	v_pk_mul_f32 v[10:11], v[42:43], s[10:11] op_sel_hi:[1,0]
	v_pk_mul_f32 v[14:15], v[46:47], s[10:11] op_sel_hi:[1,0]
	v_med3_f32 v10, v10, s97, v219
	v_med3_f32 v11, v11, s97, v219
	v_cvt_pk_fp8_f32 v12, v10, v11 op_sel:[0,0,1]
	v_med3_f32 v10, v14, s97, v219
	v_med3_f32 v11, v15, s97, v219
	v_pk_mul_f32 v[0:1], v[0:1], s[10:11] op_sel_hi:[1,0]
	v_cvt_pk_fp8_f32 v13, v10, v11 op_sel:[0,0,1]
	v_pk_mul_f32 v[4:5], v[4:5], s[10:11] op_sel_hi:[1,0]
	v_pk_mul_f32 v[2:3], v[2:3], s[10:11] op_sel_hi:[1,0]
	v_med3_f32 v0, v0, s97, v219
	v_med3_f32 v1, v1, s97, v219
	v_pk_mul_f32 v[6:7], v[6:7], s[10:11] op_sel_hi:[1,0]
	v_med3_f32 v4, v4, s97, v219
	v_med3_f32 v5, v5, s97, v219
	v_cvt_pk_fp8_f32 v11, v0, v1
	v_med3_f32 v0, v2, s97, v219
	v_med3_f32 v1, v3, s97, v219
	v_pk_mul_f32 v[2:3], v[16:17], s[10:11] op_sel_hi:[1,0]
	v_cvt_pk_fp8_f32 v10, v4, v5
	v_med3_f32 v4, v6, s97, v219
	v_med3_f32 v5, v7, s97, v219
	v_pk_mul_f32 v[6:7], v[20:21], s[10:11] op_sel_hi:[1,0]
	v_med3_f32 v2, v2, s97, v219
	v_med3_f32 v3, v3, s97, v219
	v_cvt_pk_fp8_f32 v14, v2, v3
	v_med3_f32 v2, v6, s97, v219
	v_med3_f32 v3, v7, s97, v219
	v_cvt_pk_fp8_f32 v15, v2, v3
	v_cvt_pk_fp8_f32 v11, v0, v1 op_sel:[0,0,1]
	v_pk_mul_f32 v[0:1], v[18:19], s[10:11] op_sel_hi:[1,0]
	v_cvt_pk_fp8_f32 v48, v60, v61 op_sel:[0,0,1]
	v_cvt_pk_fp8_f32 v24, v36, v37 op_sel:[0,0,1]
	v_cvt_pk_fp8_f32 v10, v4, v5 op_sel:[0,0,1]
	v_pk_mul_f32 v[4:5], v[22:23], s[10:11] op_sel_hi:[1,0]
	v_med3_f32 v0, v0, s97, v219
	v_med3_f32 v1, v1, s97, v219
	v_cvt_pk_fp8_f32 v14, v0, v1 op_sel:[0,0,1]
	v_med3_f32 v0, v4, s97, v219
	v_med3_f32 v1, v5, s97, v219
	v_add_u32_e32 v2, 0x80, v140
	v_cvt_pk_fp8_f32 v15, v0, v1 op_sel:[0,0,1]
	v_or_b32_e32 v0, v64, v2
	v_mad_i64_i32 v[0:1], s[22:23], v0, s13, v[66:67]
	v_permlane16_swap_b32_e32 v48, v50
	v_permlane16_swap_b32_e32 v49, v51
	v_lshl_add_u64 v[0:1], v[0:1], 0, v[130:131]
	v_permlane16_swap_b32_e32 v24, v26
	v_permlane16_swap_b32_e32 v25, v27
	global_store_dwordx4 v[0:1], v[48:51], off
	global_store_dwordx4 v[0:1], v[24:27], off offset:128
	v_or_b32_e32 v0, v70, v2
	v_mad_i64_i32 v[0:1], s[22:23], v0, s13, v[66:67]
	v_permlane16_swap_b32_e32 v8, v10
	v_permlane16_swap_b32_e32 v9, v11
	v_lshl_add_u64 v[0:1], v[0:1], 0, v[130:131]
	v_permlane16_swap_b32_e32 v12, v14
	v_permlane16_swap_b32_e32 v13, v15
	s_andn2_b64 vcc, exec, s[4:5]
	s_mov_b64 s[4:5], -1
	v_mov_b32_e32 v218, v220
	v_mov_b32_e32 v226, v221
	v_mov_b64_e32 v[228:229], 0x1e8481
	v_mov_b32_e32 v227, 1
	global_store_dwordx4 v[0:1], v[8:11], off
	global_store_dwordx4 v[0:1], v[12:15], off offset:128
	s_cbranch_vccnz .LBB0_278
	s_andn2_b64 vcc, exec, s[0:1]
	s_cbranch_vccnz .LBB0_277
	s_barrier
	s_branch .LBB0_277

; #define LAS __attribute__((address_space(3)))
; __device__ __forceinline__ bf16 f2bf(float f) { return (bf16)cvt_pk_bf16(f, f); }
; __device__ __forceinline__ int crow(int r, int hi) { return (r & 3) + 8 * (r >> 2) + 4 * hi; }
; __device__ __forceinline__ void datt_stream(LAS unsigned char* lds, const DattRun& c, const float C, const int wv) {
;     ...
;     auto finish = [&](const int pa) __attribute__((always_inline)) {
;         if (hi == 0) li_l[r32] = l_reg; asm volatile("s_waitcnt lgkmcnt(0)" ::: "memory");
;         const int i0 = 64 * (c.a0 + pa) + 32 * par;
;         if (hi == 0) c.lse[((size_t)c.g * S + (size_t)(i0 + r32) * c.dil + c.r) * 8 + c.h] = (m_reg + __builtin_amdgcn_logf(l_reg)) * 0.6931471805599453f;
; #pragma unroll
;         for (int r = 0; r < 16; ++r) { const int orow = crow(r, hi); const float rl = __builtin_amdgcn_rcpf(li_l[orow]);
; #pragma unroll
;             for (int d = 0; d < 4; ++d) *(LAS bf16*)(stg + orow * 256 + (d * 32 + r32) * 2) = f2bf(o[d][r] * rl); }
;         asm volatile("s_waitcnt lgkmcnt(0)" ::: "memory");
.LBB0_419:
	s_or_b64 exec, exec, s[0:1]
	v_add_u32_e32 v64, s60, v230
	ds_read_b128 v[80:83], v64
	ds_read_b128 v[84:87], v64 offset:32
	ds_read_b128 v[88:91], v64 offset:64
	ds_read_b128 v[92:95], v64 offset:96
	v_add_u32_e32 v67, v231, v232
	s_waitcnt lgkmcnt(0)
	v_rcp_f32_e32 v80, v80
	v_rcp_f32_e32 v81, v81
	v_rcp_f32_e32 v82, v82
	v_rcp_f32_e32 v83, v83
	v_rcp_f32_e32 v84, v84
	v_rcp_f32_e32 v85, v85
	v_rcp_f32_e32 v86, v86
	v_rcp_f32_e32 v87, v87
	v_rcp_f32_e32 v88, v88
	v_rcp_f32_e32 v89, v89
	v_rcp_f32_e32 v90, v90
	v_rcp_f32_e32 v91, v91
	v_rcp_f32_e32 v92, v92
	v_rcp_f32_e32 v93, v93
	v_rcp_f32_e32 v94, v94
	v_rcp_f32_e32 v95, v95
	v_mul_f32_e32 v66, v0, v80
	v_cvt_pk_bf16_f32 v66, v66, v66
	ds_write_b16 v67, v66
	v_mul_f32_e32 v68, v16, v80
	v_cvt_pk_bf16_f32 v68, v68, v68
	ds_write_b16 v67, v68 offset:64
	v_mul_f32_e32 v69, v32, v80
	v_cvt_pk_bf16_f32 v69, v69, v69
	ds_write_b16 v67, v69 offset:128
	v_mul_f32_e32 v70, v48, v80
	v_cvt_pk_bf16_f32 v70, v70, v70
	ds_write_b16 v67, v70 offset:192
	v_mul_f32_e32 v66, v1, v81
	v_cvt_pk_bf16_f32 v66, v66, v66
	ds_write_b16 v67, v66 offset:256
	v_mul_f32_e32 v68, v17, v81
	v_cvt_pk_bf16_f32 v68, v68, v68
	ds_write_b16 v67, v68 offset:320
	v_mul_f32_e32 v69, v33, v81
	v_cvt_pk_bf16_f32 v69, v69, v69
	ds_write_b16 v67, v69 offset:384
	v_mul_f32_e32 v70, v49, v81
	v_cvt_pk_bf16_f32 v70, v70, v70
	ds_write_b16 v67, v70 offset:448
	v_mul_f32_e32 v66, v2, v82
	v_cvt_pk_bf16_f32 v66, v66, v66
	ds_write_b16 v67, v66 offset:512
	v_mul_f32_e32 v68, v18, v82
	v_cvt_pk_bf16_f32 v68, v68, v68
	ds_write_b16 v67, v68 offset:576
	v_mul_f32_e32 v69, v34, v82
	v_cvt_pk_bf16_f32 v69, v69, v69
	ds_write_b16 v67, v69 offset:640
	v_mul_f32_e32 v70, v50, v82
	v_cvt_pk_bf16_f32 v70, v70, v70
	ds_write_b16 v67, v70 offset:704
	v_mul_f32_e32 v66, v3, v83
	v_cvt_pk_bf16_f32 v66, v66, v66
	ds_write_b16 v67, v66 offset:768
	v_mul_f32_e32 v68, v19, v83
	v_cvt_pk_bf16_f32 v68, v68, v68
	ds_write_b16 v67, v68 offset:832
	v_mul_f32_e32 v69, v35, v83
	v_cvt_pk_bf16_f32 v69, v69, v69
	ds_write_b16 v67, v69 offset:896
	v_mul_f32_e32 v70, v51, v83
	v_cvt_pk_bf16_f32 v70, v70, v70
	ds_write_b16 v67, v70 offset:960
	v_mul_f32_e32 v66, v4, v84
	v_cvt_pk_bf16_f32 v66, v66, v66
	ds_write_b16 v67, v66 offset:2048
	v_mul_f32_e32 v68, v20, v84
	v_cvt_pk_bf16_f32 v68, v68, v68
	ds_write_b16 v67, v68 offset:2112
	v_mul_f32_e32 v69, v36, v84
	v_cvt_pk_bf16_f32 v69, v69, v69
	ds_write_b16 v67, v69 offset:2176
	v_mul_f32_e32 v70, v52, v84
	v_cvt_pk_bf16_f32 v70, v70, v70
	ds_write_b16 v67, v70 offset:2240
	v_mul_f32_e32 v66, v5, v85
	v_cvt_pk_bf16_f32 v66, v66, v66
	ds_write_b16 v67, v66 offset:2304
	v_mul_f32_e32 v68, v21, v85
	v_cvt_pk_bf16_f32 v68, v68, v68
	ds_write_b16 v67, v68 offset:2368
	v_mul_f32_e32 v69, v37, v85
	v_cvt_pk_bf16_f32 v69, v69, v69
	ds_write_b16 v67, v69 offset:2432
	v_mul_f32_e32 v70, v53, v85
	v_cvt_pk_bf16_f32 v70, v70, v70
	ds_write_b16 v67, v70 offset:2496
	v_mul_f32_e32 v66, v6, v86
	v_cvt_pk_bf16_f32 v66, v66, v66
	ds_write_b16 v67, v66 offset:2560
	v_mul_f32_e32 v68, v22, v86
	v_cvt_pk_bf16_f32 v68, v68, v68
	ds_write_b16 v67, v68 offset:2624
	v_mul_f32_e32 v69, v38, v86
	v_cvt_pk_bf16_f32 v69, v69, v69
	ds_write_b16 v67, v69 offset:2688
	v_mul_f32_e32 v70, v54, v86
	v_cvt_pk_bf16_f32 v70, v70, v70
	ds_write_b16 v67, v70 offset:2752
	v_mul_f32_e32 v66, v7, v87
	v_cvt_pk_bf16_f32 v66, v66, v66
	ds_write_b16 v67, v66 offset:2816
	v_mul_f32_e32 v68, v23, v87
	v_cvt_pk_bf16_f32 v68, v68, v68
	ds_write_b16 v67, v68 offset:2880
	v_mul_f32_e32 v69, v39, v87
	v_cvt_pk_bf16_f32 v69, v69, v69
	ds_write_b16 v67, v69 offset:2944
	v_mul_f32_e32 v70, v55, v87
	v_cvt_pk_bf16_f32 v70, v70, v70
	ds_write_b16 v67, v70 offset:3008
	v_mul_f32_e32 v66, v8, v88
	v_cvt_pk_bf16_f32 v66, v66, v66
	ds_write_b16 v67, v66 offset:4096
	v_mul_f32_e32 v68, v24, v88
	v_cvt_pk_bf16_f32 v68, v68, v68
	ds_write_b16 v67, v68 offset:4160
	v_mul_f32_e32 v69, v40, v88
	v_cvt_pk_bf16_f32 v69, v69, v69
	ds_write_b16 v67, v69 offset:4224
	v_mul_f32_e32 v70, v56, v88
	v_cvt_pk_bf16_f32 v70, v70, v70
	ds_write_b16 v67, v70 offset:4288
	v_mul_f32_e32 v66, v9, v89
	v_cvt_pk_bf16_f32 v66, v66, v66
	ds_write_b16 v67, v66 offset:4352
	v_mul_f32_e32 v68, v25, v89
	v_cvt_pk_bf16_f32 v68, v68, v68
	ds_write_b16 v67, v68 offset:4416
	v_mul_f32_e32 v69, v41, v89
	v_cvt_pk_bf16_f32 v69, v69, v69
	ds_write_b16 v67, v69 offset:4480
	v_mul_f32_e32 v70, v57, v89
	v_cvt_pk_bf16_f32 v70, v70, v70
	ds_write_b16 v67, v70 offset:4544
	v_mul_f32_e32 v66, v10, v90
	v_cvt_pk_bf16_f32 v66, v66, v66
	ds_write_b16 v67, v66 offset:4608
	v_mul_f32_e32 v68, v26, v90
	v_cvt_pk_bf16_f32 v68, v68, v68
	ds_write_b16 v67, v68 offset:4672
	v_mul_f32_e32 v69, v42, v90
	v_cvt_pk_bf16_f32 v69, v69, v69
	ds_write_b16 v67, v69 offset:4736
	v_mul_f32_e32 v70, v58, v90
	v_cvt_pk_bf16_f32 v70, v70, v70
	ds_write_b16 v67, v70 offset:4800
	v_mul_f32_e32 v66, v11, v91
	v_cvt_pk_bf16_f32 v66, v66, v66
	ds_write_b16 v67, v66 offset:4864
	v_mul_f32_e32 v68, v27, v91
	v_cvt_pk_bf16_f32 v68, v68, v68
	ds_write_b16 v67, v68 offset:4928
	v_mul_f32_e32 v69, v43, v91
	v_cvt_pk_bf16_f32 v69, v69, v69
	ds_write_b16 v67, v69 offset:4992
	v_mul_f32_e32 v70, v59, v91
	v_cvt_pk_bf16_f32 v70, v70, v70
	ds_write_b16 v67, v70 offset:5056
	v_mul_f32_e32 v66, v12, v92
	v_cvt_pk_bf16_f32 v66, v66, v66
	ds_write_b16 v67, v66 offset:6144
	v_mul_f32_e32 v68, v28, v92
	v_cvt_pk_bf16_f32 v68, v68, v68
	ds_write_b16 v67, v68 offset:6208
	v_mul_f32_e32 v69, v44, v92
	v_cvt_pk_bf16_f32 v69, v69, v69
	ds_write_b16 v67, v69 offset:6272
	v_mul_f32_e32 v70, v60, v92
	v_cvt_pk_bf16_f32 v70, v70, v70
	ds_write_b16 v67, v70 offset:6336
	v_mul_f32_e32 v66, v13, v93
	v_cvt_pk_bf16_f32 v66, v66, v66
	ds_write_b16 v67, v66 offset:6400
	v_mul_f32_e32 v68, v29, v93
	v_cvt_pk_bf16_f32 v68, v68, v68
	ds_write_b16 v67, v68 offset:6464
	v_mul_f32_e32 v69, v45, v93
	v_cvt_pk_bf16_f32 v69, v69, v69
	ds_write_b16 v67, v69 offset:6528
	v_mul_f32_e32 v70, v61, v93
	v_cvt_pk_bf16_f32 v70, v70, v70
	ds_write_b16 v67, v70 offset:6592
	v_mul_f32_e32 v66, v14, v94
	v_cvt_pk_bf16_f32 v66, v66, v66
	ds_write_b16 v67, v66 offset:6656
	v_mul_f32_e32 v68, v30, v94
	v_cvt_pk_bf16_f32 v68, v68, v68
	ds_write_b16 v67, v68 offset:6720
	v_mul_f32_e32 v69, v46, v94
	v_cvt_pk_bf16_f32 v69, v69, v69
	ds_write_b16 v67, v69 offset:6784
	v_mul_f32_e32 v70, v62, v94
	v_cvt_pk_bf16_f32 v70, v70, v70
	ds_write_b16 v67, v70 offset:6848
	v_mul_f32_e32 v66, v15, v95
	v_cvt_pk_bf16_f32 v66, v66, v66
	ds_write_b16 v67, v66 offset:6912
	v_mul_f32_e32 v68, v31, v95
	v_cvt_pk_bf16_f32 v68, v68, v68
	ds_write_b16 v67, v68 offset:6976
	v_mul_f32_e32 v69, v47, v95
	v_cvt_pk_bf16_f32 v69, v69, v69
	ds_write_b16 v67, v69 offset:7040
	v_mul_f32_e32 v70, v63, v95
	v_cvt_pk_bf16_f32 v70, v70, v70
	ds_write_b16 v67, v70 offset:7104
	v_mov_b32_e32 v78, 0x43e00000
	v_mov_b32_e32 v79, v65
	v_mov_b32_e32 v187, 0x43e00000
	v_mov_b32_e32 v243, 0xf149f2ca
	v_mov_b32_e32 v244, 0
	s_waitcnt lgkmcnt(0)
; #define LAS __attribute__((address_space(3)))
; __device__ __forceinline__ unsigned bf4_to_f8(unsigned p01, unsigned p23) {
;     const float a = fminf(fmaxf(__uint_as_float(p01 << 16) * O8_SCALE, -448.f), 448.f), b = fminf(fmaxf(__uint_as_float(p01 & 0xffff0000u) * O8_SCALE, -448.f), 448.f);
;     const float c2 = fminf(fmaxf(__uint_as_float(p23 << 16) * O8_SCALE, -448.f), 448.f), d = fminf(fmaxf(__uint_as_float(p23 & 0xffff0000u) * O8_SCALE, -448.f), 448.f);
;     int t = __builtin_amdgcn_cvt_pk_fp8_f32(a, b, 0, false); t = __builtin_amdgcn_cvt_pk_fp8_f32(c2, d, t, true); return (unsigned)t;
; }
; __device__ __forceinline__ void datt_stream(LAS unsigned char* lds, const DattRun& c, const float C, const int wv) {
;     ...
;         for (int i = 0; i < 4; ++i) { const int idx = lane + 64 * i, row = idx >> 3, ch = idx & 7;
;             const u32x4 v0 = *(const LAS u32x4*)(stg + row * 256 + ch * 32), v1 = *(const LAS u32x4*)(stg + row * 256 + ch * 32 + 16); u32x4 w;
;             w.x = bf4_to_f8(v0.x, v0.y); w.y = bf4_to_f8(v0.z, v0.w); w.z = bf4_to_f8(v1.x, v1.y); w.w = bf4_to_f8(v1.z, v1.w);
;             const size_t go = ((size_t)c.g * S + (size_t)(i0 + row) * c.dil + c.r) * 1024 + c.h * 128 + ch * 16;
;             unsigned char* gp = c.zo ? (unsigned char*)c.zo + (go & (size_t)0xfffff0) : (unsigned char*)c.ob + go; *(u32x4*)gp = w; }
	v_add_u32_e32 v64, v249, v250
	ds_read_b128 v[66:69], v64
	ds_read_b128 v[70:73], v64 offset:16
	s_waitcnt lgkmcnt(1)
	v_lshlrev_b32_e32 v64, 16, v66
	v_and_b32_e32 v66, 0xffff0000, v66
	v_max_f32_e32 v66, v66, v66
	v_med3_f32 v74, v66, s97, v78
	v_lshlrev_b32_e32 v66, 16, v67
	v_max_f32_e32 v64, v64, v64
	v_max_f32_e32 v66, v66, v66
	v_med3_f32 v64, v64, s97, v78
	v_med3_f32 v75, v66, s97, v78
	v_cvt_pk_fp8_f32 v66, v64, v74
	v_and_b32_e32 v64, 0xffff0000, v67
	v_max_f32_e32 v64, v64, v64
	v_and_b32_e32 v67, 0xffff0000, v68
	v_med3_f32 v64, v64, s97, v78
	v_max_f32_e32 v67, v67, v67
	v_cvt_pk_fp8_f32 v66, v75, v64 op_sel:[0,0,1]
	v_lshlrev_b32_e32 v64, 16, v68
	v_med3_f32 v68, v67, s97, v78
	v_lshlrev_b32_e32 v67, 16, v69
	v_max_f32_e32 v64, v64, v64
	v_max_f32_e32 v67, v67, v67
	v_med3_f32 v64, v64, s97, v78
	v_med3_f32 v74, v67, s97, v78
	v_cvt_pk_fp8_f32 v67, v64, v68
	v_and_b32_e32 v64, 0xffff0000, v69
	v_max_f32_e32 v64, v64, v64
	s_waitcnt lgkmcnt(0)
	v_and_b32_e32 v68, 0xffff0000, v70
	v_med3_f32 v64, v64, s97, v78
	v_max_f32_e32 v68, v68, v68
	v_cvt_pk_fp8_f32 v67, v74, v64 op_sel:[0,0,1]
	v_lshlrev_b32_e32 v64, 16, v70
	v_med3_f32 v69, v68, s97, v78
	v_lshlrev_b32_e32 v68, 16, v71
	v_max_f32_e32 v64, v64, v64
	v_max_f32_e32 v68, v68, v68
	v_med3_f32 v64, v64, s97, v78
	v_med3_f32 v70, v68, s97, v78
	v_cvt_pk_fp8_f32 v68, v64, v69
	v_and_b32_e32 v64, 0xffff0000, v71
	v_max_f32_e32 v64, v64, v64
	v_and_b32_e32 v69, 0xffff0000, v72
	v_med3_f32 v64, v64, s97, v78
	v_max_f32_e32 v69, v69, v69
	v_cvt_pk_fp8_f32 v68, v70, v64 op_sel:[0,0,1]
	v_lshlrev_b32_e32 v64, 16, v72
	v_med3_f32 v70, v69, s97, v78
	v_lshlrev_b32_e32 v69, 16, v73
	v_max_f32_e32 v64, v64, v64
	v_max_f32_e32 v69, v69, v69
	v_med3_f32 v64, v64, s97, v78
	v_med3_f32 v71, v69, s97, v78
	v_cvt_pk_fp8_f32 v69, v64, v70
	v_and_b32_e32 v64, 0xffff0000, v73
	v_max_f32_e32 v64, v64, v64
	v_med3_f32 v64, v64, s97, v78
	v_or_b32_e32 v70, s6, v248
	v_cvt_pk_fp8_f32 v69, v71, v64 op_sel:[0,0,1]
	v_ashrrev_i32_e32 v71, 31, v70
	v_lshlrev_b64 v[70:71], s45, v[70:71]
	v_add_u32_e32 v64, v252, v250
	v_lshl_add_u64 v[74:75], v[70:71], 0, s[2:3]
	ds_read_b128 v[70:73], v64
	v_lshlrev_b64 v[74:75], 10, v[74:75]
	v_lshl_add_u64 v[74:75], v[208:209], 0, v[74:75]
	global_store_dwordx4 v[74:75], v[66:69], off
	ds_read_b128 v[66:69], v64 offset:16
	s_waitcnt lgkmcnt(1)
	v_lshlrev_b32_e32 v64, 16, v70
	v_and_b32_e32 v70, 0xffff0000, v70
	v_max_f32_e32 v70, v70, v70
	v_med3_f32 v74, v70, s97, v78
	v_lshlrev_b32_e32 v70, 16, v71
	v_max_f32_e32 v64, v64, v64
	v_max_f32_e32 v70, v70, v70
	v_med3_f32 v64, v64, s97, v78
	v_med3_f32 v75, v70, s97, v78
	v_cvt_pk_fp8_f32 v70, v64, v74
	v_and_b32_e32 v64, 0xffff0000, v71
	v_max_f32_e32 v64, v64, v64
	v_and_b32_e32 v71, 0xffff0000, v72
	v_med3_f32 v64, v64, s97, v78
	v_max_f32_e32 v71, v71, v71
	v_cvt_pk_fp8_f32 v70, v75, v64 op_sel:[0,0,1]
	v_lshlrev_b32_e32 v64, 16, v72
	v_med3_f32 v72, v71, s97, v78
	v_lshlrev_b32_e32 v71, 16, v73
	v_max_f32_e32 v64, v64, v64
	v_max_f32_e32 v71, v71, v71
	v_med3_f32 v64, v64, s97, v78
	v_med3_f32 v74, v71, s97, v78
	v_cvt_pk_fp8_f32 v71, v64, v72
	v_and_b32_e32 v64, 0xffff0000, v73
	v_max_f32_e32 v64, v64, v64
	v_med3_f32 v64, v64, s97, v78
	v_cvt_pk_fp8_f32 v71, v74, v64 op_sel:[0,0,1]
	s_waitcnt lgkmcnt(0)
	v_lshlrev_b32_e32 v64, 16, v66
	v_and_b32_e32 v66, 0xffff0000, v66
	v_lshlrev_b32_e32 v72, 16, v67
	v_max_f32_e32 v64, v64, v64
	v_max_f32_e32 v66, v66, v66
	v_max_f32_e32 v72, v72, v72
	v_med3_f32 v64, v64, s97, v78
	v_med3_f32 v66, v66, s97, v78
	v_med3_f32 v73, v72, s97, v78
	v_cvt_pk_fp8_f32 v72, v64, v66
	v_and_b32_e32 v64, 0xffff0000, v67
	v_max_f32_e32 v64, v64, v64
	v_med3_f32 v64, v64, s97, v78
	v_cvt_pk_fp8_f32 v72, v73, v64 op_sel:[0,0,1]
	v_lshlrev_b32_e32 v64, 16, v68
	v_and_b32_e32 v66, 0xffff0000, v68
	v_max_f32_e32 v64, v64, v64
	v_max_f32_e32 v66, v66, v66
	v_med3_f32 v64, v64, s97, v78
	v_med3_f32 v66, v66, s97, v78
	v_cvt_pk_fp8_f32 v73, v64, v66
	v_lshlrev_b32_e32 v67, 16, v69
	v_and_b32_e32 v64, 0xffff0000, v69
	v_max_f32_e32 v67, v67, v67
	v_max_f32_e32 v64, v64, v64
	v_med3_f32 v67, v67, s97, v78
	v_med3_f32 v64, v64, s97, v78
	v_or_b32_e32 v66, s6, v251
	v_cvt_pk_fp8_f32 v73, v67, v64 op_sel:[0,0,1]
	v_ashrrev_i32_e32 v67, 31, v66
	v_lshlrev_b64 v[66:67], s45, v[66:67]
	v_add_u32_e32 v64, v214, v250
	v_lshl_add_u64 v[74:75], v[66:67], 0, s[2:3]
	ds_read_b128 v[66:69], v64
	v_lshlrev_b64 v[74:75], 10, v[74:75]
	v_lshl_add_u64 v[74:75], v[208:209], 0, v[74:75]
	global_store_dwordx4 v[74:75], v[70:73], off
	ds_read_b128 v[70:73], v64 offset:16
	s_waitcnt lgkmcnt(1)
	v_lshlrev_b32_e32 v64, 16, v66
	v_and_b32_e32 v66, 0xffff0000, v66
	v_max_f32_e32 v66, v66, v66
	v_med3_f32 v74, v66, s97, v78
	v_lshlrev_b32_e32 v66, 16, v67
	v_max_f32_e32 v64, v64, v64
	v_max_f32_e32 v66, v66, v66
	v_med3_f32 v64, v64, s97, v78
	v_med3_f32 v75, v66, s97, v78
	v_cvt_pk_fp8_f32 v66, v64, v74
	v_and_b32_e32 v64, 0xffff0000, v67
	v_max_f32_e32 v64, v64, v64
	v_and_b32_e32 v67, 0xffff0000, v68
	v_med3_f32 v64, v64, s97, v78
	v_max_f32_e32 v67, v67, v67
	v_cvt_pk_fp8_f32 v66, v75, v64 op_sel:[0,0,1]
	v_lshlrev_b32_e32 v64, 16, v68
	v_med3_f32 v68, v67, s97, v78
	v_lshlrev_b32_e32 v67, 16, v69
	v_max_f32_e32 v64, v64, v64
	v_max_f32_e32 v67, v67, v67
	v_med3_f32 v64, v64, s97, v78
	v_med3_f32 v74, v67, s97, v78
	v_cvt_pk_fp8_f32 v67, v64, v68
	v_and_b32_e32 v64, 0xffff0000, v69
	v_max_f32_e32 v64, v64, v64
	s_waitcnt lgkmcnt(0)
; #define LAS __attribute__((address_space(3)))
; __device__ __forceinline__ void datt_stream(LAS unsigned char* lds, const DattRun& c, const float C, const int wv) {
;     ...
;         for (int i = 0; i < 4; ++i) { const int idx = lane + 64 * i, row = idx >> 3, ch = idx & 7;
;             const u32x4 v0 = *(const LAS u32x4*)(stg + row * 256 + ch * 32), v1 = *(const LAS u32x4*)(stg + row * 256 + ch * 32 + 16); u32x4 w;
;             w.x = bf4_to_f8(v0.x, v0.y); w.y = bf4_to_f8(v0.z, v0.w); w.z = bf4_to_f8(v1.x, v1.y); w.w = bf4_to_f8(v1.z, v1.w);
;             const size_t go = ((size_t)c.g * S + (size_t)(i0 + row) * c.dil + c.r) * 1024 + c.h * 128 + ch * 16;
;             unsigned char* gp = c.zo ? (unsigned char*)c.zo + (go & (size_t)0xfffff0) : (unsigned char*)c.ob + go; *(u32x4*)gp = w; }
	v_and_b32_e32 v68, 0xffff0000, v70
	v_med3_f32 v64, v64, s97, v78
	v_max_f32_e32 v68, v68, v68
	v_cvt_pk_fp8_f32 v67, v74, v64 op_sel:[0,0,1]
	v_lshlrev_b32_e32 v64, 16, v70
	v_med3_f32 v69, v68, s97, v78
	v_lshlrev_b32_e32 v68, 16, v71
	v_max_f32_e32 v64, v64, v64
	v_max_f32_e32 v68, v68, v68
	v_med3_f32 v64, v64, s97, v78
	v_med3_f32 v70, v68, s97, v78
	v_cvt_pk_fp8_f32 v68, v64, v69
	v_and_b32_e32 v64, 0xffff0000, v71
	v_max_f32_e32 v64, v64, v64
	v_and_b32_e32 v69, 0xffff0000, v72
	v_med3_f32 v64, v64, s97, v78
	v_max_f32_e32 v69, v69, v69
	v_cvt_pk_fp8_f32 v68, v70, v64 op_sel:[0,0,1]
	v_lshlrev_b32_e32 v64, 16, v72
	v_med3_f32 v70, v69, s97, v78
	v_lshlrev_b32_e32 v69, 16, v73
	v_max_f32_e32 v64, v64, v64
	v_max_f32_e32 v69, v69, v69
	v_med3_f32 v64, v64, s97, v78
	v_med3_f32 v71, v69, s97, v78
	v_cvt_pk_fp8_f32 v69, v64, v70
	v_and_b32_e32 v64, 0xffff0000, v73
	v_max_f32_e32 v64, v64, v64
	v_med3_f32 v64, v64, s97, v78
	v_or_b32_e32 v70, s6, v253
	v_cvt_pk_fp8_f32 v69, v71, v64 op_sel:[0,0,1]
	v_ashrrev_i32_e32 v71, 31, v70
	v_lshlrev_b64 v[70:71], s45, v[70:71]
	v_lshl_add_u64 v[70:71], v[70:71], 0, s[2:3]
	v_lshlrev_b64 v[70:71], 10, v[70:71]
	v_lshl_add_u64 v[70:71], v[208:209], 0, v[70:71]
	global_store_dwordx4 v[70:71], v[66:69], off
	v_add_u32_e32 v64, v216, v250
	ds_read_b128 v[66:69], v64
	ds_read_b128 v[70:73], v64 offset:16
	v_or_b32_e32 v74, s6, v217
	v_ashrrev_i32_e32 v75, 31, v74
	v_lshlrev_b64 v[74:75], s45, v[74:75]
	s_waitcnt lgkmcnt(1)
	v_lshlrev_b32_e32 v76, 16, v66
	v_and_b32_e32 v66, 0xffff0000, v66
	v_max_f32_e32 v76, v76, v76
	v_max_f32_e32 v66, v66, v66
	v_med3_f32 v76, v76, s97, v78
	v_med3_f32 v77, v66, s97, v78
	v_cvt_pk_fp8_f32 v66, v76, v77
	v_lshlrev_b32_e32 v64, 16, v67
	v_and_b32_e32 v67, 0xffff0000, v67
	v_max_f32_e32 v64, v64, v64
	v_max_f32_e32 v67, v67, v67
	v_med3_f32 v64, v64, s97, v78
	v_med3_f32 v67, v67, s97, v78
	v_cvt_pk_fp8_f32 v66, v64, v67 op_sel:[0,0,1]
	v_lshlrev_b32_e32 v67, 16, v68
	v_max_f32_e32 v67, v67, v67
	v_med3_f32 v76, v67, s97, v78
	v_and_b32_e32 v67, 0xffff0000, v68
	v_max_f32_e32 v67, v67, v67
	v_med3_f32 v68, v67, s97, v78
	v_cvt_pk_fp8_f32 v67, v76, v68
	v_lshlrev_b32_e32 v64, 16, v69
	v_and_b32_e32 v68, 0xffff0000, v69
	v_max_f32_e32 v64, v64, v64
	v_max_f32_e32 v68, v68, v68
	v_med3_f32 v64, v64, s97, v78
	v_med3_f32 v68, v68, s97, v78
	v_cvt_pk_fp8_f32 v67, v64, v68 op_sel:[0,0,1]
	s_waitcnt lgkmcnt(0)
	v_lshlrev_b32_e32 v68, 16, v70
	v_max_f32_e32 v68, v68, v68
	v_med3_f32 v69, v68, s97, v78
	v_and_b32_e32 v68, 0xffff0000, v70
	v_max_f32_e32 v68, v68, v68
	v_med3_f32 v70, v68, s97, v78
	v_cvt_pk_fp8_f32 v68, v69, v70
	v_lshlrev_b32_e32 v64, 16, v71
	v_and_b32_e32 v69, 0xffff0000, v71
	v_max_f32_e32 v64, v64, v64
	v_max_f32_e32 v69, v69, v69
	v_med3_f32 v64, v64, s97, v78
	v_med3_f32 v69, v69, s97, v78
	v_cvt_pk_fp8_f32 v68, v64, v69 op_sel:[0,0,1]
	v_lshlrev_b32_e32 v69, 16, v72
	v_max_f32_e32 v69, v69, v69
	v_med3_f32 v70, v69, s97, v78
	v_and_b32_e32 v69, 0xffff0000, v72
	v_max_f32_e32 v69, v69, v69
	v_med3_f32 v71, v69, s97, v78
	v_cvt_pk_fp8_f32 v69, v70, v71
	v_lshlrev_b32_e32 v64, 16, v73
	v_and_b32_e32 v70, 0xffff0000, v73
	v_max_f32_e32 v64, v64, v64
	v_max_f32_e32 v70, v70, v70
	v_med3_f32 v64, v64, s97, v78
	v_med3_f32 v70, v70, s97, v78
	v_cvt_pk_fp8_f32 v69, v64, v70 op_sel:[0,0,1]
	v_lshl_add_u64 v[70:71], v[74:75], 0, s[2:3]
	v_lshlrev_b64 v[70:71], 10, v[70:71]
	v_lshl_add_u64 v[70:71], v[208:209], 0, v[70:71]
	global_store_dwordx4 v[70:71], v[66:69], off
	s_waitcnt lgkmcnt(0)
	v_mov_b32_e32 v78, v65
	v_mov_b32_e32 v64, v65
	v_mov_b32_e32 v66, v65
	v_mov_b32_e32 v67, v65
	v_mov_b32_e32 v68, v65
	v_mov_b32_e32 v69, v65
	v_mov_b32_e32 v70, v65
	v_mov_b32_e32 v71, v65
	v_mov_b32_e32 v72, v65
	v_mov_b32_e32 v73, v65
	v_mov_b32_e32 v74, v65
	v_mov_b32_e32 v75, v65
	v_mov_b32_e32 v76, v65
	v_mov_b32_e32 v77, v65
	v_mov_b64_e32 v[94:95], v[78:79]
	v_mov_b64_e32 v[110:111], v[78:79]
	v_mov_b64_e32 v[126:127], v[78:79]
	v_mov_b64_e32 v[142:143], v[78:79]
	v_mov_b64_e32 v[92:93], v[76:77]
	v_mov_b64_e32 v[90:91], v[74:75]
	v_mov_b64_e32 v[88:89], v[72:73]
	v_mov_b64_e32 v[86:87], v[70:71]
	v_mov_b64_e32 v[84:85], v[68:69]
	v_mov_b64_e32 v[82:83], v[66:67]
	v_mov_b64_e32 v[80:81], v[64:65]
	v_mov_b64_e32 v[108:109], v[76:77]
	v_mov_b64_e32 v[106:107], v[74:75]
	v_mov_b64_e32 v[104:105], v[72:73]
	v_mov_b64_e32 v[102:103], v[70:71]
	v_mov_b64_e32 v[100:101], v[68:69]
	v_mov_b64_e32 v[98:99], v[66:67]
	v_mov_b64_e32 v[96:97], v[64:65]
	v_mov_b64_e32 v[124:125], v[76:77]
	v_mov_b64_e32 v[122:123], v[74:75]
	v_mov_b64_e32 v[120:121], v[72:73]
	v_mov_b64_e32 v[118:119], v[70:71]
	v_mov_b64_e32 v[116:117], v[68:69]
	v_mov_b64_e32 v[114:115], v[66:67]
	v_mov_b64_e32 v[112:113], v[64:65]
	v_mov_b64_e32 v[140:141], v[76:77]
	v_mov_b64_e32 v[138:139], v[74:75]
	v_mov_b64_e32 v[136:137], v[72:73]
	v_mov_b64_e32 v[134:135], v[70:71]
	v_mov_b64_e32 v[132:133], v[68:69]
	v_mov_b64_e32 v[130:131], v[66:67]
	v_mov_b64_e32 v[128:129], v[64:65]

; #define LAS __attribute__((address_space(3)))
; __device__ __forceinline__ bf16 f2bf(float f) { return (bf16)cvt_pk_bf16(f, f); }
; __device__ __forceinline__ int crow(int r, int hi) { return (r & 3) + 8 * (r >> 2) + 4 * hi; }
; __device__ __forceinline__ void datt_stream(LAS unsigned char* lds, const DattRun& c, const float C, const int wv) {
;     ...
;     auto finish = [&](const int pa) __attribute__((always_inline)) {
;         if (hi == 0) li_l[r32] = l_reg; asm volatile("s_waitcnt lgkmcnt(0)" ::: "memory");
;         const int i0 = 64 * (c.a0 + pa) + 32 * par;
;         if (hi == 0) c.lse[((size_t)c.g * S + (size_t)(i0 + r32) * c.dil + c.r) * 8 + c.h] = (m_reg + __builtin_amdgcn_logf(l_reg)) * 0.6931471805599453f;
; #pragma unroll
;         for (int r = 0; r < 16; ++r) { const int orow = crow(r, hi); const float rl = __builtin_amdgcn_rcpf(li_l[orow]);
; #pragma unroll
;             for (int d = 0; d < 4; ++d) *(LAS bf16*)(stg + orow * 256 + (d * 32 + r32) * 2) = f2bf(o[d][r] * rl); }
;         asm volatile("s_waitcnt lgkmcnt(0)" ::: "memory");
.LBB0_474:
	s_or_b64 exec, exec, s[6:7]
	v_add_u32_e32 v0, s60, v230
	ds_read_b128 v[16:19], v0
	ds_read_b128 v[20:23], v0 offset:32
	ds_read_b128 v[24:27], v0 offset:64
	ds_read_b128 v[28:31], v0 offset:96
	v_add_u32_e32 v2, v231, v232
	s_waitcnt lgkmcnt(0)
	v_rcp_f32_e32 v16, v16
	v_rcp_f32_e32 v17, v17
	v_rcp_f32_e32 v18, v18
	v_rcp_f32_e32 v19, v19
	v_rcp_f32_e32 v20, v20
	v_rcp_f32_e32 v21, v21
	v_rcp_f32_e32 v22, v22
	v_rcp_f32_e32 v23, v23
	v_rcp_f32_e32 v24, v24
	v_rcp_f32_e32 v25, v25
	v_rcp_f32_e32 v26, v26
	v_rcp_f32_e32 v27, v27
	v_rcp_f32_e32 v28, v28
	v_rcp_f32_e32 v29, v29
	v_rcp_f32_e32 v30, v30
	v_rcp_f32_e32 v31, v31
	v_mul_f32_e32 v1, v80, v16
	v_cvt_pk_bf16_f32 v1, v1, v1
	ds_write_b16 v2, v1
	v_mul_f32_e32 v3, v96, v16
	v_cvt_pk_bf16_f32 v3, v3, v3
	ds_write_b16 v2, v3 offset:64
	v_mul_f32_e32 v5, v112, v16
	v_cvt_pk_bf16_f32 v5, v5, v5
	ds_write_b16 v2, v5 offset:128
	v_mul_f32_e32 v6, v128, v16
	v_cvt_pk_bf16_f32 v6, v6, v6
	ds_write_b16 v2, v6 offset:192
	v_mul_f32_e32 v1, v81, v17
	v_cvt_pk_bf16_f32 v1, v1, v1
	ds_write_b16 v2, v1 offset:256
	v_mul_f32_e32 v3, v97, v17
	v_cvt_pk_bf16_f32 v3, v3, v3
	ds_write_b16 v2, v3 offset:320
	v_mul_f32_e32 v5, v113, v17
	v_cvt_pk_bf16_f32 v5, v5, v5
	ds_write_b16 v2, v5 offset:384
	v_mul_f32_e32 v6, v129, v17
	v_cvt_pk_bf16_f32 v6, v6, v6
	ds_write_b16 v2, v6 offset:448
	v_mul_f32_e32 v1, v82, v18
	v_cvt_pk_bf16_f32 v1, v1, v1
	ds_write_b16 v2, v1 offset:512
	v_mul_f32_e32 v3, v98, v18
	v_cvt_pk_bf16_f32 v3, v3, v3
	ds_write_b16 v2, v3 offset:576
	v_mul_f32_e32 v5, v114, v18
	v_cvt_pk_bf16_f32 v5, v5, v5
	ds_write_b16 v2, v5 offset:640
	v_mul_f32_e32 v6, v130, v18
	v_cvt_pk_bf16_f32 v6, v6, v6
	ds_write_b16 v2, v6 offset:704
	v_mul_f32_e32 v1, v83, v19
	v_cvt_pk_bf16_f32 v1, v1, v1
	ds_write_b16 v2, v1 offset:768
	v_mul_f32_e32 v3, v99, v19
	v_cvt_pk_bf16_f32 v3, v3, v3
	ds_write_b16 v2, v3 offset:832
	v_mul_f32_e32 v5, v115, v19
	v_cvt_pk_bf16_f32 v5, v5, v5
	ds_write_b16 v2, v5 offset:896
	v_mul_f32_e32 v6, v131, v19
	v_cvt_pk_bf16_f32 v6, v6, v6
	ds_write_b16 v2, v6 offset:960
	v_mul_f32_e32 v1, v84, v20
	v_cvt_pk_bf16_f32 v1, v1, v1
	ds_write_b16 v2, v1 offset:2048
	v_mul_f32_e32 v3, v100, v20
	v_cvt_pk_bf16_f32 v3, v3, v3
	ds_write_b16 v2, v3 offset:2112
	v_mul_f32_e32 v5, v116, v20
	v_cvt_pk_bf16_f32 v5, v5, v5
	ds_write_b16 v2, v5 offset:2176
	v_mul_f32_e32 v6, v132, v20
	v_cvt_pk_bf16_f32 v6, v6, v6
	ds_write_b16 v2, v6 offset:2240
	v_mul_f32_e32 v1, v85, v21
	v_cvt_pk_bf16_f32 v1, v1, v1
	ds_write_b16 v2, v1 offset:2304
	v_mul_f32_e32 v3, v101, v21
	v_cvt_pk_bf16_f32 v3, v3, v3
	ds_write_b16 v2, v3 offset:2368
	v_mul_f32_e32 v5, v117, v21
	v_cvt_pk_bf16_f32 v5, v5, v5
	ds_write_b16 v2, v5 offset:2432
	v_mul_f32_e32 v6, v133, v21
	v_cvt_pk_bf16_f32 v6, v6, v6
	ds_write_b16 v2, v6 offset:2496
	v_mul_f32_e32 v1, v86, v22
	v_cvt_pk_bf16_f32 v1, v1, v1
	ds_write_b16 v2, v1 offset:2560
	v_mul_f32_e32 v3, v102, v22
	v_cvt_pk_bf16_f32 v3, v3, v3
	ds_write_b16 v2, v3 offset:2624
	v_mul_f32_e32 v5, v118, v22
	v_cvt_pk_bf16_f32 v5, v5, v5
	ds_write_b16 v2, v5 offset:2688
	v_mul_f32_e32 v6, v134, v22
	v_cvt_pk_bf16_f32 v6, v6, v6
	ds_write_b16 v2, v6 offset:2752
	v_mul_f32_e32 v1, v87, v23
	v_cvt_pk_bf16_f32 v1, v1, v1
	ds_write_b16 v2, v1 offset:2816
	v_mul_f32_e32 v3, v103, v23
	v_cvt_pk_bf16_f32 v3, v3, v3
	ds_write_b16 v2, v3 offset:2880
	v_mul_f32_e32 v5, v119, v23
	v_cvt_pk_bf16_f32 v5, v5, v5
	ds_write_b16 v2, v5 offset:2944
	v_mul_f32_e32 v6, v135, v23
	v_cvt_pk_bf16_f32 v6, v6, v6
	ds_write_b16 v2, v6 offset:3008
	v_mul_f32_e32 v1, v88, v24
	v_cvt_pk_bf16_f32 v1, v1, v1
	ds_write_b16 v2, v1 offset:4096
	v_mul_f32_e32 v3, v104, v24
	v_cvt_pk_bf16_f32 v3, v3, v3
	ds_write_b16 v2, v3 offset:4160
	v_mul_f32_e32 v5, v120, v24
	v_cvt_pk_bf16_f32 v5, v5, v5
	ds_write_b16 v2, v5 offset:4224
	v_mul_f32_e32 v6, v136, v24
	v_cvt_pk_bf16_f32 v6, v6, v6
	ds_write_b16 v2, v6 offset:4288
	v_mul_f32_e32 v1, v89, v25
	v_cvt_pk_bf16_f32 v1, v1, v1
	ds_write_b16 v2, v1 offset:4352
	v_mul_f32_e32 v3, v105, v25
	v_cvt_pk_bf16_f32 v3, v3, v3
	ds_write_b16 v2, v3 offset:4416
	v_mul_f32_e32 v5, v121, v25
	v_cvt_pk_bf16_f32 v5, v5, v5
	ds_write_b16 v2, v5 offset:4480
	v_mul_f32_e32 v6, v137, v25
	v_cvt_pk_bf16_f32 v6, v6, v6
	ds_write_b16 v2, v6 offset:4544
	v_mul_f32_e32 v1, v90, v26
	v_cvt_pk_bf16_f32 v1, v1, v1
	ds_write_b16 v2, v1 offset:4608
	v_mul_f32_e32 v3, v106, v26
	v_cvt_pk_bf16_f32 v3, v3, v3
	ds_write_b16 v2, v3 offset:4672
	v_mul_f32_e32 v5, v122, v26
	v_cvt_pk_bf16_f32 v5, v5, v5
	ds_write_b16 v2, v5 offset:4736
	v_mul_f32_e32 v6, v138, v26
	v_cvt_pk_bf16_f32 v6, v6, v6
	ds_write_b16 v2, v6 offset:4800
	v_mul_f32_e32 v1, v91, v27
	v_cvt_pk_bf16_f32 v1, v1, v1
	ds_write_b16 v2, v1 offset:4864
	v_mul_f32_e32 v3, v107, v27
	v_cvt_pk_bf16_f32 v3, v3, v3
	ds_write_b16 v2, v3 offset:4928
	v_mul_f32_e32 v5, v123, v27
	v_cvt_pk_bf16_f32 v5, v5, v5
	ds_write_b16 v2, v5 offset:4992
	v_mul_f32_e32 v6, v139, v27
	v_cvt_pk_bf16_f32 v6, v6, v6
	ds_write_b16 v2, v6 offset:5056
	v_mul_f32_e32 v1, v92, v28
	v_cvt_pk_bf16_f32 v1, v1, v1
	ds_write_b16 v2, v1 offset:6144
	v_mul_f32_e32 v3, v108, v28
	v_cvt_pk_bf16_f32 v3, v3, v3
	ds_write_b16 v2, v3 offset:6208
	v_mul_f32_e32 v5, v124, v28
	v_cvt_pk_bf16_f32 v5, v5, v5
	ds_write_b16 v2, v5 offset:6272
	v_mul_f32_e32 v6, v140, v28
	v_cvt_pk_bf16_f32 v6, v6, v6
	ds_write_b16 v2, v6 offset:6336
	v_mul_f32_e32 v1, v93, v29
	v_cvt_pk_bf16_f32 v1, v1, v1
	ds_write_b16 v2, v1 offset:6400
	v_mul_f32_e32 v3, v109, v29
	v_cvt_pk_bf16_f32 v3, v3, v3
	ds_write_b16 v2, v3 offset:6464
	v_mul_f32_e32 v5, v125, v29
	v_cvt_pk_bf16_f32 v5, v5, v5
; #define LAS __attribute__((address_space(3)))
; __device__ __forceinline__ bf16 f2bf(float f) { return (bf16)cvt_pk_bf16(f, f); }
; __device__ __forceinline__ int crow(int r, int hi) { return (r & 3) + 8 * (r >> 2) + 4 * hi; }
; #define DS_LOADQ(pa) do { const unsigned _q = roff(64 * (c.a0 + (pa)) + 32 * par + r32) + (unsigned)hi * 8u; _Pragma("unroll") for (int d0 = 0; d0 < 8; ++d0) qraw[d0] = *(const u32x2*)(zb + (_q + d0 * 16u)); } while (0)
; #define DS_RESET() do { m_reg = -1e30f; l_reg = 0.f; _Pragma("unroll") for (int d = 0; d < 4; ++d) _Pragma("unroll") for (int r = 0; r < 16; ++r) o[d][r] = 0.f; } while (0)
; __device__ __forceinline__ void datt_stream(LAS unsigned char* lds, const DattRun& c, const float C, const int wv) {
;     ...
;     DS_LOADQ(pa0); DS_RESET();
;     ...
;         for (int r = 0; r < 16; ++r) { const int orow = crow(r, hi); const float rl = __builtin_amdgcn_rcpf(li_l[orow]);
; #pragma unroll
;             for (int d = 0; d < 4; ++d) *(LAS bf16*)(stg + orow * 256 + (d * 32 + r32) * 2) = f2bf(o[d][r] * rl); }
;         asm volatile("s_waitcnt lgkmcnt(0)" ::: "memory");
; #pragma unroll
;         for (int i = 0; i < 4; ++i) { const int idx = lane + 64 * i, row = idx >> 3, ch = idx & 7;
;             const u32x4 v0 = *(const LAS u32x4*)(stg + row * 256 + ch * 32), v1 = *(const LAS u32x4*)(stg + row * 256 + ch * 32 + 16); u32x4 w;
;             w.x = bf4_to_f8(v0.x, v0.y); w.y = bf4_to_f8(v0.z, v0.w); w.z = bf4_to_f8(v1.x, v1.y); w.w = bf4_to_f8(v1.z, v1.w);
;             const size_t go = ((size_t)c.g * S + (size_t)(i0 + row) * c.dil + c.r) * 1024 + c.h * 128 + ch * 16;
;             unsigned char* gp = c.zo ? (unsigned char*)c.zo + (go & (size_t)0xfffff0) : (unsigned char*)c.ob + go; *(u32x4*)gp = w; }
	ds_write_b16 v2, v5 offset:6528
	v_mul_f32_e32 v6, v141, v29
	v_cvt_pk_bf16_f32 v6, v6, v6
	ds_write_b16 v2, v6 offset:6592
	v_mul_f32_e32 v1, v94, v30
	v_cvt_pk_bf16_f32 v1, v1, v1
	ds_write_b16 v2, v1 offset:6656
	v_mul_f32_e32 v3, v110, v30
	v_cvt_pk_bf16_f32 v3, v3, v3
	ds_write_b16 v2, v3 offset:6720
	v_mul_f32_e32 v5, v126, v30
	v_cvt_pk_bf16_f32 v5, v5, v5
	ds_write_b16 v2, v5 offset:6784
	v_mul_f32_e32 v6, v142, v30
	v_cvt_pk_bf16_f32 v6, v6, v6
	ds_write_b16 v2, v6 offset:6848
	v_mul_f32_e32 v1, v95, v31
	v_cvt_pk_bf16_f32 v1, v1, v1
	ds_write_b16 v2, v1 offset:6912
	v_mul_f32_e32 v3, v111, v31
	v_cvt_pk_bf16_f32 v3, v3, v3
	ds_write_b16 v2, v3 offset:6976
	v_mul_f32_e32 v5, v127, v31
	v_cvt_pk_bf16_f32 v5, v5, v5
	ds_write_b16 v2, v5 offset:7040
	v_mul_f32_e32 v6, v143, v31
	v_cvt_pk_bf16_f32 v6, v6, v6
	ds_write_b16 v2, v6 offset:7104
	v_mov_b32_e32 v13, 0x43e00000
	v_mov_b32_e32 v64, v65
	v_mov_b32_e32 v66, v65
	v_mov_b32_e32 v67, v65
	v_mov_b32_e32 v68, v65
	v_mov_b32_e32 v69, v65
	v_mov_b32_e32 v70, v65
	v_mov_b32_e32 v71, v65
	v_mov_b32_e32 v72, v65
	v_mov_b32_e32 v73, v65
	v_mov_b32_e32 v74, v65
	v_mov_b32_e32 v75, v65
	v_mov_b32_e32 v76, v65
	v_mov_b32_e32 v77, v65
	v_mov_b32_e32 v78, v65
	v_mov_b32_e32 v79, v65
	v_add_u32_e32 v4, v249, v250
	v_mov_b64_e32 v[16:17], v[64:65]
	v_mov_b64_e32 v[32:33], v[64:65]
	v_mov_b64_e32 v[48:49], v[64:65]
	v_mov_b32_e32 v187, 0x43e00000
	v_mov_b32_e32 v245, 0xf149f2ca
	v_mov_b32_e32 v246, 0
	v_mov_b64_e32 v[18:19], v[66:67]
	v_mov_b64_e32 v[20:21], v[68:69]
	v_mov_b64_e32 v[22:23], v[70:71]
	v_mov_b64_e32 v[24:25], v[72:73]
	v_mov_b64_e32 v[26:27], v[74:75]
	v_mov_b64_e32 v[28:29], v[76:77]
	v_mov_b64_e32 v[30:31], v[78:79]
	v_mov_b64_e32 v[34:35], v[66:67]
	v_mov_b64_e32 v[36:37], v[68:69]
	v_mov_b64_e32 v[38:39], v[70:71]
	v_mov_b64_e32 v[40:41], v[72:73]
	v_mov_b64_e32 v[42:43], v[74:75]
	v_mov_b64_e32 v[44:45], v[76:77]
	v_mov_b64_e32 v[46:47], v[78:79]
	v_mov_b64_e32 v[50:51], v[66:67]
	v_mov_b64_e32 v[52:53], v[68:69]
	v_mov_b64_e32 v[54:55], v[70:71]
	v_mov_b64_e32 v[56:57], v[72:73]
	v_mov_b64_e32 v[58:59], v[74:75]
	v_mov_b64_e32 v[60:61], v[76:77]
	v_mov_b64_e32 v[62:63], v[78:79]
	s_waitcnt lgkmcnt(0)
	ds_read_b128 v[0:3], v4
	ds_read_b128 v[4:7], v4 offset:16
	s_waitcnt lgkmcnt(1)
	v_lshlrev_b32_e32 v8, 16, v0
	v_and_b32_e32 v0, 0xffff0000, v0
	v_max_f32_e32 v0, v0, v0
	v_med3_f32 v9, v0, s97, v13
	v_lshlrev_b32_e32 v0, 16, v1
	v_max_f32_e32 v8, v8, v8
	v_max_f32_e32 v0, v0, v0
	v_med3_f32 v8, v8, s97, v13
	v_med3_f32 v10, v0, s97, v13
	v_cvt_pk_fp8_f32 v0, v8, v9
	v_and_b32_e32 v1, 0xffff0000, v1
	v_max_f32_e32 v1, v1, v1
	v_med3_f32 v1, v1, s97, v13
	v_cvt_pk_fp8_f32 v0, v10, v1 op_sel:[0,0,1]
	v_lshlrev_b32_e32 v1, 16, v2
	v_max_f32_e32 v1, v1, v1
	v_med3_f32 v8, v1, s97, v13
	v_and_b32_e32 v1, 0xffff0000, v2
	v_max_f32_e32 v1, v1, v1
	v_med3_f32 v2, v1, s97, v13
	v_lshlrev_b32_e32 v1, 16, v3
	v_max_f32_e32 v1, v1, v1
	v_med3_f32 v9, v1, s97, v13
	v_cvt_pk_fp8_f32 v1, v8, v2
	v_and_b32_e32 v2, 0xffff0000, v3
	v_max_f32_e32 v2, v2, v2
	v_med3_f32 v2, v2, s97, v13
	v_cvt_pk_fp8_f32 v1, v9, v2 op_sel:[0,0,1]
	s_waitcnt lgkmcnt(0)
	v_lshlrev_b32_e32 v2, 16, v4
	v_max_f32_e32 v2, v2, v2
	v_med3_f32 v3, v2, s97, v13
	v_and_b32_e32 v2, 0xffff0000, v4
	v_max_f32_e32 v2, v2, v2
	v_med3_f32 v4, v2, s97, v13
	v_lshlrev_b32_e32 v2, 16, v5
	v_max_f32_e32 v2, v2, v2
	v_med3_f32 v8, v2, s97, v13
	v_cvt_pk_fp8_f32 v2, v3, v4
	v_and_b32_e32 v3, 0xffff0000, v5
	v_max_f32_e32 v3, v3, v3
	v_med3_f32 v3, v3, s97, v13
	v_cvt_pk_fp8_f32 v2, v8, v3 op_sel:[0,0,1]
	v_lshlrev_b32_e32 v3, 16, v6
	v_max_f32_e32 v3, v3, v3
	v_med3_f32 v4, v3, s97, v13
	v_and_b32_e32 v3, 0xffff0000, v6
	v_max_f32_e32 v3, v3, v3
	v_med3_f32 v5, v3, s97, v13
	v_lshlrev_b32_e32 v3, 16, v7
	v_max_f32_e32 v3, v3, v3
	v_med3_f32 v6, v3, s97, v13
	v_cvt_pk_fp8_f32 v3, v4, v5
	v_and_b32_e32 v4, 0xffff0000, v7
	v_max_f32_e32 v4, v4, v4
	v_med3_f32 v4, v4, s97, v13
	v_cvt_pk_fp8_f32 v3, v6, v4 op_sel:[0,0,1]
	v_or_b32_e32 v4, s8, v248
	v_ashrrev_i32_e32 v5, 31, v4
	v_lshlrev_b64 v[4:5], s45, v[4:5]
	v_add_u32_e32 v10, v252, v250
	v_lshl_add_u64 v[8:9], v[4:5], 0, s[2:3]
	ds_read_b128 v[4:7], v10
	v_lshlrev_b64 v[8:9], 10, v[8:9]
	v_lshl_add_u64 v[8:9], v[208:209], 0, v[8:9]
	global_store_dwordx4 v[8:9], v[0:3], off
	ds_read_b128 v[0:3], v10 offset:16
	s_waitcnt lgkmcnt(1)
	v_lshlrev_b32_e32 v8, 16, v4
	v_and_b32_e32 v4, 0xffff0000, v4
	v_max_f32_e32 v4, v4, v4
	v_med3_f32 v9, v4, s97, v13
	v_lshlrev_b32_e32 v4, 16, v5
	v_max_f32_e32 v8, v8, v8
	v_max_f32_e32 v4, v4, v4
	v_med3_f32 v8, v8, s97, v13
	v_med3_f32 v10, v4, s97, v13
	v_cvt_pk_fp8_f32 v4, v8, v9
	v_and_b32_e32 v5, 0xffff0000, v5
	v_max_f32_e32 v5, v5, v5
	v_med3_f32 v5, v5, s97, v13
	v_cvt_pk_fp8_f32 v4, v10, v5 op_sel:[0,0,1]
	v_lshlrev_b32_e32 v5, 16, v6
	v_max_f32_e32 v5, v5, v5
	v_med3_f32 v8, v5, s97, v13
	v_and_b32_e32 v5, 0xffff0000, v6
	v_max_f32_e32 v5, v5, v5
	v_med3_f32 v6, v5, s97, v13
	v_lshlrev_b32_e32 v5, 16, v7
	v_max_f32_e32 v5, v5, v5
	v_med3_f32 v9, v5, s97, v13
	v_cvt_pk_fp8_f32 v5, v8, v6
	v_and_b32_e32 v6, 0xffff0000, v7
	v_max_f32_e32 v6, v6, v6
	v_med3_f32 v6, v6, s97, v13
	v_cvt_pk_fp8_f32 v5, v9, v6 op_sel:[0,0,1]
	s_waitcnt lgkmcnt(0)
; #define LAS __attribute__((address_space(3)))
; __device__ __forceinline__ unsigned bf4_to_f8(unsigned p01, unsigned p23) {
;     const float a = fminf(fmaxf(__uint_as_float(p01 << 16) * O8_SCALE, -448.f), 448.f), b = fminf(fmaxf(__uint_as_float(p01 & 0xffff0000u) * O8_SCALE, -448.f), 448.f);
;     const float c2 = fminf(fmaxf(__uint_as_float(p23 << 16) * O8_SCALE, -448.f), 448.f), d = fminf(fmaxf(__uint_as_float(p23 & 0xffff0000u) * O8_SCALE, -448.f), 448.f);
;     int t = __builtin_amdgcn_cvt_pk_fp8_f32(a, b, 0, false); t = __builtin_amdgcn_cvt_pk_fp8_f32(c2, d, t, true); return (unsigned)t;
; }
; __device__ __forceinline__ void datt_stream(LAS unsigned char* lds, const DattRun& c, const float C, const int wv) {
;     ...
;         for (int i = 0; i < 4; ++i) { const int idx = lane + 64 * i, row = idx >> 3, ch = idx & 7;
;             const u32x4 v0 = *(const LAS u32x4*)(stg + row * 256 + ch * 32), v1 = *(const LAS u32x4*)(stg + row * 256 + ch * 32 + 16); u32x4 w;
;             w.x = bf4_to_f8(v0.x, v0.y); w.y = bf4_to_f8(v0.z, v0.w); w.z = bf4_to_f8(v1.x, v1.y); w.w = bf4_to_f8(v1.z, v1.w);
;             const size_t go = ((size_t)c.g * S + (size_t)(i0 + row) * c.dil + c.r) * 1024 + c.h * 128 + ch * 16;
;             unsigned char* gp = c.zo ? (unsigned char*)c.zo + (go & (size_t)0xfffff0) : (unsigned char*)c.ob + go; *(u32x4*)gp = w; }
	v_lshlrev_b32_e32 v6, 16, v0
	v_max_f32_e32 v6, v6, v6
	v_med3_f32 v7, v6, s97, v13
	v_and_b32_e32 v0, 0xffff0000, v0
	v_lshlrev_b32_e32 v6, 16, v1
	v_max_f32_e32 v0, v0, v0
	v_max_f32_e32 v6, v6, v6
	v_med3_f32 v0, v0, s97, v13
	v_med3_f32 v8, v6, s97, v13
	v_cvt_pk_fp8_f32 v6, v7, v0
	v_and_b32_e32 v0, 0xffff0000, v1
	v_max_f32_e32 v0, v0, v0
	v_med3_f32 v0, v0, s97, v13
	v_cvt_pk_fp8_f32 v6, v8, v0 op_sel:[0,0,1]
	v_lshlrev_b32_e32 v0, 16, v2
	v_and_b32_e32 v1, 0xffff0000, v2
	v_max_f32_e32 v0, v0, v0
	v_max_f32_e32 v1, v1, v1
	v_med3_f32 v0, v0, s97, v13
	v_med3_f32 v1, v1, s97, v13
	v_cvt_pk_fp8_f32 v7, v0, v1
	v_lshlrev_b32_e32 v2, 16, v3
	v_and_b32_e32 v0, 0xffff0000, v3
	v_max_f32_e32 v2, v2, v2
	v_max_f32_e32 v0, v0, v0
	v_med3_f32 v2, v2, s97, v13
	v_med3_f32 v0, v0, s97, v13
	v_cvt_pk_fp8_f32 v7, v2, v0 op_sel:[0,0,1]
	v_or_b32_e32 v0, s8, v251
	v_ashrrev_i32_e32 v1, 31, v0
	v_lshlrev_b64 v[0:1], s45, v[0:1]
	v_add_u32_e32 v10, v214, v250
	v_lshl_add_u64 v[8:9], v[0:1], 0, s[2:3]
	ds_read_b128 v[0:3], v10
	v_lshlrev_b64 v[8:9], 10, v[8:9]
	v_lshl_add_u64 v[8:9], v[208:209], 0, v[8:9]
	global_store_dwordx4 v[8:9], v[4:7], off
	ds_read_b128 v[4:7], v10 offset:16
	s_waitcnt lgkmcnt(1)
	v_lshlrev_b32_e32 v8, 16, v0
	v_and_b32_e32 v0, 0xffff0000, v0
	v_max_f32_e32 v0, v0, v0
	v_med3_f32 v9, v0, s97, v13
	v_lshlrev_b32_e32 v0, 16, v1
	v_max_f32_e32 v8, v8, v8
	v_max_f32_e32 v0, v0, v0
	v_med3_f32 v8, v8, s97, v13
	v_med3_f32 v10, v0, s97, v13
	v_cvt_pk_fp8_f32 v0, v8, v9
	v_and_b32_e32 v1, 0xffff0000, v1
	v_max_f32_e32 v1, v1, v1
	v_med3_f32 v1, v1, s97, v13
	v_cvt_pk_fp8_f32 v0, v10, v1 op_sel:[0,0,1]
	v_lshlrev_b32_e32 v1, 16, v2
	v_max_f32_e32 v1, v1, v1
	v_med3_f32 v8, v1, s97, v13
	v_and_b32_e32 v1, 0xffff0000, v2
	v_max_f32_e32 v1, v1, v1
	v_med3_f32 v2, v1, s97, v13
	v_lshlrev_b32_e32 v1, 16, v3
	v_max_f32_e32 v1, v1, v1
	v_med3_f32 v9, v1, s97, v13
	v_cvt_pk_fp8_f32 v1, v8, v2
	v_and_b32_e32 v2, 0xffff0000, v3
	v_max_f32_e32 v2, v2, v2
	v_med3_f32 v2, v2, s97, v13
	v_cvt_pk_fp8_f32 v1, v9, v2 op_sel:[0,0,1]
	s_waitcnt lgkmcnt(0)
	v_lshlrev_b32_e32 v2, 16, v4
	v_max_f32_e32 v2, v2, v2
	v_med3_f32 v3, v2, s97, v13
	v_and_b32_e32 v2, 0xffff0000, v4
	v_max_f32_e32 v2, v2, v2
	v_med3_f32 v4, v2, s97, v13
	v_lshlrev_b32_e32 v2, 16, v5
	v_max_f32_e32 v2, v2, v2
	v_med3_f32 v8, v2, s97, v13
	v_cvt_pk_fp8_f32 v2, v3, v4
	v_and_b32_e32 v3, 0xffff0000, v5
	v_max_f32_e32 v3, v3, v3
	v_med3_f32 v3, v3, s97, v13
	v_cvt_pk_fp8_f32 v2, v8, v3 op_sel:[0,0,1]
	v_lshlrev_b32_e32 v3, 16, v6
	v_max_f32_e32 v3, v3, v3
	v_med3_f32 v4, v3, s97, v13
	v_and_b32_e32 v3, 0xffff0000, v6
	v_max_f32_e32 v3, v3, v3
	v_med3_f32 v5, v3, s97, v13
	v_lshlrev_b32_e32 v3, 16, v7
	v_max_f32_e32 v3, v3, v3
	v_med3_f32 v6, v3, s97, v13
	v_cvt_pk_fp8_f32 v3, v4, v5
	v_and_b32_e32 v4, 0xffff0000, v7
	v_max_f32_e32 v4, v4, v4
	v_med3_f32 v4, v4, s97, v13
	v_cvt_pk_fp8_f32 v3, v6, v4 op_sel:[0,0,1]
	v_or_b32_e32 v4, s8, v253
	v_ashrrev_i32_e32 v5, 31, v4
	v_lshlrev_b64 v[4:5], s45, v[4:5]
	v_lshl_add_u64 v[4:5], v[4:5], 0, s[2:3]
	v_lshlrev_b64 v[4:5], 10, v[4:5]
	v_lshl_add_u64 v[4:5], v[208:209], 0, v[4:5]
	global_store_dwordx4 v[4:5], v[0:3], off
	v_add_u32_e32 v4, v216, v250
	ds_read_b128 v[0:3], v4
	ds_read_b128 v[4:7], v4 offset:16
	v_or_b32_e32 v8, s8, v217
	v_ashrrev_i32_e32 v9, 31, v8
	v_lshlrev_b64 v[8:9], s45, v[8:9]
	s_waitcnt lgkmcnt(1)
	v_lshlrev_b32_e32 v11, 16, v0
	v_and_b32_e32 v0, 0xffff0000, v0
	v_max_f32_e32 v11, v11, v11
	v_max_f32_e32 v0, v0, v0
	v_med3_f32 v11, v11, s97, v13
	v_med3_f32 v12, v0, s97, v13
	v_cvt_pk_fp8_f32 v0, v11, v12
	v_lshlrev_b32_e32 v10, 16, v1
	v_and_b32_e32 v1, 0xffff0000, v1
	v_max_f32_e32 v10, v10, v10
	v_max_f32_e32 v1, v1, v1
	v_med3_f32 v10, v10, s97, v13
	v_med3_f32 v1, v1, s97, v13
	v_cvt_pk_fp8_f32 v0, v10, v1 op_sel:[0,0,1]
	v_lshlrev_b32_e32 v1, 16, v3
	v_max_f32_e32 v1, v1, v1
	v_med3_f32 v10, v1, s97, v13
	v_lshlrev_b32_e32 v1, 16, v2
	v_max_f32_e32 v1, v1, v1
	v_med3_f32 v11, v1, s97, v13
	v_and_b32_e32 v1, 0xffff0000, v2
	v_max_f32_e32 v1, v1, v1
	v_med3_f32 v2, v1, s97, v13
	v_cvt_pk_fp8_f32 v1, v11, v2
	v_and_b32_e32 v2, 0xffff0000, v3
	v_max_f32_e32 v2, v2, v2
	v_med3_f32 v2, v2, s97, v13
	v_cvt_pk_fp8_f32 v1, v10, v2 op_sel:[0,0,1]
	s_waitcnt lgkmcnt(0)
	v_lshlrev_b32_e32 v2, 16, v5
	v_max_f32_e32 v2, v2, v2
	v_med3_f32 v3, v2, s97, v13
	v_lshlrev_b32_e32 v2, 16, v4
	v_max_f32_e32 v2, v2, v2
	v_med3_f32 v10, v2, s97, v13
	v_and_b32_e32 v2, 0xffff0000, v4
	v_max_f32_e32 v2, v2, v2
	v_med3_f32 v4, v2, s97, v13
	v_cvt_pk_fp8_f32 v2, v10, v4
	v_and_b32_e32 v4, 0xffff0000, v5
	v_max_f32_e32 v4, v4, v4
	v_med3_f32 v4, v4, s97, v13
	v_cvt_pk_fp8_f32 v2, v3, v4 op_sel:[0,0,1]
	v_lshlrev_b32_e32 v3, 16, v7
	v_max_f32_e32 v3, v3, v3
	v_med3_f32 v4, v3, s97, v13
	v_lshlrev_b32_e32 v3, 16, v6
	v_max_f32_e32 v3, v3, v3
	v_med3_f32 v5, v3, s97, v13
	v_and_b32_e32 v3, 0xffff0000, v6
	v_max_f32_e32 v3, v3, v3
	v_med3_f32 v6, v3, s97, v13
	v_cvt_pk_fp8_f32 v3, v5, v6
	v_and_b32_e32 v5, 0xffff0000, v7
	v_max_f32_e32 v5, v5, v5
	v_med3_f32 v5, v5, s97, v13
	v_cvt_pk_fp8_f32 v3, v4, v5 op_sel:[0,0,1]
	v_lshl_add_u64 v[4:5], v[8:9], 0, s[2:3]
	v_lshlrev_b64 v[4:5], 10, v[4:5]
	v_lshl_add_u64 v[4:5], v[208:209], 0, v[4:5]
	global_store_dwordx4 v[4:5], v[0:3], off
	s_waitcnt lgkmcnt(0)
	s_nop 1
	v_mov_b64_e32 v[0:1], v[64:65]
	v_mov_b64_e32 v[2:3], v[66:67]
	v_mov_b64_e32 v[4:5], v[68:69]
	v_mov_b64_e32 v[6:7], v[70:71]
	v_mov_b64_e32 v[8:9], v[72:73]
	v_mov_b64_e32 v[10:11], v[74:75]
	v_mov_b64_e32 v[12:13], v[76:77]
	v_mov_b64_e32 v[14:15], v[78:79]

; #define LAS __attribute__((address_space(3)))
; #define CVT_PK_FP8_SAT(a, b, old, hi) __builtin_amdgcn_cvt_pk_fp8_f32(__builtin_amdgcn_fmed3f((a), -448.0f, 448.0f), __builtin_amdgcn_fmed3f((b), -448.0f, 448.0f), (old), (hi))
; __device__ __forceinline__ unsigned cvt_pk_bf16(float lo, float hi) { unsigned r; asm volatile("v_cvt_pk_bf16_f32 %0, %1, %2" : "=v"(r) : "v"(lo), "v"(hi)); return r; }
; __device__ __forceinline__ void cvt_finish(const CvtItem& it, float (&v)[32], LAS float* scr, int lane) {
;     ...
; #pragma unroll
;     for (int i = 0; i < 32; ++i) { const int kk = 2 * i + (lane >> 5); scr[kk * 33 + (lane & 31)] = v[i]; }
;     asm volatile("s_waitcnt lgkmcnt(0)" ::: "memory");
;     const int c = lane & 7;
; #pragma unroll
;     for (int j = 0; j < 4; ++j) { const int n = it.n0 + (lane >> 3) + 8 * j; const LAS float* s = scr + (8 * c) * 33 + (lane >> 3) + 8 * j;
;         const int row = it.rowmode == 0 ? n : ((n >> 7) * 256 + (it.rowmode == 2 ? 128 : 0) + (n & 127));
;         if (it.fp8) { int w0 = CVT_PK_FP8_SAT(s[0 * 33] * FP8_WSCALE, s[1 * 33] * FP8_WSCALE, 0, false); w0 = CVT_PK_FP8_SAT(s[2 * 33] * FP8_WSCALE, s[3 * 33] * FP8_WSCALE, w0, true);
;             int w1 = CVT_PK_FP8_SAT(s[4 * 33] * FP8_WSCALE, s[5 * 33] * FP8_WSCALE, 0, false); w1 = CVT_PK_FP8_SAT(s[6 * 33] * FP8_WSCALE, s[7 * 33] * FP8_WSCALE, w1, true);
;             u32x2 o8; o8.x = (unsigned)w0; o8.y = (unsigned)w1; *(u32x2*)((unsigned char*)it.WT + (size_t)row * it.K + it.k0 + 8 * c) = o8; continue; }
;         u32x4 o; o.x = cvt_pk_bf16(s[0 * 33], s[1 * 33]); o.y = cvt_pk_bf16(s[2 * 33], s[3 * 33]); o.z = cvt_pk_bf16(s[4 * 33], s[5 * 33]); o.w = cvt_pk_bf16(s[6 * 33], s[7 * 33]);
;         *(u32x4*)(it.WT + (size_t)row * it.K + it.k0 + 8 * c) = o; }
;     asm volatile("s_waitcnt lgkmcnt(0)" ::: "memory");
; }
.LBB0_1019:
	ds_write2_b32 v78, v32, v33 offset1:66
	s_waitcnt lgkmcnt(0)
	ds_write2_b32 v78, v34, v35 offset0:132 offset1:198
	v_add_u32_e32 v32, 0x400, v78
	ds_write2_b32 v32, v36, v37 offset0:8 offset1:74
	ds_write2_b32 v32, v38, v39 offset0:140 offset1:206
	v_add_u32_e32 v32, 0x800, v78
	ds_write2_b32 v32, v40, v41 offset0:16 offset1:82
	ds_write2_b32 v32, v42, v43 offset0:148 offset1:214
	v_add_u32_e32 v32, 0xc00, v78
	ds_write2_b32 v32, v44, v45 offset0:24 offset1:90
	ds_write2_b32 v32, v46, v47 offset0:156 offset1:222
	v_add_u32_e32 v32, 0x1000, v78
	ds_write2_b32 v32, v48, v49 offset0:32 offset1:98
	ds_write2_b32 v32, v50, v51 offset0:164 offset1:230
	v_add_u32_e32 v32, 0x1400, v78
	ds_write2_b32 v32, v52, v53 offset0:40 offset1:106
	ds_write2_b32 v32, v54, v55 offset0:172 offset1:238
	v_add_u32_e32 v32, 0x1800, v78
	ds_write2_b32 v32, v56, v57 offset0:48 offset1:114
	ds_write2_b32 v32, v58, v59 offset0:180 offset1:246
	v_add_u32_e32 v32, 0x1c00, v78
	ds_write2_b32 v32, v60, v61 offset0:56 offset1:122
	ds_write2_b32 v32, v62, v63 offset0:188 offset1:254
	v_add_u32_e32 v32, s46, v73
	s_cmp_eq_u32 s47, 0
	s_cselect_b64 s[8:9], -1, 0
	v_lshlrev_b32_e32 v33, 1, v32
	s_cmp_eq_u32 s47, 2
	s_waitcnt lgkmcnt(0)
	v_and_b32_e32 v33, 0x7fffff00, v33
	s_cselect_b32 s30, 0x80, 0
	v_and_b32_e32 v34, 0x7f, v32
	v_or3_b32 v33, v33, v34, s30
	ds_read_b32 v34, v74
	s_cmp_lg_u32 s1, 0
	s_cselect_b64 s[28:29], -1, 0
	s_cmp_eq_u32 s1, 0
	v_cndmask_b32_e64 v33, v33, v32, s[8:9]
	s_cbranch_scc1 .LBB0_1033
	ds_read2_b32 v[36:37], v74 offset0:33 offset1:66
	ds_read2_b32 v[38:39], v74 offset0:99 offset1:132
	s_waitcnt lgkmcnt(0)
	v_mul_f32_e32 v32, 0x42800000, v34
	v_med3_f32 v32, v32, s97, v219
	s_mov_b32 s1, s51
	v_mul_f32_e32 v35, 0x42800000, v36
	v_med3_f32 v35, v35, s97, v219
	v_cvt_pk_fp8_f32 v36, v32, v35
	v_mul_f32_e32 v32, 0x42800000, v37
	v_mul_f32_e32 v35, 0x42800000, v38
	v_med3_f32 v32, v32, s97, v219
	v_med3_f32 v35, v35, s97, v219
	v_cvt_pk_fp8_f32 v36, v32, v35 op_sel:[0,0,1]
	v_mul_f32_e32 v32, 0x42800000, v39
	ds_read2_b32 v[38:39], v74 offset0:165 offset1:198
	v_med3_f32 v32, v32, s97, v219
	s_waitcnt lgkmcnt(0)
	v_mul_f32_e32 v35, 0x42800000, v38
	v_med3_f32 v35, v35, s97, v219
	v_cvt_pk_fp8_f32 v37, v32, v35
	ds_read_b32 v35, v74 offset:924
	v_mul_f32_e32 v32, 0x42800000, v39
	v_med3_f32 v32, v32, s97, v219
	v_mov_b64_e32 v[38:39], s[22:23]
	v_mad_u64_u32 v[38:39], s[10:11], v33, s19, v[38:39]
	s_waitcnt lgkmcnt(0)
	v_mul_f32_e32 v35, 0x42800000, v35
	v_med3_f32 v35, v35, s97, v219
	v_cvt_pk_fp8_f32 v37, v32, v35 op_sel:[0,0,1]
	v_lshl_add_u64 v[38:39], v[38:39], 0, s[0:1]
	v_lshl_add_u64 v[38:39], v[38:39], 0, v[66:67]
	global_store_dwordx2 v[38:39], v[36:37], off
	v_lshlrev_b32_e32 v32, 1, v66
	s_cbranch_execnz .LBB0_1022

; #define LAS __attribute__((address_space(3)))
; #define CVT_PK_FP8_SAT(a, b, old, hi) __builtin_amdgcn_cvt_pk_fp8_f32(__builtin_amdgcn_fmed3f((a), -448.0f, 448.0f), __builtin_amdgcn_fmed3f((b), -448.0f, 448.0f), (old), (hi))
; __device__ __forceinline__ unsigned cvt_pk_bf16(float lo, float hi) { unsigned r; asm volatile("v_cvt_pk_bf16_f32 %0, %1, %2" : "=v"(r) : "v"(lo), "v"(hi)); return r; }
; __device__ __forceinline__ void cvt_finish(const CvtItem& it, float (&v)[32], LAS float* scr, int lane) {
;     ...
;     for (int j = 0; j < 4; ++j) { const int n = it.n0 + (lane >> 3) + 8 * j; const LAS float* s = scr + (8 * c) * 33 + (lane >> 3) + 8 * j;
;         const int row = it.rowmode == 0 ? n : ((n >> 7) * 256 + (it.rowmode == 2 ? 128 : 0) + (n & 127));
;         if (it.fp8) { int w0 = CVT_PK_FP8_SAT(s[0 * 33] * FP8_WSCALE, s[1 * 33] * FP8_WSCALE, 0, false); w0 = CVT_PK_FP8_SAT(s[2 * 33] * FP8_WSCALE, s[3 * 33] * FP8_WSCALE, w0, true);
;             int w1 = CVT_PK_FP8_SAT(s[4 * 33] * FP8_WSCALE, s[5 * 33] * FP8_WSCALE, 0, false); w1 = CVT_PK_FP8_SAT(s[6 * 33] * FP8_WSCALE, s[7 * 33] * FP8_WSCALE, w1, true);
;             u32x2 o8; o8.x = (unsigned)w0; o8.y = (unsigned)w1; *(u32x2*)((unsigned char*)it.WT + (size_t)row * it.K + it.k0 + 8 * c) = o8; continue; }
;         u32x4 o; o.x = cvt_pk_bf16(s[0 * 33], s[1 * 33]); o.y = cvt_pk_bf16(s[2 * 33], s[3 * 33]); o.z = cvt_pk_bf16(s[4 * 33], s[5 * 33]); o.w = cvt_pk_bf16(s[6 * 33], s[7 * 33]);
;         *(u32x4*)(it.WT + (size_t)row * it.K + it.k0 + 8 * c) = o; }
.LBB0_1022:
	v_add_u32_e32 v33, s46, v75
	s_waitcnt lgkmcnt(0)
	v_lshlrev_b32_e32 v34, 1, v33
	v_and_b32_e32 v34, 0x7fffff00, v34
	v_and_b32_e32 v35, 0x7f, v33
	v_or3_b32 v35, v34, v35, s30
	ds_read_b32 v34, v74 offset:32
	v_cndmask_b32_e64 v36, 0, 1, s[28:29]
	v_cmp_ne_u32_e64 s[10:11], 1, v36
	s_andn2_b64 vcc, exec, s[28:29]
	v_cndmask_b32_e64 v33, v35, v33, s[8:9]
	s_cbranch_vccnz .LBB0_1034
	ds_read2_b32 v[36:37], v74 offset0:41 offset1:74
	s_waitcnt lgkmcnt(1)
	v_mul_f32_e32 v35, 0x42800000, v34
	v_med3_f32 v35, v35, s97, v219
	s_mov_b32 s1, s51
	s_waitcnt lgkmcnt(0)
	v_mul_f32_e32 v36, 0x42800000, v36
	v_med3_f32 v38, v36, s97, v219
	v_cvt_pk_fp8_f32 v36, v35, v38
	ds_read2_b32 v[38:39], v74 offset0:107 offset1:140
	v_mul_f32_e32 v35, 0x42800000, v37
	v_med3_f32 v35, v35, s97, v219
	s_waitcnt lgkmcnt(0)
	v_mul_f32_e32 v37, 0x42800000, v38
	v_med3_f32 v37, v37, s97, v219
	v_cvt_pk_fp8_f32 v36, v35, v37 op_sel:[0,0,1]
	v_mul_f32_e32 v35, 0x42800000, v39
	ds_read2_b32 v[38:39], v74 offset0:173 offset1:206
	v_med3_f32 v35, v35, s97, v219
	s_waitcnt lgkmcnt(0)
	v_mul_f32_e32 v37, 0x42800000, v38
	v_med3_f32 v38, v37, s97, v219
	v_cvt_pk_fp8_f32 v37, v35, v38
	ds_read_b32 v38, v74 offset:956
	v_mul_f32_e32 v35, 0x42800000, v39
	v_med3_f32 v35, v35, s97, v219
	s_waitcnt lgkmcnt(0)
	v_mul_f32_e32 v38, 0x42800000, v38
	v_med3_f32 v38, v38, s97, v219
	v_cvt_pk_fp8_f32 v37, v35, v38 op_sel:[0,0,1]
	v_mov_b64_e32 v[38:39], s[22:23]
	v_mad_u64_u32 v[38:39], s[28:29], v33, s19, v[38:39]
	v_lshl_add_u64 v[38:39], v[38:39], 0, s[0:1]
	v_lshl_add_u64 v[38:39], v[38:39], 0, v[66:67]
	global_store_dwordx2 v[38:39], v[36:37], off
	s_cbranch_execnz .LBB0_1025

; #define LAS __attribute__((address_space(3)))
; #define CVT_PK_FP8_SAT(a, b, old, hi) __builtin_amdgcn_cvt_pk_fp8_f32(__builtin_amdgcn_fmed3f((a), -448.0f, 448.0f), __builtin_amdgcn_fmed3f((b), -448.0f, 448.0f), (old), (hi))
; __device__ __forceinline__ unsigned cvt_pk_bf16(float lo, float hi) { unsigned r; asm volatile("v_cvt_pk_bf16_f32 %0, %1, %2" : "=v"(r) : "v"(lo), "v"(hi)); return r; }
; __device__ __forceinline__ void cvt_finish(const CvtItem& it, float (&v)[32], LAS float* scr, int lane) {
;     ...
;     for (int j = 0; j < 4; ++j) { const int n = it.n0 + (lane >> 3) + 8 * j; const LAS float* s = scr + (8 * c) * 33 + (lane >> 3) + 8 * j;
;         const int row = it.rowmode == 0 ? n : ((n >> 7) * 256 + (it.rowmode == 2 ? 128 : 0) + (n & 127));
;         if (it.fp8) { int w0 = CVT_PK_FP8_SAT(s[0 * 33] * FP8_WSCALE, s[1 * 33] * FP8_WSCALE, 0, false); w0 = CVT_PK_FP8_SAT(s[2 * 33] * FP8_WSCALE, s[3 * 33] * FP8_WSCALE, w0, true);
;             int w1 = CVT_PK_FP8_SAT(s[4 * 33] * FP8_WSCALE, s[5 * 33] * FP8_WSCALE, 0, false); w1 = CVT_PK_FP8_SAT(s[6 * 33] * FP8_WSCALE, s[7 * 33] * FP8_WSCALE, w1, true);
;             u32x2 o8; o8.x = (unsigned)w0; o8.y = (unsigned)w1; *(u32x2*)((unsigned char*)it.WT + (size_t)row * it.K + it.k0 + 8 * c) = o8; continue; }
;         u32x4 o; o.x = cvt_pk_bf16(s[0 * 33], s[1 * 33]); o.y = cvt_pk_bf16(s[2 * 33], s[3 * 33]); o.z = cvt_pk_bf16(s[4 * 33], s[5 * 33]); o.w = cvt_pk_bf16(s[6 * 33], s[7 * 33]);
;         *(u32x4*)(it.WT + (size_t)row * it.K + it.k0 + 8 * c) = o; }
.LBB0_1025:
	v_add_u32_e32 v33, s46, v76
	s_waitcnt lgkmcnt(0)
	v_lshlrev_b32_e32 v34, 1, v33
	v_and_b32_e32 v34, 0x7fffff00, v34
	v_and_b32_e32 v35, 0x7f, v33
	v_or3_b32 v34, v34, v35, s30
	v_cndmask_b32_e64 v33, v34, v33, s[8:9]
	ds_read_b32 v34, v74 offset:64
	s_and_b64 vcc, exec, s[10:11]
	s_cbranch_vccnz .LBB0_1035
	ds_read2_b32 v[36:37], v74 offset0:49 offset1:82
	s_waitcnt lgkmcnt(1)
	v_mul_f32_e32 v35, 0x42800000, v34
	v_med3_f32 v35, v35, s97, v219
	s_mov_b32 s1, s51
	s_waitcnt lgkmcnt(0)
	v_mul_f32_e32 v36, 0x42800000, v36
	v_med3_f32 v38, v36, s97, v219
	v_cvt_pk_fp8_f32 v36, v35, v38
	ds_read2_b32 v[38:39], v74 offset0:115 offset1:148
	v_mul_f32_e32 v35, 0x42800000, v37
	v_med3_f32 v35, v35, s97, v219
	s_waitcnt lgkmcnt(0)
	v_mul_f32_e32 v37, 0x42800000, v38
	v_med3_f32 v37, v37, s97, v219
	v_cvt_pk_fp8_f32 v36, v35, v37 op_sel:[0,0,1]
	v_mul_f32_e32 v35, 0x42800000, v39
	ds_read2_b32 v[38:39], v74 offset0:181 offset1:214
	v_med3_f32 v35, v35, s97, v219
	s_waitcnt lgkmcnt(0)
	v_mul_f32_e32 v37, 0x42800000, v38
	v_med3_f32 v38, v37, s97, v219
	v_cvt_pk_fp8_f32 v37, v35, v38
	ds_read_b32 v38, v74 offset:988
	v_mul_f32_e32 v35, 0x42800000, v39
	v_med3_f32 v35, v35, s97, v219
	s_waitcnt lgkmcnt(0)
	v_mul_f32_e32 v38, 0x42800000, v38
	v_med3_f32 v38, v38, s97, v219
	v_cvt_pk_fp8_f32 v37, v35, v38 op_sel:[0,0,1]
	v_mov_b64_e32 v[38:39], s[22:23]
	v_mad_u64_u32 v[38:39], s[28:29], v33, s19, v[38:39]
	v_lshl_add_u64 v[38:39], v[38:39], 0, s[0:1]
	v_lshl_add_u64 v[38:39], v[38:39], 0, v[66:67]
	global_store_dwordx2 v[38:39], v[36:37], off
	s_cbranch_execnz .LBB0_1028

; #define LAS __attribute__((address_space(3)))
; #define CVT_PK_FP8_SAT(a, b, old, hi) __builtin_amdgcn_cvt_pk_fp8_f32(__builtin_amdgcn_fmed3f((a), -448.0f, 448.0f), __builtin_amdgcn_fmed3f((b), -448.0f, 448.0f), (old), (hi))
; __device__ __forceinline__ unsigned cvt_pk_bf16(float lo, float hi) { unsigned r; asm volatile("v_cvt_pk_bf16_f32 %0, %1, %2" : "=v"(r) : "v"(lo), "v"(hi)); return r; }
; __device__ __forceinline__ void cvt_finish(const CvtItem& it, float (&v)[32], LAS float* scr, int lane) {
;     ...
;     for (int j = 0; j < 4; ++j) { const int n = it.n0 + (lane >> 3) + 8 * j; const LAS float* s = scr + (8 * c) * 33 + (lane >> 3) + 8 * j;
;         const int row = it.rowmode == 0 ? n : ((n >> 7) * 256 + (it.rowmode == 2 ? 128 : 0) + (n & 127));
;         if (it.fp8) { int w0 = CVT_PK_FP8_SAT(s[0 * 33] * FP8_WSCALE, s[1 * 33] * FP8_WSCALE, 0, false); w0 = CVT_PK_FP8_SAT(s[2 * 33] * FP8_WSCALE, s[3 * 33] * FP8_WSCALE, w0, true);
;             int w1 = CVT_PK_FP8_SAT(s[4 * 33] * FP8_WSCALE, s[5 * 33] * FP8_WSCALE, 0, false); w1 = CVT_PK_FP8_SAT(s[6 * 33] * FP8_WSCALE, s[7 * 33] * FP8_WSCALE, w1, true);
;             u32x2 o8; o8.x = (unsigned)w0; o8.y = (unsigned)w1; *(u32x2*)((unsigned char*)it.WT + (size_t)row * it.K + it.k0 + 8 * c) = o8; continue; }
;         u32x4 o; o.x = cvt_pk_bf16(s[0 * 33], s[1 * 33]); o.y = cvt_pk_bf16(s[2 * 33], s[3 * 33]); o.z = cvt_pk_bf16(s[4 * 33], s[5 * 33]); o.w = cvt_pk_bf16(s[6 * 33], s[7 * 33]);
;         *(u32x4*)(it.WT + (size_t)row * it.K + it.k0 + 8 * c) = o; }
.LBB0_1028:
	v_add_u32_e32 v33, s46, v77
	s_waitcnt lgkmcnt(0)
	v_lshlrev_b32_e32 v34, 1, v33
	v_and_b32_e32 v34, 0x7fffff00, v34
	v_and_b32_e32 v35, 0x7f, v33
	v_or3_b32 v34, v34, v35, s30
	v_cndmask_b32_e64 v33, v34, v33, s[8:9]
	ds_read_b32 v34, v74 offset:96
	s_and_b64 vcc, exec, s[10:11]
	s_cbranch_vccnz .LBB0_1036
	ds_read2_b32 v[36:37], v74 offset0:57 offset1:90
	s_waitcnt lgkmcnt(1)
	v_mul_f32_e32 v35, 0x42800000, v34
	v_med3_f32 v35, v35, s97, v219
	s_mov_b32 s1, s51
	s_waitcnt lgkmcnt(0)
	v_mul_f32_e32 v36, 0x42800000, v36
	v_med3_f32 v38, v36, s97, v219
	v_cvt_pk_fp8_f32 v36, v35, v38
	ds_read2_b32 v[38:39], v74 offset0:123 offset1:156
	v_mul_f32_e32 v35, 0x42800000, v37
	v_med3_f32 v35, v35, s97, v219
	s_waitcnt lgkmcnt(0)
	v_mul_f32_e32 v37, 0x42800000, v38
	v_med3_f32 v37, v37, s97, v219
	v_cvt_pk_fp8_f32 v36, v35, v37 op_sel:[0,0,1]
	v_mul_f32_e32 v35, 0x42800000, v39
	ds_read2_b32 v[38:39], v74 offset0:189 offset1:222
	v_med3_f32 v35, v35, s97, v219
	s_waitcnt lgkmcnt(0)
	v_mul_f32_e32 v37, 0x42800000, v38
	v_med3_f32 v38, v37, s97, v219
	v_cvt_pk_fp8_f32 v37, v35, v38
	ds_read_b32 v38, v74 offset:1020
	v_mul_f32_e32 v35, 0x42800000, v39
	v_med3_f32 v35, v35, s97, v219
	s_waitcnt lgkmcnt(0)
	v_mul_f32_e32 v38, 0x42800000, v38
	v_med3_f32 v38, v38, s97, v219
	v_cvt_pk_fp8_f32 v37, v35, v38 op_sel:[0,0,1]
	v_mov_b64_e32 v[38:39], s[22:23]
	v_mad_u64_u32 v[38:39], s[8:9], v33, s19, v[38:39]
	v_lshl_add_u64 v[38:39], v[38:39], 0, s[0:1]
	v_lshl_add_u64 v[38:39], v[38:39], 0, v[66:67]
	global_store_dwordx2 v[38:39], v[36:37], off
	s_cbranch_execnz .LBB0_1031

; template <int PH, bool PRB = false>
; __device__ __forceinline__ void run_phase(int layer, LAS unsigned char* lds, const int wv_) {
;     ...
;             for (int s0 = 0; s0 < 32; s0 += 16) {
;                 bf16x8 av[16], bv[16];
; #pragma unroll
;                 for (int s = 0; s < 16; ++s) { av[s] = *(const bf16x8*)(ap + 32 * (s0 + s)); bv[s] = *(const bf16x8*)(bp + 32 * (s0 + s)); }
; #pragma unroll
;                 for (int s = 0; s < 16; ++s) asm volatile("" : "+v"(av[s]), "+v"(bv[s]));
; #pragma unroll
;                 for (int s = 0; s < 16; ++s) acc = __builtin_amdgcn_mfma_f32_16x16x32_bf16(av[s], bv[s], acc, 0, 0, 0);
;                 if (cb == 0 && !PRB) {
; #pragma unroll
;                     for (int s = 0; s < 16; ++s) { const u32x4 b = __builtin_bit_cast(u32x4, av[s]);
;                         int w0 = __builtin_amdgcn_cvt_pk_fp8_f32(__uint_as_float(b.x << 16) * rs8, __uint_as_float(b.x & 0xffff0000u) * rs8, 0, false);
;                         w0 = __builtin_amdgcn_cvt_pk_fp8_f32(__uint_as_float(b.y << 16) * rs8, __uint_as_float(b.y & 0xffff0000u) * rs8, w0, true);
;                         int w1 = __builtin_amdgcn_cvt_pk_fp8_f32(__uint_as_float(b.z << 16) * rs8, __uint_as_float(b.z & 0xffff0000u) * rs8, 0, false);
;                         w1 = __builtin_amdgcn_cvt_pk_fp8_f32(__uint_as_float(b.w << 16) * rs8, __uint_as_float(b.w & 0xffff0000u) * rs8, w1, true);
;                         u32x2 o8; o8.x = (unsigned)w0; o8.y = (unsigned)w1; *(u32x2*)(h8 + 32 * (s0 + s)) = o8; }
;                 }
.LBB0_1445:
	v_lshlrev_b64 v[2:3], 11, v[0:1]
	v_lshl_add_u64 v[80:81], v[70:71], 0, v[2:3]
	global_load_dwordx4 v[88:91], v[72:73], off
	global_load_dwordx4 v[66:69], v[80:81], off
	global_load_dwordx4 v[60:63], v[80:81], off offset:64
	global_load_dwordx4 v[92:95], v[72:73], off offset:64
	global_load_dwordx4 v[96:99], v[72:73], off offset:128
	global_load_dwordx4 v[56:59], v[80:81], off offset:128
	global_load_dwordx4 v[52:55], v[80:81], off offset:192
	global_load_dwordx4 v[100:103], v[72:73], off offset:192
	global_load_dwordx4 v[104:107], v[72:73], off offset:256
	global_load_dwordx4 v[48:51], v[80:81], off offset:256
	global_load_dwordx4 v[44:47], v[80:81], off offset:320
	global_load_dwordx4 v[108:111], v[72:73], off offset:320
	global_load_dwordx4 v[112:115], v[72:73], off offset:384
	global_load_dwordx4 v[40:43], v[80:81], off offset:384
	global_load_dwordx4 v[36:39], v[80:81], off offset:448
	global_load_dwordx4 v[116:119], v[72:73], off offset:448
	global_load_dwordx4 v[120:123], v[72:73], off offset:512
	global_load_dwordx4 v[32:35], v[80:81], off offset:512
	global_load_dwordx4 v[28:31], v[80:81], off offset:576
	global_load_dwordx4 v[124:127], v[72:73], off offset:576
	global_load_dwordx4 v[128:131], v[72:73], off offset:640
	global_load_dwordx4 v[24:27], v[80:81], off offset:640
	global_load_dwordx4 v[20:23], v[80:81], off offset:704
	global_load_dwordx4 v[132:135], v[72:73], off offset:704
	global_load_dwordx4 v[136:139], v[72:73], off offset:768
	global_load_dwordx4 v[16:19], v[80:81], off offset:768
	global_load_dwordx4 v[12:15], v[80:81], off offset:832
	global_load_dwordx4 v[140:143], v[72:73], off offset:832
	global_load_dwordx4 v[144:147], v[72:73], off offset:896
	global_load_dwordx4 v[8:11], v[80:81], off offset:896
	global_load_dwordx4 v[4:7], v[80:81], off offset:960
	global_load_dwordx4 v[148:151], v[72:73], off offset:960
	v_lshlrev_b64 v[78:79], 10, v[0:1]
	v_lshl_add_u64 v[78:79], v[74:75], 0, v[78:79]
	s_and_b64 vcc, exec, s[10:11]
	s_waitcnt vmcnt(30)
	s_nop 0
	v_mfma_f32_16x16x32_bf16 v[88:91], v[66:69], v[88:91], 0
	s_waitcnt vmcnt(28)
	s_waitcnt vmcnt(26)
	v_mfma_f32_16x16x32_bf16 v[88:91], v[60:63], v[92:95], v[88:91]
	s_waitcnt vmcnt(24)
	s_waitcnt vmcnt(22)
	v_mfma_f32_16x16x32_bf16 v[88:91], v[56:59], v[96:99], v[88:91]
	s_waitcnt vmcnt(20)
	s_waitcnt vmcnt(18)
	v_mfma_f32_16x16x32_bf16 v[88:91], v[52:55], v[100:103], v[88:91]
	s_waitcnt vmcnt(16)
	s_waitcnt vmcnt(14)
	v_mfma_f32_16x16x32_bf16 v[88:91], v[48:51], v[104:107], v[88:91]
	s_waitcnt vmcnt(12)
	s_waitcnt vmcnt(10)
	v_mfma_f32_16x16x32_bf16 v[88:91], v[44:47], v[108:111], v[88:91]
	s_waitcnt vmcnt(8)
	s_waitcnt vmcnt(6)
	v_mfma_f32_16x16x32_bf16 v[88:91], v[40:43], v[112:115], v[88:91]
	s_waitcnt vmcnt(4)
	s_waitcnt vmcnt(2)
	v_mfma_f32_16x16x32_bf16 v[88:91], v[36:39], v[116:119], v[88:91]
	s_waitcnt vmcnt(0)
	v_mfma_f32_16x16x32_bf16 v[88:91], v[32:35], v[120:123], v[88:91]
	v_mfma_f32_16x16x32_bf16 v[88:91], v[28:31], v[124:127], v[88:91]
	v_mfma_f32_16x16x32_bf16 v[88:91], v[24:27], v[128:131], v[88:91]
	v_mfma_f32_16x16x32_bf16 v[88:91], v[20:23], v[132:135], v[88:91]
	v_mfma_f32_16x16x32_bf16 v[88:91], v[16:19], v[136:139], v[88:91]
	v_mfma_f32_16x16x32_bf16 v[88:91], v[12:15], v[140:143], v[88:91]
	v_mfma_f32_16x16x32_bf16 v[0:3], v[8:11], v[144:147], v[88:91]
	v_mfma_f32_16x16x32_bf16 v[0:3], v[4:7], v[148:151], v[0:3]
	s_cbranch_vccnz .LBB0_1447
	s_nop 4
	v_lshlrev_b32_e32 v88, 16, v66
	v_and_b32_e32 v66, 0xffff0000, v66
	v_mul_f32_e32 v88, v64, v88
	v_mul_f32_e32 v89, v64, v66
	v_cvt_pk_fp8_f32 v66, v88, v89
	v_lshlrev_b32_e32 v88, 16, v67
	v_and_b32_e32 v67, 0xffff0000, v67
	v_mul_f32_e32 v88, v64, v88
	v_mul_f32_e32 v67, v64, v67
	v_cvt_pk_fp8_f32 v66, v88, v67 op_sel:[0,0,1]
	v_lshlrev_b32_e32 v67, 16, v68
	v_mul_f32_e32 v88, v64, v67
	v_and_b32_e32 v67, 0xffff0000, v68
	v_mul_f32_e32 v68, v64, v67
	v_cvt_pk_fp8_f32 v67, v88, v68
	v_lshlrev_b32_e32 v68, 16, v69
	v_and_b32_e32 v69, 0xffff0000, v69
	v_mul_f32_e32 v68, v64, v68
	v_mul_f32_e32 v69, v64, v69
	v_cvt_pk_fp8_f32 v67, v68, v69 op_sel:[0,0,1]
	v_lshlrev_b32_e32 v68, 16, v60
	v_and_b32_e32 v60, 0xffff0000, v60
	v_mul_f32_e32 v68, v64, v68
	v_mul_f32_e32 v69, v64, v60
	v_cvt_pk_fp8_f32 v60, v68, v69
	v_lshlrev_b32_e32 v68, 16, v61
	v_and_b32_e32 v61, 0xffff0000, v61
	v_mul_f32_e32 v68, v64, v68
	v_mul_f32_e32 v61, v64, v61
	v_cvt_pk_fp8_f32 v60, v68, v61 op_sel:[0,0,1]
	v_lshlrev_b32_e32 v61, 16, v62
	v_mul_f32_e32 v68, v64, v61
	v_and_b32_e32 v61, 0xffff0000, v62
	v_mul_f32_e32 v62, v64, v61
	v_cvt_pk_fp8_f32 v61, v68, v62
	v_lshlrev_b32_e32 v62, 16, v63
	v_and_b32_e32 v63, 0xffff0000, v63
	v_mul_f32_e32 v62, v64, v62
	v_mul_f32_e32 v63, v64, v63
	v_cvt_pk_fp8_f32 v61, v62, v63 op_sel:[0,0,1]
	v_lshlrev_b32_e32 v62, 16, v56
	v_and_b32_e32 v56, 0xffff0000, v56
	v_mul_f32_e32 v62, v64, v62
	v_mul_f32_e32 v63, v64, v56
	v_cvt_pk_fp8_f32 v56, v62, v63
	v_lshlrev_b32_e32 v62, 16, v57
	v_and_b32_e32 v57, 0xffff0000, v57
	v_mul_f32_e32 v62, v64, v62
	v_mul_f32_e32 v57, v64, v57
	v_cvt_pk_fp8_f32 v56, v62, v57 op_sel:[0,0,1]
	v_lshlrev_b32_e32 v57, 16, v58
	v_mul_f32_e32 v62, v64, v57
	v_and_b32_e32 v57, 0xffff0000, v58
	v_mul_f32_e32 v58, v64, v57
	v_cvt_pk_fp8_f32 v57, v62, v58
	v_lshlrev_b32_e32 v58, 16, v59
	v_and_b32_e32 v59, 0xffff0000, v59
	v_mul_f32_e32 v58, v64, v58
	v_mul_f32_e32 v59, v64, v59
	v_cvt_pk_fp8_f32 v57, v58, v59 op_sel:[0,0,1]
	v_lshlrev_b32_e32 v58, 16, v52
	v_and_b32_e32 v52, 0xffff0000, v52
	v_mul_f32_e32 v58, v64, v58
	v_mul_f32_e32 v59, v64, v52
	v_cvt_pk_fp8_f32 v52, v58, v59
	v_lshlrev_b32_e32 v58, 16, v53
	v_and_b32_e32 v53, 0xffff0000, v53
; template <int PH, bool PRB = false>
; __device__ __forceinline__ void run_phase(int layer, LAS unsigned char* lds, const int wv_) {
;     ...
;                 if (cb == 0 && !PRB) {
; #pragma unroll
;                     for (int s = 0; s < 16; ++s) { const u32x4 b = __builtin_bit_cast(u32x4, av[s]);
;                         int w0 = __builtin_amdgcn_cvt_pk_fp8_f32(__uint_as_float(b.x << 16) * rs8, __uint_as_float(b.x & 0xffff0000u) * rs8, 0, false);
;                         w0 = __builtin_amdgcn_cvt_pk_fp8_f32(__uint_as_float(b.y << 16) * rs8, __uint_as_float(b.y & 0xffff0000u) * rs8, w0, true);
;                         int w1 = __builtin_amdgcn_cvt_pk_fp8_f32(__uint_as_float(b.z << 16) * rs8, __uint_as_float(b.z & 0xffff0000u) * rs8, 0, false);
;                         w1 = __builtin_amdgcn_cvt_pk_fp8_f32(__uint_as_float(b.w << 16) * rs8, __uint_as_float(b.w & 0xffff0000u) * rs8, w1, true);
;                         u32x2 o8; o8.x = (unsigned)w0; o8.y = (unsigned)w1; *(u32x2*)(h8 + 32 * (s0 + s)) = o8; }
;                 }
	v_mul_f32_e32 v58, v64, v58
	v_mul_f32_e32 v53, v64, v53
	v_cvt_pk_fp8_f32 v52, v58, v53 op_sel:[0,0,1]
	v_lshlrev_b32_e32 v53, 16, v54
	v_mul_f32_e32 v58, v64, v53
	v_and_b32_e32 v53, 0xffff0000, v54
	v_mul_f32_e32 v54, v64, v53
	v_cvt_pk_fp8_f32 v53, v58, v54
	v_lshlrev_b32_e32 v54, 16, v55
	v_and_b32_e32 v55, 0xffff0000, v55
	v_mul_f32_e32 v54, v64, v54
	v_mul_f32_e32 v55, v64, v55
	v_cvt_pk_fp8_f32 v53, v54, v55 op_sel:[0,0,1]
	global_store_dwordx2 v[78:79], v[66:67], off
	global_store_dwordx2 v[78:79], v[60:61], off offset:32
	global_store_dwordx2 v[78:79], v[56:57], off offset:64
	global_store_dwordx2 v[78:79], v[52:53], off offset:96
	v_lshlrev_b32_e32 v52, 16, v48
	v_and_b32_e32 v48, 0xffff0000, v48
	v_mul_f32_e32 v52, v64, v52
	v_mul_f32_e32 v53, v64, v48
	v_cvt_pk_fp8_f32 v48, v52, v53
	v_lshlrev_b32_e32 v52, 16, v49
	v_and_b32_e32 v49, 0xffff0000, v49
	v_mul_f32_e32 v52, v64, v52
	v_mul_f32_e32 v49, v64, v49
	v_cvt_pk_fp8_f32 v48, v52, v49 op_sel:[0,0,1]
	v_lshlrev_b32_e32 v49, 16, v50
	v_mul_f32_e32 v52, v64, v49
	v_and_b32_e32 v49, 0xffff0000, v50
	v_mul_f32_e32 v50, v64, v49
	v_cvt_pk_fp8_f32 v49, v52, v50
	v_lshlrev_b32_e32 v50, 16, v51
	v_and_b32_e32 v51, 0xffff0000, v51
	v_mul_f32_e32 v50, v64, v50
	v_mul_f32_e32 v51, v64, v51
	v_cvt_pk_fp8_f32 v49, v50, v51 op_sel:[0,0,1]
	v_lshlrev_b32_e32 v50, 16, v44
	v_and_b32_e32 v44, 0xffff0000, v44
	v_mul_f32_e32 v50, v64, v50
	v_mul_f32_e32 v51, v64, v44
	v_cvt_pk_fp8_f32 v44, v50, v51
	v_lshlrev_b32_e32 v50, 16, v45
	v_and_b32_e32 v45, 0xffff0000, v45
	v_mul_f32_e32 v50, v64, v50
	v_mul_f32_e32 v45, v64, v45
	v_cvt_pk_fp8_f32 v44, v50, v45 op_sel:[0,0,1]
	v_lshlrev_b32_e32 v45, 16, v46
	v_mul_f32_e32 v50, v64, v45
	v_and_b32_e32 v45, 0xffff0000, v46
	v_mul_f32_e32 v46, v64, v45
	v_cvt_pk_fp8_f32 v45, v50, v46
	v_lshlrev_b32_e32 v46, 16, v47
	v_and_b32_e32 v47, 0xffff0000, v47
	v_mul_f32_e32 v46, v64, v46
	v_mul_f32_e32 v47, v64, v47
	v_cvt_pk_fp8_f32 v45, v46, v47 op_sel:[0,0,1]
	v_lshlrev_b32_e32 v46, 16, v40
	v_and_b32_e32 v40, 0xffff0000, v40
	v_mul_f32_e32 v46, v64, v46
	v_mul_f32_e32 v47, v64, v40
	v_cvt_pk_fp8_f32 v40, v46, v47
	v_lshlrev_b32_e32 v46, 16, v41
	v_and_b32_e32 v41, 0xffff0000, v41
	v_mul_f32_e32 v46, v64, v46
	v_mul_f32_e32 v41, v64, v41
	v_cvt_pk_fp8_f32 v40, v46, v41 op_sel:[0,0,1]
	v_lshlrev_b32_e32 v41, 16, v42
	v_mul_f32_e32 v46, v64, v41
	v_and_b32_e32 v41, 0xffff0000, v42
	v_mul_f32_e32 v42, v64, v41
	v_cvt_pk_fp8_f32 v41, v46, v42
	v_lshlrev_b32_e32 v42, 16, v43
	v_and_b32_e32 v43, 0xffff0000, v43
	v_mul_f32_e32 v42, v64, v42
	v_mul_f32_e32 v43, v64, v43
	v_cvt_pk_fp8_f32 v41, v42, v43 op_sel:[0,0,1]
	v_lshlrev_b32_e32 v42, 16, v36
	v_and_b32_e32 v36, 0xffff0000, v36
	v_mul_f32_e32 v42, v64, v42
	v_mul_f32_e32 v43, v64, v36
	v_cvt_pk_fp8_f32 v36, v42, v43
	v_lshlrev_b32_e32 v42, 16, v37
	v_and_b32_e32 v37, 0xffff0000, v37
	v_mul_f32_e32 v42, v64, v42
	v_mul_f32_e32 v37, v64, v37
	v_cvt_pk_fp8_f32 v36, v42, v37 op_sel:[0,0,1]
	v_lshlrev_b32_e32 v37, 16, v38
	v_mul_f32_e32 v42, v64, v37
	v_and_b32_e32 v37, 0xffff0000, v38
	v_mul_f32_e32 v38, v64, v37
	v_cvt_pk_fp8_f32 v37, v42, v38
	v_lshlrev_b32_e32 v38, 16, v39
	v_and_b32_e32 v39, 0xffff0000, v39
	v_mul_f32_e32 v38, v64, v38
	v_mul_f32_e32 v39, v64, v39
	v_cvt_pk_fp8_f32 v37, v38, v39 op_sel:[0,0,1]
	global_store_dwordx2 v[78:79], v[48:49], off offset:128
	global_store_dwordx2 v[78:79], v[44:45], off offset:160
	global_store_dwordx2 v[78:79], v[40:41], off offset:192
	global_store_dwordx2 v[78:79], v[36:37], off offset:224
	v_lshlrev_b32_e32 v36, 16, v32
	v_and_b32_e32 v32, 0xffff0000, v32
	v_mul_f32_e32 v36, v64, v36
	v_mul_f32_e32 v37, v64, v32
	v_cvt_pk_fp8_f32 v32, v36, v37
	v_lshlrev_b32_e32 v36, 16, v33
	v_and_b32_e32 v33, 0xffff0000, v33
	v_mul_f32_e32 v36, v64, v36
	v_mul_f32_e32 v33, v64, v33
	v_cvt_pk_fp8_f32 v32, v36, v33 op_sel:[0,0,1]
	v_lshlrev_b32_e32 v33, 16, v34
	v_mul_f32_e32 v36, v64, v33
	v_and_b32_e32 v33, 0xffff0000, v34
	v_mul_f32_e32 v34, v64, v33
	v_cvt_pk_fp8_f32 v33, v36, v34
	v_lshlrev_b32_e32 v34, 16, v35
	v_and_b32_e32 v35, 0xffff0000, v35
	v_mul_f32_e32 v34, v64, v34
	v_mul_f32_e32 v35, v64, v35
	v_cvt_pk_fp8_f32 v33, v34, v35 op_sel:[0,0,1]
	v_lshlrev_b32_e32 v34, 16, v28
	v_and_b32_e32 v28, 0xffff0000, v28
	v_mul_f32_e32 v34, v64, v34
	v_mul_f32_e32 v35, v64, v28
	v_cvt_pk_fp8_f32 v28, v34, v35
	v_lshlrev_b32_e32 v34, 16, v29
	v_and_b32_e32 v29, 0xffff0000, v29
	v_mul_f32_e32 v34, v64, v34
	v_mul_f32_e32 v29, v64, v29
	v_cvt_pk_fp8_f32 v28, v34, v29 op_sel:[0,0,1]
	v_lshlrev_b32_e32 v29, 16, v30
	v_mul_f32_e32 v34, v64, v29
	v_and_b32_e32 v29, 0xffff0000, v30
	v_mul_f32_e32 v30, v64, v29
	v_cvt_pk_fp8_f32 v29, v34, v30
	v_lshlrev_b32_e32 v30, 16, v31
	v_and_b32_e32 v31, 0xffff0000, v31
	v_mul_f32_e32 v30, v64, v30
	v_mul_f32_e32 v31, v64, v31
	v_cvt_pk_fp8_f32 v29, v30, v31 op_sel:[0,0,1]
	v_lshlrev_b32_e32 v30, 16, v24
	v_and_b32_e32 v24, 0xffff0000, v24
	v_mul_f32_e32 v30, v64, v30
	v_mul_f32_e32 v31, v64, v24
	v_cvt_pk_fp8_f32 v24, v30, v31
	v_lshlrev_b32_e32 v30, 16, v25
	v_and_b32_e32 v25, 0xffff0000, v25
	v_mul_f32_e32 v30, v64, v30
	v_mul_f32_e32 v25, v64, v25
	v_cvt_pk_fp8_f32 v24, v30, v25 op_sel:[0,0,1]
	v_lshlrev_b32_e32 v25, 16, v26
	v_mul_f32_e32 v30, v64, v25
	v_and_b32_e32 v25, 0xffff0000, v26
	v_mul_f32_e32 v26, v64, v25
	v_cvt_pk_fp8_f32 v25, v30, v26
	v_lshlrev_b32_e32 v26, 16, v27
	v_and_b32_e32 v27, 0xffff0000, v27
	v_mul_f32_e32 v26, v64, v26
	v_mul_f32_e32 v27, v64, v27
	v_cvt_pk_fp8_f32 v25, v26, v27 op_sel:[0,0,1]
	v_lshlrev_b32_e32 v26, 16, v20
	v_and_b32_e32 v20, 0xffff0000, v20
	v_mul_f32_e32 v26, v64, v26
	v_mul_f32_e32 v27, v64, v20
; template <int PH, bool PRB = false>
; __device__ __forceinline__ void run_phase(int layer, LAS unsigned char* lds, const int wv_) {
;     ...
;             for (int s0 = 0; s0 < 32; s0 += 16) {
;                 bf16x8 av[16], bv[16];
; #pragma unroll
;                 for (int s = 0; s < 16; ++s) { av[s] = *(const bf16x8*)(ap + 32 * (s0 + s)); bv[s] = *(const bf16x8*)(bp + 32 * (s0 + s)); }
; #pragma unroll
;                 for (int s = 0; s < 16; ++s) asm volatile("" : "+v"(av[s]), "+v"(bv[s]));
; #pragma unroll
;                 for (int s = 0; s < 16; ++s) acc = __builtin_amdgcn_mfma_f32_16x16x32_bf16(av[s], bv[s], acc, 0, 0, 0);
;                 if (cb == 0 && !PRB) {
; #pragma unroll
;                     for (int s = 0; s < 16; ++s) { const u32x4 b = __builtin_bit_cast(u32x4, av[s]);
;                         int w0 = __builtin_amdgcn_cvt_pk_fp8_f32(__uint_as_float(b.x << 16) * rs8, __uint_as_float(b.x & 0xffff0000u) * rs8, 0, false);
;                         w0 = __builtin_amdgcn_cvt_pk_fp8_f32(__uint_as_float(b.y << 16) * rs8, __uint_as_float(b.y & 0xffff0000u) * rs8, w0, true);
;                         int w1 = __builtin_amdgcn_cvt_pk_fp8_f32(__uint_as_float(b.z << 16) * rs8, __uint_as_float(b.z & 0xffff0000u) * rs8, 0, false);
;                         w1 = __builtin_amdgcn_cvt_pk_fp8_f32(__uint_as_float(b.w << 16) * rs8, __uint_as_float(b.w & 0xffff0000u) * rs8, w1, true);
;                         u32x2 o8; o8.x = (unsigned)w0; o8.y = (unsigned)w1; *(u32x2*)(h8 + 32 * (s0 + s)) = o8; }
;                 }
	v_cvt_pk_fp8_f32 v20, v26, v27
	v_lshlrev_b32_e32 v26, 16, v21
	v_and_b32_e32 v21, 0xffff0000, v21
	v_mul_f32_e32 v26, v64, v26
	v_mul_f32_e32 v21, v64, v21
	v_cvt_pk_fp8_f32 v20, v26, v21 op_sel:[0,0,1]
	v_lshlrev_b32_e32 v21, 16, v22
	v_mul_f32_e32 v26, v64, v21
	v_and_b32_e32 v21, 0xffff0000, v22
	v_mul_f32_e32 v22, v64, v21
	v_cvt_pk_fp8_f32 v21, v26, v22
	v_lshlrev_b32_e32 v22, 16, v23
	v_and_b32_e32 v23, 0xffff0000, v23
	v_mul_f32_e32 v22, v64, v22
	v_mul_f32_e32 v23, v64, v23
	v_cvt_pk_fp8_f32 v21, v22, v23 op_sel:[0,0,1]
	global_store_dwordx2 v[78:79], v[32:33], off offset:256
	global_store_dwordx2 v[78:79], v[28:29], off offset:288
	global_store_dwordx2 v[78:79], v[24:25], off offset:320
	global_store_dwordx2 v[78:79], v[20:21], off offset:352
	v_lshlrev_b32_e32 v20, 16, v16
	v_and_b32_e32 v16, 0xffff0000, v16
	v_mul_f32_e32 v20, v64, v20
	v_mul_f32_e32 v21, v64, v16
	v_cvt_pk_fp8_f32 v16, v20, v21
	v_lshlrev_b32_e32 v20, 16, v17
	v_and_b32_e32 v17, 0xffff0000, v17
	v_mul_f32_e32 v20, v64, v20
	v_mul_f32_e32 v17, v64, v17
	v_cvt_pk_fp8_f32 v16, v20, v17 op_sel:[0,0,1]
	v_lshlrev_b32_e32 v17, 16, v18
	v_mul_f32_e32 v20, v64, v17
	v_and_b32_e32 v17, 0xffff0000, v18
	v_mul_f32_e32 v18, v64, v17
	v_cvt_pk_fp8_f32 v17, v20, v18
	v_lshlrev_b32_e32 v18, 16, v19
	v_and_b32_e32 v19, 0xffff0000, v19
	v_mul_f32_e32 v18, v64, v18
	v_mul_f32_e32 v19, v64, v19
	v_cvt_pk_fp8_f32 v17, v18, v19 op_sel:[0,0,1]
	v_lshlrev_b32_e32 v18, 16, v12
	v_and_b32_e32 v12, 0xffff0000, v12
	v_mul_f32_e32 v18, v64, v18
	v_mul_f32_e32 v19, v64, v12
	v_cvt_pk_fp8_f32 v12, v18, v19
	v_lshlrev_b32_e32 v18, 16, v13
	v_and_b32_e32 v13, 0xffff0000, v13
	v_mul_f32_e32 v18, v64, v18
	v_mul_f32_e32 v13, v64, v13
	v_cvt_pk_fp8_f32 v12, v18, v13 op_sel:[0,0,1]
	v_lshlrev_b32_e32 v13, 16, v14
	v_mul_f32_e32 v18, v64, v13
	v_and_b32_e32 v13, 0xffff0000, v14
	v_mul_f32_e32 v14, v64, v13
	v_cvt_pk_fp8_f32 v13, v18, v14
	v_lshlrev_b32_e32 v14, 16, v15
	v_and_b32_e32 v15, 0xffff0000, v15
	v_mul_f32_e32 v14, v64, v14
	v_mul_f32_e32 v15, v64, v15
	v_cvt_pk_fp8_f32 v13, v14, v15 op_sel:[0,0,1]
	v_lshlrev_b32_e32 v14, 16, v8
	v_and_b32_e32 v8, 0xffff0000, v8
	v_mul_f32_e32 v14, v64, v14
	v_mul_f32_e32 v15, v64, v8
	v_cvt_pk_fp8_f32 v8, v14, v15
	v_lshlrev_b32_e32 v14, 16, v9
	v_and_b32_e32 v9, 0xffff0000, v9
	v_mul_f32_e32 v14, v64, v14
	v_mul_f32_e32 v9, v64, v9
	v_cvt_pk_fp8_f32 v8, v14, v9 op_sel:[0,0,1]
	v_lshlrev_b32_e32 v9, 16, v10
	v_mul_f32_e32 v14, v64, v9
	v_and_b32_e32 v9, 0xffff0000, v10
	v_mul_f32_e32 v10, v64, v9
	v_cvt_pk_fp8_f32 v9, v14, v10
	v_lshlrev_b32_e32 v10, 16, v11
	v_and_b32_e32 v11, 0xffff0000, v11
	v_mul_f32_e32 v10, v64, v10
	v_mul_f32_e32 v11, v64, v11
	v_cvt_pk_fp8_f32 v9, v10, v11 op_sel:[0,0,1]
	v_lshlrev_b32_e32 v10, 16, v4
	v_and_b32_e32 v4, 0xffff0000, v4
	v_mul_f32_e32 v10, v64, v10
	v_mul_f32_e32 v11, v64, v4
	v_cvt_pk_fp8_f32 v4, v10, v11
	v_lshlrev_b32_e32 v10, 16, v5
	v_and_b32_e32 v5, 0xffff0000, v5
	v_mul_f32_e32 v10, v64, v10
	v_mul_f32_e32 v5, v64, v5
	v_cvt_pk_fp8_f32 v4, v10, v5 op_sel:[0,0,1]
	v_lshlrev_b32_e32 v5, 16, v6
	v_mul_f32_e32 v10, v64, v5
	v_and_b32_e32 v5, 0xffff0000, v6
	v_mul_f32_e32 v6, v64, v5
	v_cvt_pk_fp8_f32 v5, v10, v6
	v_lshlrev_b32_e32 v6, 16, v7
	v_and_b32_e32 v7, 0xffff0000, v7
	v_mul_f32_e32 v6, v64, v6
	v_mul_f32_e32 v7, v64, v7
	v_cvt_pk_fp8_f32 v5, v6, v7 op_sel:[0,0,1]
	global_store_dwordx2 v[78:79], v[16:17], off offset:384
	global_store_dwordx2 v[78:79], v[12:13], off offset:416
	global_store_dwordx2 v[78:79], v[8:9], off offset:448
	global_store_dwordx2 v[78:79], v[4:5], off offset:480
.LBB0_1447:
	global_load_dwordx4 v[66:69], v[80:81], off offset:1024
	s_nop 3
	global_load_dwordx4 v[88:91], v[72:73], off offset:1024
	global_load_dwordx4 v[92:95], v[72:73], off offset:1088
	global_load_dwordx4 v[60:63], v[80:81], off offset:1088
	global_load_dwordx4 v[56:59], v[80:81], off offset:1152
	global_load_dwordx4 v[96:99], v[72:73], off offset:1152
	global_load_dwordx4 v[100:103], v[72:73], off offset:1216
	global_load_dwordx4 v[52:55], v[80:81], off offset:1216
	global_load_dwordx4 v[48:51], v[80:81], off offset:1280
	global_load_dwordx4 v[104:107], v[72:73], off offset:1280
	global_load_dwordx4 v[108:111], v[72:73], off offset:1344
	global_load_dwordx4 v[44:47], v[80:81], off offset:1344
	global_load_dwordx4 v[40:43], v[80:81], off offset:1408
	global_load_dwordx4 v[112:115], v[72:73], off offset:1408
	global_load_dwordx4 v[116:119], v[72:73], off offset:1472
	global_load_dwordx4 v[36:39], v[80:81], off offset:1472
	global_load_dwordx4 v[32:35], v[80:81], off offset:1536
	global_load_dwordx4 v[120:123], v[72:73], off offset:1536
	global_load_dwordx4 v[124:127], v[72:73], off offset:1600
	global_load_dwordx4 v[28:31], v[80:81], off offset:1600
	global_load_dwordx4 v[24:27], v[80:81], off offset:1664
	global_load_dwordx4 v[128:131], v[72:73], off offset:1664
	global_load_dwordx4 v[132:135], v[72:73], off offset:1728
	global_load_dwordx4 v[20:23], v[80:81], off offset:1728
	global_load_dwordx4 v[16:19], v[80:81], off offset:1792
	global_load_dwordx4 v[136:139], v[72:73], off offset:1792
	global_load_dwordx4 v[140:143], v[72:73], off offset:1856
	global_load_dwordx4 v[12:15], v[80:81], off offset:1856
	global_load_dwordx4 v[8:11], v[80:81], off offset:1920
	global_load_dwordx4 v[144:147], v[72:73], off offset:1920
	global_load_dwordx4 v[148:151], v[72:73], off offset:1984
	global_load_dwordx4 v[4:7], v[80:81], off offset:1984
	s_and_b64 vcc, exec, s[10:11]
	s_waitcnt vmcnt(30)
	s_nop 0
	v_mfma_f32_16x16x32_bf16 v[0:3], v[66:69], v[88:91], v[0:3]
	s_waitcnt vmcnt(28)
	s_waitcnt vmcnt(26)
	v_mfma_f32_16x16x32_bf16 v[0:3], v[60:63], v[92:95], v[0:3]
	s_waitcnt vmcnt(24)
	s_waitcnt vmcnt(22)
	v_mfma_f32_16x16x32_bf16 v[0:3], v[56:59], v[96:99], v[0:3]
	s_waitcnt vmcnt(20)
	s_waitcnt vmcnt(18)
	v_mfma_f32_16x16x32_bf16 v[0:3], v[52:55], v[100:103], v[0:3]
	s_waitcnt vmcnt(16)
	s_waitcnt vmcnt(14)
	v_mfma_f32_16x16x32_bf16 v[0:3], v[48:51], v[104:107], v[0:3]
	s_waitcnt vmcnt(12)
	s_waitcnt vmcnt(10)
	v_mfma_f32_16x16x32_bf16 v[0:3], v[44:47], v[108:111], v[0:3]
	s_waitcnt vmcnt(8)
	s_waitcnt vmcnt(6)
	v_mfma_f32_16x16x32_bf16 v[0:3], v[40:43], v[112:115], v[0:3]
	s_waitcnt vmcnt(4)
	s_waitcnt vmcnt(2)
	v_mfma_f32_16x16x32_bf16 v[0:3], v[36:39], v[116:119], v[0:3]
	s_waitcnt vmcnt(0)
	v_mfma_f32_16x16x32_bf16 v[0:3], v[32:35], v[120:123], v[0:3]
	v_mfma_f32_16x16x32_bf16 v[0:3], v[28:31], v[124:127], v[0:3]
	v_mfma_f32_16x16x32_bf16 v[0:3], v[24:27], v[128:131], v[0:3]
	v_mfma_f32_16x16x32_bf16 v[0:3], v[20:23], v[132:135], v[0:3]
	v_mfma_f32_16x16x32_bf16 v[0:3], v[16:19], v[136:139], v[0:3]
	v_mfma_f32_16x16x32_bf16 v[0:3], v[12:15], v[140:143], v[0:3]
	v_mfma_f32_16x16x32_bf16 v[0:3], v[8:11], v[144:147], v[0:3]
	v_mfma_f32_16x16x32_bf16 v[0:3], v[4:7], v[148:151], v[0:3]
	s_cbranch_vccnz .LBB0_1449
; template <int PH, bool PRB = false>
; __device__ __forceinline__ void run_phase(int layer, LAS unsigned char* lds, const int wv_) {
;     ...
;                 if (cb == 0 && !PRB) {
; #pragma unroll
;                     for (int s = 0; s < 16; ++s) { const u32x4 b = __builtin_bit_cast(u32x4, av[s]);
;                         int w0 = __builtin_amdgcn_cvt_pk_fp8_f32(__uint_as_float(b.x << 16) * rs8, __uint_as_float(b.x & 0xffff0000u) * rs8, 0, false);
;                         w0 = __builtin_amdgcn_cvt_pk_fp8_f32(__uint_as_float(b.y << 16) * rs8, __uint_as_float(b.y & 0xffff0000u) * rs8, w0, true);
;                         int w1 = __builtin_amdgcn_cvt_pk_fp8_f32(__uint_as_float(b.z << 16) * rs8, __uint_as_float(b.z & 0xffff0000u) * rs8, 0, false);
;                         w1 = __builtin_amdgcn_cvt_pk_fp8_f32(__uint_as_float(b.w << 16) * rs8, __uint_as_float(b.w & 0xffff0000u) * rs8, w1, true);
;                         u32x2 o8; o8.x = (unsigned)w0; o8.y = (unsigned)w1; *(u32x2*)(h8 + 32 * (s0 + s)) = o8; }
;                 }
	v_lshlrev_b32_e32 v80, 16, v66
	v_and_b32_e32 v66, 0xffff0000, v66
	v_mul_f32_e32 v80, v64, v80
	v_mul_f32_e32 v81, v64, v66
	v_cvt_pk_fp8_f32 v66, v80, v81
	v_lshlrev_b32_e32 v80, 16, v67
	v_and_b32_e32 v67, 0xffff0000, v67
	v_mul_f32_e32 v80, v64, v80
	v_mul_f32_e32 v67, v64, v67
	v_cvt_pk_fp8_f32 v66, v80, v67 op_sel:[0,0,1]
	v_lshlrev_b32_e32 v67, 16, v68
	v_mul_f32_e32 v80, v64, v67
	v_and_b32_e32 v67, 0xffff0000, v68
	v_mul_f32_e32 v68, v64, v67
	v_cvt_pk_fp8_f32 v67, v80, v68
	v_lshlrev_b32_e32 v68, 16, v69
	v_and_b32_e32 v69, 0xffff0000, v69
	v_mul_f32_e32 v68, v64, v68
	v_mul_f32_e32 v69, v64, v69
	v_cvt_pk_fp8_f32 v67, v68, v69 op_sel:[0,0,1]
	v_lshlrev_b32_e32 v68, 16, v60
	v_and_b32_e32 v60, 0xffff0000, v60
	v_mul_f32_e32 v68, v64, v68
	v_mul_f32_e32 v69, v64, v60
	v_cvt_pk_fp8_f32 v60, v68, v69
	v_lshlrev_b32_e32 v68, 16, v61
	v_and_b32_e32 v61, 0xffff0000, v61
	v_mul_f32_e32 v68, v64, v68
	v_mul_f32_e32 v61, v64, v61
	v_cvt_pk_fp8_f32 v60, v68, v61 op_sel:[0,0,1]
	v_lshlrev_b32_e32 v61, 16, v62
	v_mul_f32_e32 v68, v64, v61
	v_and_b32_e32 v61, 0xffff0000, v62
	v_mul_f32_e32 v62, v64, v61
	v_cvt_pk_fp8_f32 v61, v68, v62
	v_lshlrev_b32_e32 v62, 16, v63
	v_and_b32_e32 v63, 0xffff0000, v63
	v_mul_f32_e32 v62, v64, v62
	v_mul_f32_e32 v63, v64, v63
	v_cvt_pk_fp8_f32 v61, v62, v63 op_sel:[0,0,1]
	v_lshlrev_b32_e32 v62, 16, v56
	v_and_b32_e32 v56, 0xffff0000, v56
	v_mul_f32_e32 v62, v64, v62
	v_mul_f32_e32 v63, v64, v56
	v_cvt_pk_fp8_f32 v56, v62, v63
	v_lshlrev_b32_e32 v62, 16, v57
	v_and_b32_e32 v57, 0xffff0000, v57
	v_mul_f32_e32 v62, v64, v62
	v_mul_f32_e32 v57, v64, v57
	v_cvt_pk_fp8_f32 v56, v62, v57 op_sel:[0,0,1]
	v_lshlrev_b32_e32 v57, 16, v58
	v_mul_f32_e32 v62, v64, v57
	v_and_b32_e32 v57, 0xffff0000, v58
	v_mul_f32_e32 v58, v64, v57
	v_cvt_pk_fp8_f32 v57, v62, v58
	v_lshlrev_b32_e32 v58, 16, v59
	v_and_b32_e32 v59, 0xffff0000, v59
	v_mul_f32_e32 v58, v64, v58
	v_mul_f32_e32 v59, v64, v59
	v_cvt_pk_fp8_f32 v57, v58, v59 op_sel:[0,0,1]
	v_lshlrev_b32_e32 v58, 16, v52
	v_and_b32_e32 v52, 0xffff0000, v52
	v_mul_f32_e32 v58, v64, v58
	v_mul_f32_e32 v59, v64, v52
	v_cvt_pk_fp8_f32 v52, v58, v59
	v_lshlrev_b32_e32 v58, 16, v53
	v_and_b32_e32 v53, 0xffff0000, v53
	v_mul_f32_e32 v58, v64, v58
	v_mul_f32_e32 v53, v64, v53
	v_cvt_pk_fp8_f32 v52, v58, v53 op_sel:[0,0,1]
	v_lshlrev_b32_e32 v53, 16, v54
	v_mul_f32_e32 v58, v64, v53
	v_and_b32_e32 v53, 0xffff0000, v54
	v_mul_f32_e32 v54, v64, v53
	v_cvt_pk_fp8_f32 v53, v58, v54
	v_lshlrev_b32_e32 v54, 16, v55
	v_and_b32_e32 v55, 0xffff0000, v55
	v_mul_f32_e32 v54, v64, v54
	v_mul_f32_e32 v55, v64, v55
	v_cvt_pk_fp8_f32 v53, v54, v55 op_sel:[0,0,1]
	global_store_dwordx2 v[78:79], v[66:67], off offset:512
	global_store_dwordx2 v[78:79], v[60:61], off offset:544
	global_store_dwordx2 v[78:79], v[56:57], off offset:576
	global_store_dwordx2 v[78:79], v[52:53], off offset:608
	v_lshlrev_b32_e32 v52, 16, v48
	v_and_b32_e32 v48, 0xffff0000, v48
	v_mul_f32_e32 v52, v64, v52
	v_mul_f32_e32 v53, v64, v48
	v_cvt_pk_fp8_f32 v48, v52, v53
	v_lshlrev_b32_e32 v52, 16, v49
	v_and_b32_e32 v49, 0xffff0000, v49
	v_mul_f32_e32 v52, v64, v52
	v_mul_f32_e32 v49, v64, v49
	v_cvt_pk_fp8_f32 v48, v52, v49 op_sel:[0,0,1]
	v_lshlrev_b32_e32 v49, 16, v50
	v_mul_f32_e32 v52, v64, v49
	v_and_b32_e32 v49, 0xffff0000, v50
	v_mul_f32_e32 v50, v64, v49
	v_cvt_pk_fp8_f32 v49, v52, v50
	v_lshlrev_b32_e32 v50, 16, v51
	v_and_b32_e32 v51, 0xffff0000, v51
	v_mul_f32_e32 v50, v64, v50
	v_mul_f32_e32 v51, v64, v51
	v_cvt_pk_fp8_f32 v49, v50, v51 op_sel:[0,0,1]
	v_lshlrev_b32_e32 v50, 16, v44
	v_and_b32_e32 v44, 0xffff0000, v44
	v_mul_f32_e32 v50, v64, v50
	v_mul_f32_e32 v51, v64, v44
	v_cvt_pk_fp8_f32 v44, v50, v51
	v_lshlrev_b32_e32 v50, 16, v45
	v_and_b32_e32 v45, 0xffff0000, v45
	v_mul_f32_e32 v50, v64, v50
	v_mul_f32_e32 v45, v64, v45
	v_cvt_pk_fp8_f32 v44, v50, v45 op_sel:[0,0,1]
	v_lshlrev_b32_e32 v45, 16, v46
	v_mul_f32_e32 v50, v64, v45
	v_and_b32_e32 v45, 0xffff0000, v46
	v_mul_f32_e32 v46, v64, v45
	v_cvt_pk_fp8_f32 v45, v50, v46
	v_lshlrev_b32_e32 v46, 16, v47
	v_and_b32_e32 v47, 0xffff0000, v47
	v_mul_f32_e32 v46, v64, v46
	v_mul_f32_e32 v47, v64, v47
	v_cvt_pk_fp8_f32 v45, v46, v47 op_sel:[0,0,1]
	v_lshlrev_b32_e32 v46, 16, v40
	v_and_b32_e32 v40, 0xffff0000, v40
	v_mul_f32_e32 v46, v64, v46
	v_mul_f32_e32 v47, v64, v40
	v_cvt_pk_fp8_f32 v40, v46, v47
	v_lshlrev_b32_e32 v46, 16, v41
	v_and_b32_e32 v41, 0xffff0000, v41
	v_mul_f32_e32 v46, v64, v46
	v_mul_f32_e32 v41, v64, v41
	v_cvt_pk_fp8_f32 v40, v46, v41 op_sel:[0,0,1]
	v_lshlrev_b32_e32 v41, 16, v42
	v_mul_f32_e32 v46, v64, v41
	v_and_b32_e32 v41, 0xffff0000, v42
	v_mul_f32_e32 v42, v64, v41
	v_cvt_pk_fp8_f32 v41, v46, v42
	v_lshlrev_b32_e32 v42, 16, v43
	v_and_b32_e32 v43, 0xffff0000, v43
	v_mul_f32_e32 v42, v64, v42
	v_mul_f32_e32 v43, v64, v43
	v_cvt_pk_fp8_f32 v41, v42, v43 op_sel:[0,0,1]
	v_lshlrev_b32_e32 v42, 16, v36
	v_and_b32_e32 v36, 0xffff0000, v36
	v_mul_f32_e32 v42, v64, v42
	v_mul_f32_e32 v43, v64, v36
	v_cvt_pk_fp8_f32 v36, v42, v43
	v_lshlrev_b32_e32 v42, 16, v37
	v_and_b32_e32 v37, 0xffff0000, v37
	v_mul_f32_e32 v42, v64, v42
	v_mul_f32_e32 v37, v64, v37
	v_cvt_pk_fp8_f32 v36, v42, v37 op_sel:[0,0,1]
	v_lshlrev_b32_e32 v37, 16, v38
	v_mul_f32_e32 v42, v64, v37
	v_and_b32_e32 v37, 0xffff0000, v38
	v_mul_f32_e32 v38, v64, v37
	v_cvt_pk_fp8_f32 v37, v42, v38
	v_lshlrev_b32_e32 v38, 16, v39
	v_and_b32_e32 v39, 0xffff0000, v39
	v_mul_f32_e32 v38, v64, v38
	v_mul_f32_e32 v39, v64, v39
	v_cvt_pk_fp8_f32 v37, v38, v39 op_sel:[0,0,1]
	global_store_dwordx2 v[78:79], v[48:49], off offset:640
	global_store_dwordx2 v[78:79], v[44:45], off offset:672
; template <int PH, bool PRB = false>
; __device__ __forceinline__ void run_phase(int layer, LAS unsigned char* lds, const int wv_) {
;     ...
;                 if (cb == 0 && !PRB) {
; #pragma unroll
;                     for (int s = 0; s < 16; ++s) { const u32x4 b = __builtin_bit_cast(u32x4, av[s]);
;                         int w0 = __builtin_amdgcn_cvt_pk_fp8_f32(__uint_as_float(b.x << 16) * rs8, __uint_as_float(b.x & 0xffff0000u) * rs8, 0, false);
;                         w0 = __builtin_amdgcn_cvt_pk_fp8_f32(__uint_as_float(b.y << 16) * rs8, __uint_as_float(b.y & 0xffff0000u) * rs8, w0, true);
;                         int w1 = __builtin_amdgcn_cvt_pk_fp8_f32(__uint_as_float(b.z << 16) * rs8, __uint_as_float(b.z & 0xffff0000u) * rs8, 0, false);
;                         w1 = __builtin_amdgcn_cvt_pk_fp8_f32(__uint_as_float(b.w << 16) * rs8, __uint_as_float(b.w & 0xffff0000u) * rs8, w1, true);
;                         u32x2 o8; o8.x = (unsigned)w0; o8.y = (unsigned)w1; *(u32x2*)(h8 + 32 * (s0 + s)) = o8; }
;                 }
	global_store_dwordx2 v[78:79], v[40:41], off offset:704
	global_store_dwordx2 v[78:79], v[36:37], off offset:736
	v_lshlrev_b32_e32 v36, 16, v32
	v_and_b32_e32 v32, 0xffff0000, v32
	v_mul_f32_e32 v36, v64, v36
	v_mul_f32_e32 v37, v64, v32
	v_cvt_pk_fp8_f32 v32, v36, v37
	v_lshlrev_b32_e32 v36, 16, v33
	v_and_b32_e32 v33, 0xffff0000, v33
	v_mul_f32_e32 v36, v64, v36
	v_mul_f32_e32 v33, v64, v33
	v_cvt_pk_fp8_f32 v32, v36, v33 op_sel:[0,0,1]
	v_lshlrev_b32_e32 v33, 16, v34
	v_mul_f32_e32 v36, v64, v33
	v_and_b32_e32 v33, 0xffff0000, v34
	v_mul_f32_e32 v34, v64, v33
	v_cvt_pk_fp8_f32 v33, v36, v34
	v_lshlrev_b32_e32 v34, 16, v35
	v_and_b32_e32 v35, 0xffff0000, v35
	v_mul_f32_e32 v34, v64, v34
	v_mul_f32_e32 v35, v64, v35
	v_cvt_pk_fp8_f32 v33, v34, v35 op_sel:[0,0,1]
	v_lshlrev_b32_e32 v34, 16, v28
	v_and_b32_e32 v28, 0xffff0000, v28
	v_mul_f32_e32 v34, v64, v34
	v_mul_f32_e32 v35, v64, v28
	v_cvt_pk_fp8_f32 v28, v34, v35
	v_lshlrev_b32_e32 v34, 16, v29
	v_and_b32_e32 v29, 0xffff0000, v29
	v_mul_f32_e32 v34, v64, v34
	v_mul_f32_e32 v29, v64, v29
	v_cvt_pk_fp8_f32 v28, v34, v29 op_sel:[0,0,1]
	v_lshlrev_b32_e32 v29, 16, v30
	v_mul_f32_e32 v34, v64, v29
	v_and_b32_e32 v29, 0xffff0000, v30
	v_mul_f32_e32 v30, v64, v29
	v_cvt_pk_fp8_f32 v29, v34, v30
	v_lshlrev_b32_e32 v30, 16, v31
	v_and_b32_e32 v31, 0xffff0000, v31
	v_mul_f32_e32 v30, v64, v30
	v_mul_f32_e32 v31, v64, v31
	v_cvt_pk_fp8_f32 v29, v30, v31 op_sel:[0,0,1]
	v_lshlrev_b32_e32 v30, 16, v24
	v_and_b32_e32 v24, 0xffff0000, v24
	v_mul_f32_e32 v30, v64, v30
	v_mul_f32_e32 v31, v64, v24
	v_cvt_pk_fp8_f32 v24, v30, v31
	v_lshlrev_b32_e32 v30, 16, v25
	v_and_b32_e32 v25, 0xffff0000, v25
	v_mul_f32_e32 v30, v64, v30
	v_mul_f32_e32 v25, v64, v25
	v_cvt_pk_fp8_f32 v24, v30, v25 op_sel:[0,0,1]
	v_lshlrev_b32_e32 v25, 16, v26
	v_mul_f32_e32 v30, v64, v25
	v_and_b32_e32 v25, 0xffff0000, v26
	v_mul_f32_e32 v26, v64, v25
	v_cvt_pk_fp8_f32 v25, v30, v26
	v_lshlrev_b32_e32 v26, 16, v27
	v_and_b32_e32 v27, 0xffff0000, v27
	v_mul_f32_e32 v26, v64, v26
	v_mul_f32_e32 v27, v64, v27
	v_cvt_pk_fp8_f32 v25, v26, v27 op_sel:[0,0,1]
	v_lshlrev_b32_e32 v26, 16, v20
	v_and_b32_e32 v20, 0xffff0000, v20
	v_mul_f32_e32 v26, v64, v26
	v_mul_f32_e32 v27, v64, v20
	v_cvt_pk_fp8_f32 v20, v26, v27
	v_lshlrev_b32_e32 v26, 16, v21
	v_and_b32_e32 v21, 0xffff0000, v21
	v_mul_f32_e32 v26, v64, v26
	v_mul_f32_e32 v21, v64, v21
	v_cvt_pk_fp8_f32 v20, v26, v21 op_sel:[0,0,1]
	v_lshlrev_b32_e32 v21, 16, v22
	v_mul_f32_e32 v26, v64, v21
	v_and_b32_e32 v21, 0xffff0000, v22
	v_mul_f32_e32 v22, v64, v21
	v_cvt_pk_fp8_f32 v21, v26, v22
	v_lshlrev_b32_e32 v22, 16, v23
	v_and_b32_e32 v23, 0xffff0000, v23
	v_mul_f32_e32 v22, v64, v22
	v_mul_f32_e32 v23, v64, v23
	v_cvt_pk_fp8_f32 v21, v22, v23 op_sel:[0,0,1]
	global_store_dwordx2 v[78:79], v[32:33], off offset:768
	global_store_dwordx2 v[78:79], v[28:29], off offset:800
	global_store_dwordx2 v[78:79], v[24:25], off offset:832
	global_store_dwordx2 v[78:79], v[20:21], off offset:864
	v_lshlrev_b32_e32 v20, 16, v16
	v_and_b32_e32 v16, 0xffff0000, v16
	v_mul_f32_e32 v20, v64, v20
	v_mul_f32_e32 v21, v64, v16
	v_cvt_pk_fp8_f32 v16, v20, v21
	v_lshlrev_b32_e32 v20, 16, v17
	v_and_b32_e32 v17, 0xffff0000, v17
	v_mul_f32_e32 v20, v64, v20
	v_mul_f32_e32 v17, v64, v17
	v_cvt_pk_fp8_f32 v16, v20, v17 op_sel:[0,0,1]
	v_lshlrev_b32_e32 v17, 16, v18
	v_mul_f32_e32 v20, v64, v17
	v_and_b32_e32 v17, 0xffff0000, v18
	v_mul_f32_e32 v18, v64, v17
	v_cvt_pk_fp8_f32 v17, v20, v18
	v_lshlrev_b32_e32 v18, 16, v19
	v_and_b32_e32 v19, 0xffff0000, v19
	v_mul_f32_e32 v18, v64, v18
	v_mul_f32_e32 v19, v64, v19
	v_cvt_pk_fp8_f32 v17, v18, v19 op_sel:[0,0,1]
	v_lshlrev_b32_e32 v18, 16, v12
	v_and_b32_e32 v12, 0xffff0000, v12
	v_mul_f32_e32 v18, v64, v18
	v_mul_f32_e32 v19, v64, v12
	v_cvt_pk_fp8_f32 v12, v18, v19
	v_lshlrev_b32_e32 v18, 16, v13
	v_and_b32_e32 v13, 0xffff0000, v13
	v_mul_f32_e32 v18, v64, v18
	v_mul_f32_e32 v13, v64, v13
	v_cvt_pk_fp8_f32 v12, v18, v13 op_sel:[0,0,1]
	v_lshlrev_b32_e32 v13, 16, v14
	v_mul_f32_e32 v18, v64, v13
	v_and_b32_e32 v13, 0xffff0000, v14
	v_mul_f32_e32 v14, v64, v13
	v_cvt_pk_fp8_f32 v13, v18, v14
	v_lshlrev_b32_e32 v14, 16, v15
	v_and_b32_e32 v15, 0xffff0000, v15
	v_mul_f32_e32 v14, v64, v14
	v_mul_f32_e32 v15, v64, v15
	v_cvt_pk_fp8_f32 v13, v14, v15 op_sel:[0,0,1]
	v_lshlrev_b32_e32 v14, 16, v8
	v_and_b32_e32 v8, 0xffff0000, v8
	v_mul_f32_e32 v14, v64, v14
	v_mul_f32_e32 v15, v64, v8
	v_cvt_pk_fp8_f32 v8, v14, v15
	v_lshlrev_b32_e32 v14, 16, v9
	v_and_b32_e32 v9, 0xffff0000, v9
	v_mul_f32_e32 v14, v64, v14
	v_mul_f32_e32 v9, v64, v9
	v_cvt_pk_fp8_f32 v8, v14, v9 op_sel:[0,0,1]
	v_lshlrev_b32_e32 v9, 16, v10
	v_mul_f32_e32 v14, v64, v9
	v_and_b32_e32 v9, 0xffff0000, v10
	v_mul_f32_e32 v10, v64, v9
	v_cvt_pk_fp8_f32 v9, v14, v10
	v_lshlrev_b32_e32 v10, 16, v11
	v_and_b32_e32 v11, 0xffff0000, v11
	v_mul_f32_e32 v10, v64, v10
	v_mul_f32_e32 v11, v64, v11
	v_cvt_pk_fp8_f32 v9, v10, v11 op_sel:[0,0,1]
	v_lshlrev_b32_e32 v10, 16, v4
	v_and_b32_e32 v4, 0xffff0000, v4
	v_mul_f32_e32 v10, v64, v10
	v_mul_f32_e32 v11, v64, v4
	v_cvt_pk_fp8_f32 v4, v10, v11
	v_lshlrev_b32_e32 v10, 16, v5
	v_and_b32_e32 v5, 0xffff0000, v5
	v_mul_f32_e32 v10, v64, v10
	v_mul_f32_e32 v5, v64, v5
	v_cvt_pk_fp8_f32 v4, v10, v5 op_sel:[0,0,1]
	v_lshlrev_b32_e32 v5, 16, v6
	v_mul_f32_e32 v10, v64, v5
	v_and_b32_e32 v5, 0xffff0000, v6
	v_mul_f32_e32 v6, v64, v5
	v_cvt_pk_fp8_f32 v5, v10, v6
	v_lshlrev_b32_e32 v6, 16, v7
	v_and_b32_e32 v7, 0xffff0000, v7
	v_mul_f32_e32 v6, v64, v6
	v_mul_f32_e32 v7, v64, v7
	v_cvt_pk_fp8_f32 v5, v6, v7 op_sel:[0,0,1]
	global_store_dwordx2 v[78:79], v[16:17], off offset:896
	global_store_dwordx2 v[78:79], v[12:13], off offset:928
	global_store_dwordx2 v[78:79], v[8:9], off offset:960
	global_store_dwordx2 v[78:79], v[4:5], off offset:992

; #define LAS __attribute__((address_space(3)))
; #define CVT_PK_FP8_SAT(a, b, old, hi) __builtin_amdgcn_cvt_pk_fp8_f32(__builtin_amdgcn_fmed3f((a), -448.0f, 448.0f), __builtin_amdgcn_fmed3f((b), -448.0f, 448.0f), (old), (hi))
; __device__ __forceinline__ unsigned cvt_pk_bf16(float lo, float hi) { unsigned r; asm volatile("v_cvt_pk_bf16_f32 %0, %1, %2" : "=v"(r) : "v"(lo), "v"(hi)); return r; }
; __device__ __forceinline__ void cvt_finish(const CvtItem& it, float (&v)[32], LAS float* scr, int lane) {
;     ...
; #pragma unroll
;     for (int i = 0; i < 32; ++i) { const int kk = 2 * i + (lane >> 5); scr[kk * 33 + (lane & 31)] = v[i]; }
;     asm volatile("s_waitcnt lgkmcnt(0)" ::: "memory");
;     const int c = lane & 7;
; #pragma unroll
;     for (int j = 0; j < 4; ++j) { const int n = it.n0 + (lane >> 3) + 8 * j; const LAS float* s = scr + (8 * c) * 33 + (lane >> 3) + 8 * j;
;         const int row = it.rowmode == 0 ? n : ((n >> 7) * 256 + (it.rowmode == 2 ? 128 : 0) + (n & 127));
;         if (it.fp8) { int w0 = CVT_PK_FP8_SAT(s[0 * 33] * FP8_WSCALE, s[1 * 33] * FP8_WSCALE, 0, false); w0 = CVT_PK_FP8_SAT(s[2 * 33] * FP8_WSCALE, s[3 * 33] * FP8_WSCALE, w0, true);
;             int w1 = CVT_PK_FP8_SAT(s[4 * 33] * FP8_WSCALE, s[5 * 33] * FP8_WSCALE, 0, false); w1 = CVT_PK_FP8_SAT(s[6 * 33] * FP8_WSCALE, s[7 * 33] * FP8_WSCALE, w1, true);
;             u32x2 o8; o8.x = (unsigned)w0; o8.y = (unsigned)w1; *(u32x2*)((unsigned char*)it.WT + (size_t)row * it.K + it.k0 + 8 * c) = o8; continue; }
;         u32x4 o; o.x = cvt_pk_bf16(s[0 * 33], s[1 * 33]); o.y = cvt_pk_bf16(s[2 * 33], s[3 * 33]); o.z = cvt_pk_bf16(s[4 * 33], s[5 * 33]); o.w = cvt_pk_bf16(s[6 * 33], s[7 * 33]);
;         *(u32x4*)(it.WT + (size_t)row * it.K + it.k0 + 8 * c) = o; }
;     asm volatile("s_waitcnt lgkmcnt(0)" ::: "memory");
; }
.LBB0_1527:
	s_waitcnt vmcnt(30)
	ds_write2_b32 v76, v32, v33 offset1:66
	s_waitcnt vmcnt(28) lgkmcnt(1)
	ds_write2_b32 v76, v34, v35 offset0:132 offset1:198
	v_add_u32_e32 v32, 0x400, v76
	s_waitcnt vmcnt(26)
	ds_write2_b32 v32, v36, v37 offset0:8 offset1:74
	s_waitcnt vmcnt(24)
	ds_write2_b32 v32, v38, v39 offset0:140 offset1:206
	v_add_u32_e32 v32, 0x800, v76
	s_waitcnt vmcnt(22)
	ds_write2_b32 v32, v40, v41 offset0:16 offset1:82
	s_waitcnt vmcnt(20)
	ds_write2_b32 v32, v42, v43 offset0:148 offset1:214
	v_add_u32_e32 v32, 0xc00, v76
	s_waitcnt vmcnt(18)
	ds_write2_b32 v32, v44, v45 offset0:24 offset1:90
	s_waitcnt vmcnt(16)
	ds_write2_b32 v32, v46, v47 offset0:156 offset1:222
	v_add_u32_e32 v32, 0x1000, v76
	s_waitcnt vmcnt(14)
	ds_write2_b32 v32, v48, v49 offset0:32 offset1:98
	s_waitcnt vmcnt(12)
	ds_write2_b32 v32, v50, v51 offset0:164 offset1:230
	v_add_u32_e32 v32, 0x1400, v76
	s_waitcnt vmcnt(10)
	ds_write2_b32 v32, v52, v53 offset0:40 offset1:106
	s_waitcnt vmcnt(8)
	ds_write2_b32 v32, v54, v55 offset0:172 offset1:238
	v_add_u32_e32 v32, 0x1800, v76
	s_waitcnt vmcnt(6)
	ds_write2_b32 v32, v56, v57 offset0:48 offset1:114
	s_waitcnt vmcnt(4)
	ds_write2_b32 v32, v58, v59 offset0:180 offset1:246
	v_add_u32_e32 v32, 0x1c00, v76
	s_waitcnt vmcnt(2)
	ds_write2_b32 v32, v60, v61 offset0:56 offset1:122
	s_waitcnt vmcnt(0)
	ds_write2_b32 v32, v62, v63 offset0:188 offset1:254
	v_add_u32_e32 v32, s41, v71
	s_cmp_eq_u32 s42, 0
	s_cselect_b64 s[8:9], -1, 0
	v_lshlrev_b32_e32 v33, 1, v32
	s_cmp_eq_u32 s42, 2
	s_waitcnt lgkmcnt(0)
	v_and_b32_e32 v33, 0x7fffff00, v33
	s_cselect_b32 s26, 0x80, 0
	v_and_b32_e32 v34, 0x7f, v32
	v_or3_b32 v33, v33, v34, s26
	ds_read_b32 v34, v72
	s_cmp_lg_u32 s1, 0
	s_cselect_b64 s[24:25], -1, 0
	s_cmp_eq_u32 s1, 0
	v_cndmask_b32_e64 v33, v33, v32, s[8:9]
	s_cbranch_scc1 .LBB0_1541
	ds_read2_b32 v[36:37], v72 offset0:33 offset1:66
	ds_read2_b32 v[38:39], v72 offset0:99 offset1:132
	s_waitcnt lgkmcnt(2)
	v_mul_f32_e32 v32, 0x42800000, v34
	v_med3_f32 v32, v32, s97, v219
	s_mov_b32 s1, s51
	s_waitcnt lgkmcnt(1)
	v_mul_f32_e32 v35, 0x42800000, v36
	v_med3_f32 v35, v35, s97, v219
	v_cvt_pk_fp8_f32 v36, v32, v35
	v_mul_f32_e32 v32, 0x42800000, v37
	s_waitcnt lgkmcnt(0)
	v_mul_f32_e32 v35, 0x42800000, v38
	v_med3_f32 v32, v32, s97, v219
	v_med3_f32 v35, v35, s97, v219
	v_cvt_pk_fp8_f32 v36, v32, v35 op_sel:[0,0,1]
	v_mul_f32_e32 v32, 0x42800000, v39
	ds_read2_b32 v[38:39], v72 offset0:165 offset1:198
	v_med3_f32 v32, v32, s97, v219
	s_waitcnt lgkmcnt(0)
	v_mul_f32_e32 v35, 0x42800000, v38
	v_med3_f32 v35, v35, s97, v219
	v_cvt_pk_fp8_f32 v37, v32, v35
	ds_read_b32 v35, v72 offset:924
	v_mul_f32_e32 v32, 0x42800000, v39
	v_med3_f32 v32, v32, s97, v219
	v_mov_b64_e32 v[38:39], s[16:17]
	v_mad_u64_u32 v[38:39], s[10:11], v33, s31, v[38:39]
	s_waitcnt lgkmcnt(0)
	v_mul_f32_e32 v35, 0x42800000, v35
	v_med3_f32 v35, v35, s97, v219
	v_cvt_pk_fp8_f32 v37, v32, v35 op_sel:[0,0,1]
	v_lshl_add_u64 v[38:39], v[38:39], 0, s[0:1]
	v_lshl_add_u64 v[38:39], v[38:39], 0, v[66:67]
	global_store_dwordx2 v[38:39], v[36:37], off
	v_lshlrev_b32_e32 v32, 1, v66
	s_cbranch_execnz .LBB0_1530

; #define LAS __attribute__((address_space(3)))
; #define CVT_PK_FP8_SAT(a, b, old, hi) __builtin_amdgcn_cvt_pk_fp8_f32(__builtin_amdgcn_fmed3f((a), -448.0f, 448.0f), __builtin_amdgcn_fmed3f((b), -448.0f, 448.0f), (old), (hi))
; __device__ __forceinline__ unsigned cvt_pk_bf16(float lo, float hi) { unsigned r; asm volatile("v_cvt_pk_bf16_f32 %0, %1, %2" : "=v"(r) : "v"(lo), "v"(hi)); return r; }
; __device__ __forceinline__ void cvt_finish(const CvtItem& it, float (&v)[32], LAS float* scr, int lane) {
;     ...
;     for (int j = 0; j < 4; ++j) { const int n = it.n0 + (lane >> 3) + 8 * j; const LAS float* s = scr + (8 * c) * 33 + (lane >> 3) + 8 * j;
;         const int row = it.rowmode == 0 ? n : ((n >> 7) * 256 + (it.rowmode == 2 ? 128 : 0) + (n & 127));
;         if (it.fp8) { int w0 = CVT_PK_FP8_SAT(s[0 * 33] * FP8_WSCALE, s[1 * 33] * FP8_WSCALE, 0, false); w0 = CVT_PK_FP8_SAT(s[2 * 33] * FP8_WSCALE, s[3 * 33] * FP8_WSCALE, w0, true);
;             int w1 = CVT_PK_FP8_SAT(s[4 * 33] * FP8_WSCALE, s[5 * 33] * FP8_WSCALE, 0, false); w1 = CVT_PK_FP8_SAT(s[6 * 33] * FP8_WSCALE, s[7 * 33] * FP8_WSCALE, w1, true);
;             u32x2 o8; o8.x = (unsigned)w0; o8.y = (unsigned)w1; *(u32x2*)((unsigned char*)it.WT + (size_t)row * it.K + it.k0 + 8 * c) = o8; continue; }
;         u32x4 o; o.x = cvt_pk_bf16(s[0 * 33], s[1 * 33]); o.y = cvt_pk_bf16(s[2 * 33], s[3 * 33]); o.z = cvt_pk_bf16(s[4 * 33], s[5 * 33]); o.w = cvt_pk_bf16(s[6 * 33], s[7 * 33]);
;         *(u32x4*)(it.WT + (size_t)row * it.K + it.k0 + 8 * c) = o; }
.LBB0_1530:
	v_add_u32_e32 v33, s41, v73
	s_waitcnt lgkmcnt(0)
	v_lshlrev_b32_e32 v34, 1, v33
	v_and_b32_e32 v34, 0x7fffff00, v34
	v_and_b32_e32 v35, 0x7f, v33
	v_or3_b32 v35, v34, v35, s26
	ds_read_b32 v34, v72 offset:32
	v_cndmask_b32_e64 v36, 0, 1, s[24:25]
	v_cmp_ne_u32_e64 s[10:11], 1, v36
	s_andn2_b64 vcc, exec, s[24:25]
	v_cndmask_b32_e64 v33, v35, v33, s[8:9]
	s_cbranch_vccnz .LBB0_1542
	ds_read2_b32 v[36:37], v72 offset0:41 offset1:74
	s_waitcnt lgkmcnt(1)
	v_mul_f32_e32 v35, 0x42800000, v34
	v_med3_f32 v35, v35, s97, v219
	s_mov_b32 s1, s51
	s_waitcnt lgkmcnt(0)
	v_mul_f32_e32 v36, 0x42800000, v36
	v_med3_f32 v38, v36, s97, v219
	v_cvt_pk_fp8_f32 v36, v35, v38
	ds_read2_b32 v[38:39], v72 offset0:107 offset1:140
	v_mul_f32_e32 v35, 0x42800000, v37
	v_med3_f32 v35, v35, s97, v219
	s_waitcnt lgkmcnt(0)
	v_mul_f32_e32 v37, 0x42800000, v38
	v_med3_f32 v37, v37, s97, v219
	v_cvt_pk_fp8_f32 v36, v35, v37 op_sel:[0,0,1]
	v_mul_f32_e32 v35, 0x42800000, v39
	ds_read2_b32 v[38:39], v72 offset0:173 offset1:206
	v_med3_f32 v35, v35, s97, v219
	s_waitcnt lgkmcnt(0)
	v_mul_f32_e32 v37, 0x42800000, v38
	v_med3_f32 v38, v37, s97, v219
	v_cvt_pk_fp8_f32 v37, v35, v38
	ds_read_b32 v38, v72 offset:956
	v_mul_f32_e32 v35, 0x42800000, v39
	v_med3_f32 v35, v35, s97, v219
	s_waitcnt lgkmcnt(0)
	v_mul_f32_e32 v38, 0x42800000, v38
	v_med3_f32 v38, v38, s97, v219
	v_cvt_pk_fp8_f32 v37, v35, v38 op_sel:[0,0,1]
	v_mov_b64_e32 v[38:39], s[16:17]
	v_mad_u64_u32 v[38:39], s[24:25], v33, s31, v[38:39]
	v_lshl_add_u64 v[38:39], v[38:39], 0, s[0:1]
	v_lshl_add_u64 v[38:39], v[38:39], 0, v[66:67]
	global_store_dwordx2 v[38:39], v[36:37], off
	s_cbranch_execnz .LBB0_1533

; #define LAS __attribute__((address_space(3)))
; #define CVT_PK_FP8_SAT(a, b, old, hi) __builtin_amdgcn_cvt_pk_fp8_f32(__builtin_amdgcn_fmed3f((a), -448.0f, 448.0f), __builtin_amdgcn_fmed3f((b), -448.0f, 448.0f), (old), (hi))
; __device__ __forceinline__ unsigned cvt_pk_bf16(float lo, float hi) { unsigned r; asm volatile("v_cvt_pk_bf16_f32 %0, %1, %2" : "=v"(r) : "v"(lo), "v"(hi)); return r; }
; __device__ __forceinline__ void cvt_finish(const CvtItem& it, float (&v)[32], LAS float* scr, int lane) {
;     ...
;     for (int j = 0; j < 4; ++j) { const int n = it.n0 + (lane >> 3) + 8 * j; const LAS float* s = scr + (8 * c) * 33 + (lane >> 3) + 8 * j;
;         const int row = it.rowmode == 0 ? n : ((n >> 7) * 256 + (it.rowmode == 2 ? 128 : 0) + (n & 127));
;         if (it.fp8) { int w0 = CVT_PK_FP8_SAT(s[0 * 33] * FP8_WSCALE, s[1 * 33] * FP8_WSCALE, 0, false); w0 = CVT_PK_FP8_SAT(s[2 * 33] * FP8_WSCALE, s[3 * 33] * FP8_WSCALE, w0, true);
;             int w1 = CVT_PK_FP8_SAT(s[4 * 33] * FP8_WSCALE, s[5 * 33] * FP8_WSCALE, 0, false); w1 = CVT_PK_FP8_SAT(s[6 * 33] * FP8_WSCALE, s[7 * 33] * FP8_WSCALE, w1, true);
;             u32x2 o8; o8.x = (unsigned)w0; o8.y = (unsigned)w1; *(u32x2*)((unsigned char*)it.WT + (size_t)row * it.K + it.k0 + 8 * c) = o8; continue; }
;         u32x4 o; o.x = cvt_pk_bf16(s[0 * 33], s[1 * 33]); o.y = cvt_pk_bf16(s[2 * 33], s[3 * 33]); o.z = cvt_pk_bf16(s[4 * 33], s[5 * 33]); o.w = cvt_pk_bf16(s[6 * 33], s[7 * 33]);
;         *(u32x4*)(it.WT + (size_t)row * it.K + it.k0 + 8 * c) = o; }
.LBB0_1533:
	v_add_u32_e32 v33, s41, v74
	s_waitcnt lgkmcnt(0)
	v_lshlrev_b32_e32 v34, 1, v33
	v_and_b32_e32 v34, 0x7fffff00, v34
	v_and_b32_e32 v35, 0x7f, v33
	v_or3_b32 v34, v34, v35, s26
	v_cndmask_b32_e64 v33, v34, v33, s[8:9]
	ds_read_b32 v34, v72 offset:64
	s_and_b64 vcc, exec, s[10:11]
	s_cbranch_vccnz .LBB0_1543
	ds_read2_b32 v[36:37], v72 offset0:49 offset1:82
	s_waitcnt lgkmcnt(1)
	v_mul_f32_e32 v35, 0x42800000, v34
	v_med3_f32 v35, v35, s97, v219
	s_mov_b32 s1, s51
	s_waitcnt lgkmcnt(0)
	v_mul_f32_e32 v36, 0x42800000, v36
	v_med3_f32 v38, v36, s97, v219
	v_cvt_pk_fp8_f32 v36, v35, v38
	ds_read2_b32 v[38:39], v72 offset0:115 offset1:148
	v_mul_f32_e32 v35, 0x42800000, v37
	v_med3_f32 v35, v35, s97, v219
	s_waitcnt lgkmcnt(0)
	v_mul_f32_e32 v37, 0x42800000, v38
	v_med3_f32 v37, v37, s97, v219
	v_cvt_pk_fp8_f32 v36, v35, v37 op_sel:[0,0,1]
	v_mul_f32_e32 v35, 0x42800000, v39
	ds_read2_b32 v[38:39], v72 offset0:181 offset1:214
	v_med3_f32 v35, v35, s97, v219
	s_waitcnt lgkmcnt(0)
	v_mul_f32_e32 v37, 0x42800000, v38
	v_med3_f32 v38, v37, s97, v219
	v_cvt_pk_fp8_f32 v37, v35, v38
	ds_read_b32 v38, v72 offset:988
	v_mul_f32_e32 v35, 0x42800000, v39
	v_med3_f32 v35, v35, s97, v219
	s_waitcnt lgkmcnt(0)
	v_mul_f32_e32 v38, 0x42800000, v38
	v_med3_f32 v38, v38, s97, v219
	v_cvt_pk_fp8_f32 v37, v35, v38 op_sel:[0,0,1]
	v_mov_b64_e32 v[38:39], s[16:17]
	v_mad_u64_u32 v[38:39], s[24:25], v33, s31, v[38:39]
	v_lshl_add_u64 v[38:39], v[38:39], 0, s[0:1]
	v_lshl_add_u64 v[38:39], v[38:39], 0, v[66:67]
	global_store_dwordx2 v[38:39], v[36:37], off
	s_cbranch_execnz .LBB0_1536

; #define LAS __attribute__((address_space(3)))
; #define CVT_PK_FP8_SAT(a, b, old, hi) __builtin_amdgcn_cvt_pk_fp8_f32(__builtin_amdgcn_fmed3f((a), -448.0f, 448.0f), __builtin_amdgcn_fmed3f((b), -448.0f, 448.0f), (old), (hi))
; __device__ __forceinline__ unsigned cvt_pk_bf16(float lo, float hi) { unsigned r; asm volatile("v_cvt_pk_bf16_f32 %0, %1, %2" : "=v"(r) : "v"(lo), "v"(hi)); return r; }
; __device__ __forceinline__ void cvt_finish(const CvtItem& it, float (&v)[32], LAS float* scr, int lane) {
;     ...
;     for (int j = 0; j < 4; ++j) { const int n = it.n0 + (lane >> 3) + 8 * j; const LAS float* s = scr + (8 * c) * 33 + (lane >> 3) + 8 * j;
;         const int row = it.rowmode == 0 ? n : ((n >> 7) * 256 + (it.rowmode == 2 ? 128 : 0) + (n & 127));
;         if (it.fp8) { int w0 = CVT_PK_FP8_SAT(s[0 * 33] * FP8_WSCALE, s[1 * 33] * FP8_WSCALE, 0, false); w0 = CVT_PK_FP8_SAT(s[2 * 33] * FP8_WSCALE, s[3 * 33] * FP8_WSCALE, w0, true);
;             int w1 = CVT_PK_FP8_SAT(s[4 * 33] * FP8_WSCALE, s[5 * 33] * FP8_WSCALE, 0, false); w1 = CVT_PK_FP8_SAT(s[6 * 33] * FP8_WSCALE, s[7 * 33] * FP8_WSCALE, w1, true);
;             u32x2 o8; o8.x = (unsigned)w0; o8.y = (unsigned)w1; *(u32x2*)((unsigned char*)it.WT + (size_t)row * it.K + it.k0 + 8 * c) = o8; continue; }
;         u32x4 o; o.x = cvt_pk_bf16(s[0 * 33], s[1 * 33]); o.y = cvt_pk_bf16(s[2 * 33], s[3 * 33]); o.z = cvt_pk_bf16(s[4 * 33], s[5 * 33]); o.w = cvt_pk_bf16(s[6 * 33], s[7 * 33]);
;         *(u32x4*)(it.WT + (size_t)row * it.K + it.k0 + 8 * c) = o; }
.LBB0_1536:
	v_add_u32_e32 v33, s41, v75
	s_waitcnt lgkmcnt(0)
	v_lshlrev_b32_e32 v34, 1, v33
	v_and_b32_e32 v34, 0x7fffff00, v34
	v_and_b32_e32 v35, 0x7f, v33
	v_or3_b32 v34, v34, v35, s26
	v_cndmask_b32_e64 v33, v34, v33, s[8:9]
	ds_read_b32 v34, v72 offset:96
	s_and_b64 vcc, exec, s[10:11]
	s_cbranch_vccnz .LBB0_1544
	ds_read2_b32 v[36:37], v72 offset0:57 offset1:90
	s_waitcnt lgkmcnt(1)
	v_mul_f32_e32 v35, 0x42800000, v34
	v_med3_f32 v35, v35, s97, v219
	s_mov_b32 s1, s51
	s_waitcnt lgkmcnt(0)
	v_mul_f32_e32 v36, 0x42800000, v36
	v_med3_f32 v38, v36, s97, v219
	v_cvt_pk_fp8_f32 v36, v35, v38
	ds_read2_b32 v[38:39], v72 offset0:123 offset1:156
	v_mul_f32_e32 v35, 0x42800000, v37
	v_med3_f32 v35, v35, s97, v219
	s_waitcnt lgkmcnt(0)
	v_mul_f32_e32 v37, 0x42800000, v38
	v_med3_f32 v37, v37, s97, v219
	v_cvt_pk_fp8_f32 v36, v35, v37 op_sel:[0,0,1]
	v_mul_f32_e32 v35, 0x42800000, v39
	ds_read2_b32 v[38:39], v72 offset0:189 offset1:222
	v_med3_f32 v35, v35, s97, v219
	s_waitcnt lgkmcnt(0)
	v_mul_f32_e32 v37, 0x42800000, v38
	v_med3_f32 v38, v37, s97, v219
	v_cvt_pk_fp8_f32 v37, v35, v38
	ds_read_b32 v38, v72 offset:1020
	v_mul_f32_e32 v35, 0x42800000, v39
	v_med3_f32 v35, v35, s97, v219
	s_waitcnt lgkmcnt(0)
	v_mul_f32_e32 v38, 0x42800000, v38
	v_med3_f32 v38, v38, s97, v219
	v_cvt_pk_fp8_f32 v37, v35, v38 op_sel:[0,0,1]
	v_mov_b64_e32 v[38:39], s[16:17]
	v_mad_u64_u32 v[38:39], s[8:9], v33, s31, v[38:39]
	v_lshl_add_u64 v[38:39], v[38:39], 0, s[0:1]
	v_lshl_add_u64 v[38:39], v[38:39], 0, v[66:67]
	global_store_dwordx2 v[38:39], v[36:37], off
	s_cbranch_execnz .LBB0_1539

; #define CVT_PK_FP8_SAT(a, b, old, hi) __builtin_amdgcn_cvt_pk_fp8_f32(__builtin_amdgcn_fmed3f((a), -448.0f, 448.0f), __builtin_amdgcn_fmed3f((b), -448.0f, 448.0f), (old), (hi))
;     __device__ __forceinline__ void operator()(const f32x4 (&acc)[2][2][4][2], const Unit& u, int wr, int wc, int fr, int fq) const {
;         const int col0 = u.pn * BM + wc * 32 + 8 * fq;
;         int slots[4];
; #pragma unroll
;         for (int j = 0; j < 4; ++j) { const int r = (j >> 1) * HALF + wr * 64 + (2 * (j & 1) + (fq & 1)) * 16 + fr; slots[j] = list[u.e * LCAP + u.pm * BM + (r < u.rows ? r : u.rows - 1)]; }
; #pragma unroll
;         for (int ai = 0; ai < 2; ++ai) {
;             u32x2 p8[4][2];
; #pragma unroll
;             for (int m = 0; m < 4; ++m)
; #pragma unroll
;                 for (int bj = 0; bj < 2; ++bj) {
;                     const f32x4 v0 = acc[ai][bj][m][0] * YS8_SCALE, v1 = acc[ai][bj][m][1] * YS8_SCALE;
;                     int a = CVT_PK_FP8_SAT(v0[0], v0[1], 0, false); a = CVT_PK_FP8_SAT(v0[2], v0[3], a, true);
;                     int b = CVT_PK_FP8_SAT(v1[0], v1[1], 0, false); b = CVT_PK_FP8_SAT(v1[2], v1[3], b, true);
;                     p8[m][bj].x = (unsigned)a; p8[m][bj].y = (unsigned)b;
;                 }
; #pragma unroll
;             for (int mp = 0; mp < 2; ++mp) {
;                 const int r = ai * HALF + wr * 64 + (2 * mp + (fq & 1)) * 16 + fr; const bool valid = r < u.rows; const int slot = slots[ai * 2 + mp];
; #pragma unroll
;                 for (int bj = 0; bj < 2; ++bj) {
;                     auto r0 = __builtin_amdgcn_permlane16_swap(p8[2 * mp][bj].x, p8[2 * mp + 1][bj].x, false, false);
;                     auto r1 = __builtin_amdgcn_permlane16_swap(p8[2 * mp][bj].y, p8[2 * mp + 1][bj].y, false, false);
;                     u32x4 w8 = {r0[0], r1[0], r0[1], r1[1]};
;                     if (valid) *(u32x4*)(ys + (size_t)slot * D + col0 - (fq & 1) * 8 + bj * HALF) = w8; }
.LBB0_1678:
	v_mbcnt_lo_u32_b32 v64, -1, 0
	v_mbcnt_hi_u32_b32 v64, -1, v64
	s_lshl_b32 s1, s20, 14
	v_add_u32_e32 v64, s93, v64
	s_lshl_b32 s6, s63, 8
	v_and_b32_e32 v132, 15, v64
	v_bfe_u32 v152, v64, 4, 1
	v_lshlrev_b32_e32 v133, 4, v152
	v_or_b32_e32 v135, s55, v132
	s_add_i32 s1, s1, s6
	s_add_i32 s6, s38, -1
	v_or_b32_e32 v153, v133, v135
	v_bfe_u32 v139, v64, 4, 2
	v_min_i32_e32 v64, s6, v153
	v_add_u32_e32 v136, s1, v64
	v_ashrrev_i32_e32 v137, 31, v136
	v_lshl_add_u64 v[136:137], v[136:137], 2, s[12:13]
	v_lshl_or_b32 v64, v139, 4, 32
	global_load_dword v138, v[136:137], off
	v_or_b32_e32 v137, v64, v135
	v_min_i32_e32 v134, s6, v137
	v_or_b32_e32 v132, s60, v132
	v_add_u32_e32 v146, s1, v134
	v_or_b32_e32 v134, v133, v132
	v_or_b32_e32 v132, v64, v132
	v_min_i32_e32 v134, s6, v134
	v_min_i32_e32 v132, s6, v132
	v_ashrrev_i32_e32 v147, 31, v146
	v_add_u32_e32 v148, s1, v134
	v_add_u32_e32 v150, s1, v132
	v_lshl_add_u64 v[146:147], v[146:147], 2, s[12:13]
	v_ashrrev_i32_e32 v149, 31, v148
	v_ashrrev_i32_e32 v151, 31, v150
	v_lshl_add_u64 v[148:149], v[148:149], 2, s[12:13]
	v_lshl_add_u64 v[150:151], v[150:151], 2, s[12:13]
	global_load_dword v136, v[146:147], off
	global_load_dword v134, v[148:149], off
	global_load_dword v132, v[150:151], off
	v_pk_add_f32 v[126:127], v[126:127], v[126:127]
	v_pk_add_f32 v[148:149], v[122:123], v[122:123]
	v_pk_add_f32 v[118:119], v[118:119], v[118:119]
	v_pk_add_f32 v[114:115], v[114:115], v[114:115]
	v_pk_add_f32 v[146:147], v[124:125], v[124:125]
	v_med3_f32 v126, v126, s97, v219
	v_med3_f32 v127, v127, s97, v219
	v_med3_f32 v148, v148, s97, v219
	v_med3_f32 v149, v149, s97, v219
	v_med3_f32 v118, v118, s97, v219
	v_med3_f32 v119, v119, s97, v219
	v_med3_f32 v114, v114, s97, v219
	v_med3_f32 v115, v115, s97, v219
	v_cvt_pk_fp8_f32 v122, v126, v127
	v_cvt_pk_fp8_f32 v123, v148, v149
	v_cvt_pk_fp8_f32 v124, v118, v119
	v_cvt_pk_fp8_f32 v125, v114, v115
	v_pk_add_f32 v[128:129], v[128:129], v[128:129]
	v_pk_add_f32 v[120:121], v[120:121], v[120:121]
	v_pk_add_f32 v[116:117], v[116:117], v[116:117]
	v_med3_f32 v128, v128, s97, v219
	v_med3_f32 v129, v129, s97, v219
	v_med3_f32 v146, v146, s97, v219
	v_med3_f32 v147, v147, s97, v219
	v_med3_f32 v120, v120, s97, v219
	v_med3_f32 v121, v121, s97, v219
	v_med3_f32 v150, v116, s97, v219
	v_med3_f32 v151, v117, s97, v219
	s_lshl_b32 s0, s0, 8
	v_cvt_pk_fp8_f32 v122, v128, v129 op_sel:[0,0,1]
	v_cvt_pk_fp8_f32 v123, v146, v147 op_sel:[0,0,1]
	v_cvt_pk_fp8_f32 v124, v120, v121 op_sel:[0,0,1]
	v_cvt_pk_fp8_f32 v125, v150, v151 op_sel:[0,0,1]
	v_lshl_or_b32 v114, v139, 3, s0
	v_lshlrev_b32_e32 v115, 3, v152
	v_or_b32_e32 v116, s56, v114
	v_sub_co_u32_e32 v114, vcc, 0, v115
	v_ashrrev_i32_e32 v117, 31, v116
	s_nop 0
	v_subb_co_u32_e64 v115, s[0:1], 0, 0, vcc
	v_cmp_gt_i32_e32 vcc, s38, v153
	v_permlane16_swap_b32_e32 v122, v124
	v_permlane16_swap_b32_e32 v123, v125
	s_waitcnt vmcnt(0)
	v_ashrrev_i32_e32 v139, 31, v138
	v_lshlrev_b64 v[118:119], 10, v[138:139]
	v_lshl_add_u64 v[118:119], s[14:15], 0, v[118:119]
	v_lshl_add_u64 v[118:119], v[118:119], 0, v[116:117]
	s_and_saveexec_b64 s[0:1], vcc
	s_mov_b64 s[68:69], 0x40000
	s_cbranch_execz .LBB0_1680
	v_lshl_add_u64 v[120:121], v[118:119], 0, v[114:115]
	global_store_dwordx4 v[120:121], v[122:125], off
.LBB0_1680:
	s_or_b64 exec, exec, s[0:1]
	v_pk_add_f32 v[110:111], v[110:111], v[110:111]
	v_pk_add_f32 v[112:113], v[112:113], v[112:113]
	v_pk_add_f32 v[120:121], v[106:107], v[106:107]
	v_med3_f32 v107, v110, s97, v219
	v_med3_f32 v110, v111, s97, v219
	v_cvt_pk_fp8_f32 v106, v107, v110
	v_med3_f32 v110, v112, s97, v219
	v_med3_f32 v111, v113, s97, v219
	v_med3_f32 v112, v120, s97, v219
	v_med3_f32 v113, v121, s97, v219
	v_cvt_pk_fp8_f32 v107, v112, v113
	v_pk_add_f32 v[108:109], v[108:109], v[108:109]
	v_pk_add_f32 v[102:103], v[102:103], v[102:103]
	v_med3_f32 v108, v108, s97, v219
	v_med3_f32 v109, v109, s97, v219
	v_pk_add_f32 v[98:99], v[98:99], v[98:99]
	v_cvt_pk_fp8_f32 v107, v108, v109 op_sel:[0,0,1]
	v_med3_f32 v102, v102, s97, v219
	v_med3_f32 v103, v103, s97, v219
	v_med3_f32 v98, v98, s97, v219
	v_med3_f32 v99, v99, s97, v219
	v_cvt_pk_fp8_f32 v108, v102, v103
	v_cvt_pk_fp8_f32 v109, v98, v99
	v_pk_add_f32 v[104:105], v[104:105], v[104:105]
	v_pk_add_f32 v[100:101], v[100:101], v[100:101]
	v_med3_f32 v102, v104, s97, v219
	v_med3_f32 v103, v105, s97, v219
	v_med3_f32 v98, v100, s97, v219
	v_med3_f32 v99, v101, s97, v219
	v_cvt_pk_fp8_f32 v106, v110, v111 op_sel:[0,0,1]
	v_cvt_pk_fp8_f32 v108, v102, v103 op_sel:[0,0,1]
	v_cvt_pk_fp8_f32 v109, v98, v99 op_sel:[0,0,1]
	s_nop 0
	v_permlane16_swap_b32_e32 v106, v108
	v_permlane16_swap_b32_e32 v107, v109
	s_and_saveexec_b64 s[0:1], vcc
	s_cbranch_execz .LBB0_1682
	v_lshl_add_u64 v[98:99], v[118:119], 0, v[114:115]
	global_store_dwordx4 v[98:99], v[106:109], off offset:128
; #define CVT_PK_FP8_SAT(a, b, old, hi) __builtin_amdgcn_cvt_pk_fp8_f32(__builtin_amdgcn_fmed3f((a), -448.0f, 448.0f), __builtin_amdgcn_fmed3f((b), -448.0f, 448.0f), (old), (hi))
;     __device__ __forceinline__ void operator()(const f32x4 (&acc)[2][2][4][2], const Unit& u, int wr, int wc, int fr, int fq) const {
;     ...
;         for (int ai = 0; ai < 2; ++ai) {
;             u32x2 p8[4][2];
; #pragma unroll
;             for (int m = 0; m < 4; ++m)
; #pragma unroll
;                 for (int bj = 0; bj < 2; ++bj) {
;                     const f32x4 v0 = acc[ai][bj][m][0] * YS8_SCALE, v1 = acc[ai][bj][m][1] * YS8_SCALE;
;                     int a = CVT_PK_FP8_SAT(v0[0], v0[1], 0, false); a = CVT_PK_FP8_SAT(v0[2], v0[3], a, true);
;                     int b = CVT_PK_FP8_SAT(v1[0], v1[1], 0, false); b = CVT_PK_FP8_SAT(v1[2], v1[3], b, true);
;                     p8[m][bj].x = (unsigned)a; p8[m][bj].y = (unsigned)b;
;                 }
; #pragma unroll
;             for (int mp = 0; mp < 2; ++mp) {
;                 const int r = ai * HALF + wr * 64 + (2 * mp + (fq & 1)) * 16 + fr; const bool valid = r < u.rows; const int slot = slots[ai * 2 + mp];
; #pragma unroll
;                 for (int bj = 0; bj < 2; ++bj) {
;                     auto r0 = __builtin_amdgcn_permlane16_swap(p8[2 * mp][bj].x, p8[2 * mp + 1][bj].x, false, false);
;                     auto r1 = __builtin_amdgcn_permlane16_swap(p8[2 * mp][bj].y, p8[2 * mp + 1][bj].y, false, false);
;                     u32x4 w8 = {r0[0], r1[0], r0[1], r1[1]};
;                     if (valid) *(u32x4*)(ys + (size_t)slot * D + col0 - (fq & 1) * 8 + bj * HALF) = w8; }
.LBB0_1682:
	s_or_b64 exec, exec, s[0:1]
	v_pk_add_f32 v[94:95], v[94:95], v[94:95]
	v_pk_add_f32 v[96:97], v[96:97], v[96:97]
	v_pk_add_f32 v[98:99], v[90:91], v[90:91]
	v_med3_f32 v91, v94, s97, v219
	v_med3_f32 v94, v95, s97, v219
	v_cvt_pk_fp8_f32 v90, v91, v94
	v_med3_f32 v94, v96, s97, v219
	v_med3_f32 v95, v97, s97, v219
	v_med3_f32 v96, v98, s97, v219
	v_med3_f32 v97, v99, s97, v219
	v_cvt_pk_fp8_f32 v91, v96, v97
	v_pk_add_f32 v[92:93], v[92:93], v[92:93]
	v_pk_add_f32 v[86:87], v[86:87], v[86:87]
	v_med3_f32 v92, v92, s97, v219
	v_med3_f32 v93, v93, s97, v219
	v_pk_add_f32 v[82:83], v[82:83], v[82:83]
	v_cvt_pk_fp8_f32 v91, v92, v93 op_sel:[0,0,1]
	v_med3_f32 v86, v86, s97, v219
	v_med3_f32 v87, v87, s97, v219
	v_med3_f32 v82, v82, s97, v219
	v_med3_f32 v83, v83, s97, v219
	v_cvt_pk_fp8_f32 v92, v86, v87
	v_cvt_pk_fp8_f32 v93, v82, v83
	v_pk_add_f32 v[88:89], v[88:89], v[88:89]
	v_pk_add_f32 v[84:85], v[84:85], v[84:85]
	v_med3_f32 v86, v88, s97, v219
	v_med3_f32 v87, v89, s97, v219
	v_med3_f32 v82, v84, s97, v219
	v_med3_f32 v83, v85, s97, v219
	v_cvt_pk_fp8_f32 v90, v94, v95 op_sel:[0,0,1]
	v_cvt_pk_fp8_f32 v92, v86, v87 op_sel:[0,0,1]
	v_cvt_pk_fp8_f32 v93, v82, v83 op_sel:[0,0,1]
	v_cmp_gt_i32_e32 vcc, s38, v137
	v_ashrrev_i32_e32 v137, 31, v136
	v_lshlrev_b64 v[82:83], 10, v[136:137]
	v_lshl_add_u64 v[82:83], s[14:15], 0, v[82:83]
	v_permlane16_swap_b32_e32 v90, v92
	v_permlane16_swap_b32_e32 v91, v93
	v_lshl_add_u64 v[82:83], v[82:83], 0, v[116:117]
	s_and_saveexec_b64 s[0:1], vcc
	s_cbranch_execz .LBB0_1684
	v_lshl_add_u64 v[84:85], v[82:83], 0, v[114:115]
	global_store_dwordx4 v[84:85], v[90:93], off
.LBB0_1684:
	s_or_b64 exec, exec, s[0:1]
	v_pk_add_f32 v[78:79], v[78:79], v[78:79]
	v_pk_add_f32 v[80:81], v[80:81], v[80:81]
	v_pk_add_f32 v[84:85], v[74:75], v[74:75]
	v_med3_f32 v75, v78, s97, v219
	v_med3_f32 v78, v79, s97, v219
	v_cvt_pk_fp8_f32 v74, v75, v78
	v_med3_f32 v78, v80, s97, v219
	v_med3_f32 v79, v81, s97, v219
	v_med3_f32 v80, v84, s97, v219
	v_med3_f32 v81, v85, s97, v219
	v_cvt_pk_fp8_f32 v75, v80, v81
	v_pk_add_f32 v[76:77], v[76:77], v[76:77]
	v_pk_add_f32 v[70:71], v[70:71], v[70:71]
	v_med3_f32 v76, v76, s97, v219
	v_med3_f32 v77, v77, s97, v219
	v_pk_add_f32 v[66:67], v[66:67], v[66:67]
	v_cvt_pk_fp8_f32 v75, v76, v77 op_sel:[0,0,1]
	v_med3_f32 v70, v70, s97, v219
	v_med3_f32 v71, v71, s97, v219
	v_med3_f32 v66, v66, s97, v219
	v_med3_f32 v67, v67, s97, v219
	v_cvt_pk_fp8_f32 v76, v70, v71
	v_cvt_pk_fp8_f32 v77, v66, v67
	v_pk_add_f32 v[72:73], v[72:73], v[72:73]
	v_pk_add_f32 v[68:69], v[68:69], v[68:69]
	v_med3_f32 v70, v72, s97, v219
	v_med3_f32 v71, v73, s97, v219
	v_med3_f32 v66, v68, s97, v219
	v_med3_f32 v67, v69, s97, v219
	v_cvt_pk_fp8_f32 v74, v78, v79 op_sel:[0,0,1]
	v_cvt_pk_fp8_f32 v76, v70, v71 op_sel:[0,0,1]
	v_cvt_pk_fp8_f32 v77, v66, v67 op_sel:[0,0,1]
	s_nop 0
	v_permlane16_swap_b32_e32 v74, v76
	v_permlane16_swap_b32_e32 v75, v77
	s_and_saveexec_b64 s[0:1], vcc
	s_cbranch_execz .LBB0_1686
	v_lshl_add_u64 v[66:67], v[82:83], 0, v[114:115]
	global_store_dwordx4 v[66:67], v[74:77], off offset:128
.LBB0_1686:
	s_or_b64 exec, exec, s[0:1]
	v_pk_add_f32 v[60:61], v[60:61], v[60:61]
	v_pk_add_f32 v[62:63], v[62:63], v[62:63]
	v_pk_add_f32 v[66:67], v[56:57], v[56:57]
	v_med3_f32 v57, v60, s97, v219
	v_med3_f32 v60, v61, s97, v219
	v_cvt_pk_fp8_f32 v56, v57, v60
	v_med3_f32 v60, v62, s97, v219
	v_med3_f32 v61, v63, s97, v219
	v_med3_f32 v62, v66, s97, v219
	v_med3_f32 v63, v67, s97, v219
	v_cvt_pk_fp8_f32 v57, v62, v63
	v_pk_add_f32 v[58:59], v[58:59], v[58:59]
	v_pk_add_f32 v[52:53], v[52:53], v[52:53]
	v_med3_f32 v58, v58, s97, v219
	v_med3_f32 v59, v59, s97, v219
	v_pk_add_f32 v[48:49], v[48:49], v[48:49]
	v_cvt_pk_fp8_f32 v57, v58, v59 op_sel:[0,0,1]
	v_med3_f32 v52, v52, s97, v219
	v_med3_f32 v53, v53, s97, v219
	v_med3_f32 v48, v48, s97, v219
	v_med3_f32 v49, v49, s97, v219
	v_cvt_pk_fp8_f32 v58, v52, v53
	v_cvt_pk_fp8_f32 v59, v48, v49
	v_pk_add_f32 v[54:55], v[54:55], v[54:55]
	v_pk_add_f32 v[50:51], v[50:51], v[50:51]
	v_med3_f32 v52, v54, s97, v219
	v_med3_f32 v53, v55, s97, v219
	v_med3_f32 v48, v50, s97, v219
	v_med3_f32 v49, v51, s97, v219
	v_cvt_pk_fp8_f32 v56, v60, v61 op_sel:[0,0,1]
	v_cvt_pk_fp8_f32 v58, v52, v53 op_sel:[0,0,1]
	v_cvt_pk_fp8_f32 v59, v48, v49 op_sel:[0,0,1]
	v_add_u32_e32 v50, 0x80, v135
	v_or_b32_e32 v48, v133, v50
	v_ashrrev_i32_e32 v135, 31, v134
	v_cmp_gt_i32_e32 vcc, s38, v48
	v_lshlrev_b64 v[48:49], 10, v[134:135]
	v_lshl_add_u64 v[48:49], s[14:15], 0, v[48:49]
	v_permlane16_swap_b32_e32 v56, v58
	v_permlane16_swap_b32_e32 v57, v59
	v_lshl_add_u64 v[48:49], v[48:49], 0, v[116:117]
	s_and_saveexec_b64 s[0:1], vcc
	s_cbranch_execz .LBB0_1688
	v_lshl_add_u64 v[52:53], v[48:49], 0, v[114:115]
	global_store_dwordx4 v[52:53], v[56:59], off
; #define CVT_PK_FP8_SAT(a, b, old, hi) __builtin_amdgcn_cvt_pk_fp8_f32(__builtin_amdgcn_fmed3f((a), -448.0f, 448.0f), __builtin_amdgcn_fmed3f((b), -448.0f, 448.0f), (old), (hi))
;     __device__ __forceinline__ void operator()(const f32x4 (&acc)[2][2][4][2], const Unit& u, int wr, int wc, int fr, int fq) const {
;     ...
;         for (int ai = 0; ai < 2; ++ai) {
;             u32x2 p8[4][2];
; #pragma unroll
;             for (int m = 0; m < 4; ++m)
; #pragma unroll
;                 for (int bj = 0; bj < 2; ++bj) {
;                     const f32x4 v0 = acc[ai][bj][m][0] * YS8_SCALE, v1 = acc[ai][bj][m][1] * YS8_SCALE;
;                     int a = CVT_PK_FP8_SAT(v0[0], v0[1], 0, false); a = CVT_PK_FP8_SAT(v0[2], v0[3], a, true);
;                     int b = CVT_PK_FP8_SAT(v1[0], v1[1], 0, false); b = CVT_PK_FP8_SAT(v1[2], v1[3], b, true);
;                     p8[m][bj].x = (unsigned)a; p8[m][bj].y = (unsigned)b;
;                 }
; #pragma unroll
;             for (int mp = 0; mp < 2; ++mp) {
;                 const int r = ai * HALF + wr * 64 + (2 * mp + (fq & 1)) * 16 + fr; const bool valid = r < u.rows; const int slot = slots[ai * 2 + mp];
; #pragma unroll
;                 for (int bj = 0; bj < 2; ++bj) {
;                     auto r0 = __builtin_amdgcn_permlane16_swap(p8[2 * mp][bj].x, p8[2 * mp + 1][bj].x, false, false);
;                     auto r1 = __builtin_amdgcn_permlane16_swap(p8[2 * mp][bj].y, p8[2 * mp + 1][bj].y, false, false);
;                     u32x4 w8 = {r0[0], r1[0], r0[1], r1[1]};
;                     if (valid) *(u32x4*)(ys + (size_t)slot * D + col0 - (fq & 1) * 8 + bj * HALF) = w8; }
.LBB0_1688:
	s_or_b64 exec, exec, s[0:1]
	v_pk_add_f32 v[44:45], v[44:45], v[44:45]
	v_pk_add_f32 v[46:47], v[46:47], v[46:47]
	v_pk_add_f32 v[52:53], v[40:41], v[40:41]
	v_med3_f32 v41, v44, s97, v219
	v_med3_f32 v44, v45, s97, v219
	v_cvt_pk_fp8_f32 v40, v41, v44
	v_med3_f32 v44, v46, s97, v219
	v_med3_f32 v45, v47, s97, v219
	v_med3_f32 v46, v52, s97, v219
	v_med3_f32 v47, v53, s97, v219
	v_cvt_pk_fp8_f32 v41, v46, v47
	v_pk_add_f32 v[42:43], v[42:43], v[42:43]
	v_pk_add_f32 v[36:37], v[36:37], v[36:37]
	v_med3_f32 v42, v42, s97, v219
	v_med3_f32 v43, v43, s97, v219
	v_pk_add_f32 v[32:33], v[32:33], v[32:33]
	v_cvt_pk_fp8_f32 v41, v42, v43 op_sel:[0,0,1]
	v_med3_f32 v36, v36, s97, v219
	v_med3_f32 v37, v37, s97, v219
	v_med3_f32 v32, v32, s97, v219
	v_med3_f32 v33, v33, s97, v219
	v_cvt_pk_fp8_f32 v42, v36, v37
	v_cvt_pk_fp8_f32 v43, v32, v33
	v_pk_add_f32 v[38:39], v[38:39], v[38:39]
	v_pk_add_f32 v[34:35], v[34:35], v[34:35]
	v_med3_f32 v36, v38, s97, v219
	v_med3_f32 v37, v39, s97, v219
	v_med3_f32 v32, v34, s97, v219
	v_med3_f32 v33, v35, s97, v219
	v_cvt_pk_fp8_f32 v40, v44, v45 op_sel:[0,0,1]
	v_cvt_pk_fp8_f32 v42, v36, v37 op_sel:[0,0,1]
	v_cvt_pk_fp8_f32 v43, v32, v33 op_sel:[0,0,1]
	s_nop 0
	v_permlane16_swap_b32_e32 v40, v42
	v_permlane16_swap_b32_e32 v41, v43
	s_and_saveexec_b64 s[0:1], vcc
	s_cbranch_execz .LBB0_1690
	v_lshl_add_u64 v[32:33], v[48:49], 0, v[114:115]
	global_store_dwordx4 v[32:33], v[40:43], off offset:128
.LBB0_1690:
	s_or_b64 exec, exec, s[0:1]
	v_pk_add_f32 v[20:21], v[20:21], v[20:21]
	v_pk_add_f32 v[22:23], v[22:23], v[22:23]
	v_pk_add_f32 v[32:33], v[16:17], v[16:17]
	v_med3_f32 v17, v20, s97, v219
	v_med3_f32 v20, v21, s97, v219
	v_cvt_pk_fp8_f32 v16, v17, v20
	v_med3_f32 v20, v22, s97, v219
	v_med3_f32 v21, v23, s97, v219
	v_med3_f32 v22, v32, s97, v219
	v_med3_f32 v23, v33, s97, v219
	v_cvt_pk_fp8_f32 v17, v22, v23
	v_pk_add_f32 v[18:19], v[18:19], v[18:19]
	v_pk_add_f32 v[4:5], v[4:5], v[4:5]
	v_med3_f32 v18, v18, s97, v219
	v_med3_f32 v19, v19, s97, v219
	v_pk_add_f32 v[0:1], v[0:1], v[0:1]
	v_cvt_pk_fp8_f32 v17, v18, v19 op_sel:[0,0,1]
	v_med3_f32 v4, v4, s97, v219
	v_med3_f32 v5, v5, s97, v219
	v_med3_f32 v0, v0, s97, v219
	v_med3_f32 v1, v1, s97, v219
	v_cvt_pk_fp8_f32 v18, v4, v5
	v_cvt_pk_fp8_f32 v19, v0, v1
	v_pk_add_f32 v[6:7], v[6:7], v[6:7]
	v_pk_add_f32 v[2:3], v[2:3], v[2:3]
	v_med3_f32 v4, v6, s97, v219
	v_med3_f32 v5, v7, s97, v219
	v_med3_f32 v0, v2, s97, v219
	v_med3_f32 v1, v3, s97, v219
	v_cvt_pk_fp8_f32 v16, v20, v21 op_sel:[0,0,1]
	v_cvt_pk_fp8_f32 v18, v4, v5 op_sel:[0,0,1]
	v_cvt_pk_fp8_f32 v19, v0, v1 op_sel:[0,0,1]
	v_or_b32_e32 v0, v64, v50
	v_ashrrev_i32_e32 v133, 31, v132
	v_cmp_gt_i32_e32 vcc, s38, v0
	v_lshlrev_b64 v[0:1], 10, v[132:133]
	v_lshl_add_u64 v[0:1], s[14:15], 0, v[0:1]
	v_permlane16_swap_b32_e32 v16, v18
	v_permlane16_swap_b32_e32 v17, v19
	v_lshl_add_u64 v[4:5], v[0:1], 0, v[116:117]
	s_and_saveexec_b64 s[0:1], vcc
	s_cbranch_execz .LBB0_1692
	v_lshl_add_u64 v[0:1], v[4:5], 0, v[114:115]
	global_store_dwordx4 v[0:1], v[16:19], off
.LBB0_1692:
	s_or_b64 exec, exec, s[0:1]
	v_pk_add_f32 v[0:1], v[24:25], v[24:25]
	v_pk_add_f32 v[16:17], v[28:29], v[28:29]
	v_med3_f32 v18, v0, s97, v219
	v_med3_f32 v1, v1, s97, v219
	v_cvt_pk_fp8_f32 v0, v18, v1
	v_med3_f32 v16, v16, s97, v219
	v_med3_f32 v17, v17, s97, v219
	v_cvt_pk_fp8_f32 v1, v16, v17
	v_pk_add_f32 v[2:3], v[26:27], v[26:27]
	v_pk_add_f32 v[6:7], v[30:31], v[30:31]
	v_med3_f32 v2, v2, s97, v219
	v_med3_f32 v3, v3, s97, v219
	v_cvt_pk_fp8_f32 v0, v2, v3 op_sel:[0,0,1]
	v_med3_f32 v2, v6, s97, v219
	v_med3_f32 v3, v7, s97, v219
	v_cvt_pk_fp8_f32 v1, v2, v3 op_sel:[0,0,1]
	v_pk_add_f32 v[2:3], v[8:9], v[8:9]
	v_pk_add_f32 v[6:7], v[10:11], v[10:11]
	v_pk_add_f32 v[10:11], v[12:13], v[12:13]
	v_med3_f32 v12, v2, s97, v219
	v_med3_f32 v3, v3, s97, v219
	v_cvt_pk_fp8_f32 v2, v12, v3
	v_med3_f32 v10, v10, s97, v219
	v_med3_f32 v11, v11, s97, v219
	v_cvt_pk_fp8_f32 v3, v10, v11
	v_pk_add_f32 v[8:9], v[14:15], v[14:15]
	v_med3_f32 v6, v6, s97, v219
	v_med3_f32 v7, v7, s97, v219
	v_cvt_pk_fp8_f32 v2, v6, v7 op_sel:[0,0,1]
	v_med3_f32 v6, v8, s97, v219
	v_med3_f32 v7, v9, s97, v219
	v_cvt_pk_fp8_f32 v3, v6, v7 op_sel:[0,0,1]
	v_permlane16_swap_b32_e32 v0, v2
	s_nop 0
	v_permlane16_swap_b32_e32 v1, v3
	s_and_saveexec_b64 s[0:1], vcc
	s_cbranch_execz .LBB0_1694
	v_lshl_add_u64 v[4:5], v[4:5], 0, v[114:115]
	global_store_dwordx4 v[4:5], v[0:3], off offset:128

; template <int PH, bool PRB = false>
; __device__ __forceinline__ void run_phase(int layer, LAS unsigned char* lds, const int wv_) {
;     ...
;         for (int r0 = gw; r0 < S; r0 += 2 * NGW) {
;             u32x2 cc[2][4]; unsigned aa[2][4], bb[2][4];
; #pragma unroll
;             for (int q = 0; q < 2; ++q) { const int r = r0 + q * NGW < S ? r0 + q * NGW : r0;
;                 const u32x2* hr = (const u32x2*)(hb + (size_t)r * D); const unsigned* y0 = (const unsigned*)((const unsigned char*)ys + (size_t)(2 * r) * D); const unsigned* y1 = (const unsigned*)((const unsigned char*)ys + (size_t)(2 * r + 1) * D);
; #pragma unroll
;                 for (int j = 0; j < 4; ++j) { cc[q][j] = hr[lane + 64 * j]; aa[q][j] = y0[lane + 64 * j]; bb[q][j] = y1[lane + 64 * j]; } }
; #pragma unroll
;             for (int q = 0; q < 2; ++q) { const int r = r0 + q * NGW; if (r < S) {
;                 float4 v[4]; float ss = 0.f;
; #pragma unroll
;                 for (int j = 0; j < 4; ++j) {
;                     typedef float f2_ __attribute__((ext_vector_type(2)));
;                     const u32x2 c = cc[q][j]; const f2_ a0 = __builtin_amdgcn_cvt_pk_f32_fp8((int)aa[q][j], false), a1 = __builtin_amdgcn_cvt_pk_f32_fp8((int)aa[q][j], true), b0 = __builtin_amdgcn_cvt_pk_f32_fp8((int)bb[q][j], false), b1 = __builtin_amdgcn_cvt_pk_f32_fp8((int)bb[q][j], true);
;                     constexpr float iy = 1.0f / pg8::YS8_SCALE;
;                     v[j].x = __uint_as_float(c.x << 16) + (a0[0] + b0[0]) * iy; v[j].y = __uint_as_float(c.x & 0xffff0000u) + (a0[1] + b0[1]) * iy;
;                     v[j].z = __uint_as_float(c.y << 16) + (a1[0] + b1[0]) * iy; v[j].w = __uint_as_float(c.y & 0xffff0000u) + (a1[1] + b1[1]) * iy;
;                     ss += v[j].x * v[j].x + v[j].y * v[j].y + v[j].z * v[j].z + v[j].w * v[j].w;
;                 }
;                 ss = wave_sum(ss);
.LBB0_1762:
	s_add_i32 s3, s90, s2
	s_cmpk_lt_i32 s3, 0x4000
	s_cselect_b64 s[18:19], -1, 0
	v_lshl_add_u64 v[56:57], s[10:11], 0, v[20:21]
	s_and_b64 s[8:9], s[18:19], exec
	v_add_co_u32_e32 v32, vcc, s29, v56
	s_cselect_b32 s8, s3, s2
	s_ashr_i32 s13, s12, 31
	v_addc_co_u32_e32 v33, vcc, 0, v57, vcc
	s_lshl_b64 s[20:21], s[12:13], 10
	global_load_dwordx2 v[40:41], v[32:33], off
	global_load_dwordx2 v[42:43], v[32:33], off offset:1024
	global_load_dwordx2 v[50:51], v[32:33], off offset:1536
	global_load_dwordx2 v[44:45], v[32:33], off offset:512
	v_lshl_add_u64 v[32:33], v[18:19], 0, s[20:21]
	s_add_i32 s20, s12, 1
	s_ashr_i32 s21, s20, 31
	global_load_dword v92, v[32:33], off offset:768
	global_load_dword v52, v[32:33], off offset:256
	global_load_dword v72, v[32:33], off offset:512
	s_lshl_b64 s[20:21], s[20:21], 10
	global_load_dword v78, v[32:33], off
	v_lshl_add_u64 v[32:33], v[18:19], 0, s[20:21]
	global_load_dword v82, v[32:33], off
	global_load_dword v86, v[32:33], off offset:256
	global_load_dword v90, v[32:33], off offset:512
	global_load_dword v93, v[32:33], off offset:768
	s_lshl_b32 s20, s8, 1
	s_ashr_i32 s9, s8, 31
	s_ashr_i32 s21, s20, 31
	s_or_b32 s26, s20, 1
	s_lshl_b64 s[8:9], s[8:9], 11
	s_lshl_b64 s[20:21], s[20:21], 10
	s_ashr_i32 s27, s26, 31
	v_lshl_add_u64 v[32:33], v[16:17], 0, s[8:9]
	s_lshl_b64 s[8:9], s[26:27], 10
	v_lshl_add_u64 v[46:47], v[18:19], 0, s[20:21]
	global_load_dwordx2 v[38:39], v[32:33], off
	global_load_dwordx2 v[36:37], v[32:33], off offset:512
	global_load_dwordx2 v[34:35], v[32:33], off offset:1024
	s_nop 0
	global_load_dwordx2 v[32:33], v[32:33], off offset:1536
	v_lshl_add_u64 v[48:49], v[18:19], 0, s[8:9]
	global_load_dword v66, v[46:47], off
	global_load_dword v62, v[46:47], off offset:256
	global_load_dword v60, v[46:47], off offset:512
	global_load_dword v67, v[48:49], off
	global_load_dword v63, v[48:49], off offset:256
	global_load_dword v61, v[48:49], off offset:512
	global_load_dword v58, v[48:49], off offset:768
	global_load_dword v59, v[46:47], off offset:768
	s_mov_b64 s[20:21], -1
	s_and_b64 vcc, exec, s[0:1]
	s_waitcnt vmcnt(23)
	v_lshlrev_b32_e32 v46, 16, v40
	s_waitcnt vmcnt(22)
	v_lshlrev_b32_e32 v68, 16, v42
	v_and_b32_e32 v69, 0xffff0000, v42
	v_lshlrev_b32_e32 v70, 16, v43
	v_and_b32_e32 v71, 0xffff0000, v43
	v_and_b32_e32 v47, 0xffff0000, v40
	s_waitcnt vmcnt(18)
	v_cvt_pk_f32_fp8_e32 v[42:43], v52
	s_waitcnt vmcnt(17)
	v_cvt_pk_f32_fp8_e32 v[54:55], v72
	s_waitcnt vmcnt(15)
	v_cvt_pk_f32_fp8_e32 v[80:81], v82
	v_cvt_pk_f32_fp8_e32 v[76:77], v78
	s_waitcnt vmcnt(14)
	v_cvt_pk_f32_fp8_e32 v[84:85], v86
	v_cvt_pk_f32_fp8_sdwa v[78:79], v78 src0_sel:WORD_1
	v_cvt_pk_f32_fp8_sdwa v[82:83], v82 src0_sel:WORD_1
	s_waitcnt vmcnt(13)
	v_cvt_pk_f32_fp8_e32 v[88:89], v90
	v_cvt_pk_f32_fp8_sdwa v[52:53], v52 src0_sel:WORD_1
	v_cvt_pk_f32_fp8_sdwa v[72:73], v72 src0_sel:WORD_1
	v_cvt_pk_f32_fp8_sdwa v[86:87], v86 src0_sel:WORD_1
	v_cvt_pk_f32_fp8_sdwa v[90:91], v90 src0_sel:WORD_1
	v_lshlrev_b32_e32 v48, 16, v44
	v_and_b32_e32 v49, 0xffff0000, v44
	v_pk_add_f32 v[76:77], v[76:77], v[80:81]
	v_pk_add_f32 v[42:43], v[42:43], v[84:85]
	v_cvt_pk_f32_fp8_e32 v[74:75], v92
	v_pk_add_f32 v[78:79], v[78:79], v[82:83]
	v_pk_add_f32 v[82:83], v[54:55], v[88:89]
	v_pk_fma_f32 v[54:55], v[76:77], 0.5, v[46:47] op_sel_hi:[1,0,1]
	v_pk_fma_f32 v[46:47], v[42:43], 0.5, v[48:49] op_sel_hi:[1,0,1]
	s_waitcnt vmcnt(12)
	v_cvt_pk_f32_fp8_e32 v[48:49], v93
	v_lshlrev_b32_e32 v40, 16, v41
	v_and_b32_e32 v41, 0xffff0000, v41
	v_lshlrev_b32_e32 v44, 16, v45
	v_and_b32_e32 v45, 0xffff0000, v45
	v_pk_add_f32 v[80:81], v[52:53], v[86:87]
	v_pk_add_f32 v[72:73], v[72:73], v[90:91]
	v_pk_fma_f32 v[42:43], v[82:83], 0.5, v[68:69] op_sel_hi:[1,0,1]
	v_cvt_pk_f32_fp8_sdwa v[82:83], v92 src0_sel:WORD_1
	v_cvt_pk_f32_fp8_sdwa v[84:85], v93 src0_sel:WORD_1
	v_pk_fma_f32 v[52:53], v[78:79], 0.5, v[40:41] op_sel_hi:[1,0,1]
	v_pk_fma_f32 v[44:45], v[80:81], 0.5, v[44:45] op_sel_hi:[1,0,1]
	v_pk_fma_f32 v[40:41], v[72:73], 0.5, v[70:71] op_sel_hi:[1,0,1]
	v_pk_mul_f32 v[68:69], v[54:55], v[54:55]
	v_pk_mul_f32 v[72:73], v[46:47], v[46:47]
	v_pk_mul_f32 v[70:71], v[52:53], v[52:53]
	v_pk_mul_f32 v[76:77], v[44:45], v[44:45]
	v_pk_mul_f32 v[78:79], v[42:43], v[42:43]
	v_add_f32_e32 v72, v72, v73
	v_add_f32_e32 v68, v68, v69
	v_pk_mul_f32 v[80:81], v[40:41], v[40:41]
	v_lshlrev_b32_e32 v86, 16, v50
	v_and_b32_e32 v87, 0xffff0000, v50
	v_pk_add_f32 v[48:49], v[74:75], v[48:49]
	v_add_f32_e32 v72, v72, v76
	v_add_f32_e32 v68, v68, v70
	v_add_f32_e32 v69, v78, v79
	v_pk_fma_f32 v[48:49], v[48:49], 0.5, v[86:87] op_sel_hi:[1,0,1]
	v_lshlrev_b32_e32 v50, 16, v51
	v_and_b32_e32 v51, 0xffff0000, v51
	v_pk_add_f32 v[74:75], v[82:83], v[84:85]
	v_add_f32_e32 v72, v77, v72
	v_add_f32_e32 v68, v71, v68
	v_add_f32_e32 v69, v69, v80
	v_pk_fma_f32 v[50:51], v[74:75], 0.5, v[50:51] op_sel_hi:[1,0,1]
	v_pk_mul_f32 v[74:75], v[48:49], v[48:49]
	v_add_f32_e32 v68, v68, v72
	v_add_f32_e32 v69, v81, v69
	v_pk_mul_f32 v[82:83], v[50:51], v[50:51]
	v_add_f32_e32 v68, v68, v69
	v_add_f32_e32 v69, v74, v75
	v_add_f32_e32 v69, v69, v82
	v_add_f32_e32 v69, v83, v69
	v_add_f32_e32 v68, v68, v69
	s_nop 1
	s_waitcnt lgkmcnt(0)
	v_add_f32_dpp v68, v68, v68 quad_perm:[1,0,3,2] row_mask:0xf bank_mask:0xf
	s_nop 1
	s_waitcnt lgkmcnt(0)
	v_add_f32_dpp v68, v68, v68 quad_perm:[2,3,0,1] row_mask:0xf bank_mask:0xf
	s_nop 1
	s_waitcnt lgkmcnt(0)
	v_add_f32_dpp v68, v68, v68 row_half_mirror row_mask:0xf bank_mask:0xf
	s_nop 1
	s_waitcnt lgkmcnt(0)
	v_add_f32_dpp v68, v68, v68 row_mirror row_mask:0xf bank_mask:0xf
	v_mov_b32_e32 v69, v68
	s_nop 1
	v_permlane16_swap_b32_e32 v68, v69
	s_waitcnt lgkmcnt(0)
	v_add_f32_e32 v68, v68, v69
	v_mov_b32_e32 v69, v68
	s_nop 1
	v_permlane32_swap_b32_e32 v68, v69
	v_add_f32_e32 v70, v68, v69
	v_fmamk_f32 v68, v70, 0x3a800000, v218
	v_cmp_gt_f32_e64 s[8:9], s61, v68
	v_mul_f32_e32 v69, 0x4b800000, v68
	s_cbranch_vccz .LBB0_1769
; template <int PH, bool PRB = false>
; __device__ __forceinline__ void run_phase(int layer, LAS unsigned char* lds, const int wv_) {
;     ...
;                     rms_row_bf16(v, 1.0f, nullptr, hbo + (size_t)r * D, lane);
;                     if (!PRB) {
;                         const float rs8 = rsqrtf(ss * (1.0f / D) + 1e-6f); unsigned char* h8 = ws + WS_H + 32 * MiB + (size_t)r * D;
; #pragma unroll
;                         for (int j = 0; j < 4; ++j) { int w = __builtin_amdgcn_cvt_pk_fp8_f32(v[j].x * rs8, v[j].y * rs8, 0, false); w = __builtin_amdgcn_cvt_pk_fp8_f32(v[j].z * rs8, v[j].w * rs8, w, true); ((int*)h8)[lane + 64 * j] = w; }
;                     }
;                     if (lane < 16) sso[(size_t)r * 16 + lane] = lane == 0 ? ss : 0.f;
;                     if (lane == 0 && !PRB) ((float*)(ws + WS_MISC + MISC_RSROW))[r] = rsqrtf(ss * (1.0f / D) + 1e-6f);
	s_mov_b64 s[20:21], 0x4100000
	v_lshl_add_u64 v[72:73], v[56:57], 0, s[20:21]
	s_mov_b64 s[20:21], 0x4100600
	v_lshl_add_u64 v[74:75], v[56:57], 0, s[20:21]
	s_mov_b64 s[20:21], 0x4100400
	v_lshl_add_u64 v[76:77], v[56:57], 0, s[20:21]
	s_mov_b64 s[20:21], 0x4100200
	v_lshl_add_u64 v[56:57], v[56:57], 0, s[20:21]
	v_cvt_pk_bf16_f32 v78, v54, v55
	v_cvt_pk_bf16_f32 v79, v52, v53
	global_store_dwordx2 v[72:73], v[78:79], off
	v_cvt_pk_bf16_f32 v72, v46, v47
	v_cvt_pk_bf16_f32 v73, v44, v45
	global_store_dwordx2 v[56:57], v[72:73], off
	v_cvt_pk_bf16_f32 v56, v42, v43
	v_cvt_pk_bf16_f32 v57, v40, v41
	global_store_dwordx2 v[76:77], v[56:57], off
	v_cvt_pk_bf16_f32 v56, v48, v49
	v_cvt_pk_bf16_f32 v57, v50, v51
	global_store_dwordx2 v[74:75], v[56:57], off
	v_cndmask_b32_e64 v56, v68, v69, s[8:9]
	v_rsq_f32_e32 v56, v56
	v_lshl_add_u64 v[72:73], s[10:11], 0, v[30:31]
	s_mov_b32 s3, 0x2100000
	v_mul_f32_e32 v57, 0x45800000, v56
	v_cndmask_b32_e64 v56, v56, v57, s[8:9]
	v_mul_f32_e32 v57, v54, v56
	v_mul_f32_e32 v71, v55, v56
	v_cvt_pk_fp8_f32 v74, v57, v71
	v_mul_f32_e32 v57, v52, v56
	v_mul_f32_e32 v71, v53, v56
	v_add_co_u32_e32 v72, vcc, s3, v72
	v_cvt_pk_fp8_f32 v74, v57, v71 op_sel:[0,0,1]
	s_nop 0
	v_addc_co_u32_e32 v73, vcc, 0, v73, vcc
	v_mul_f32_e32 v57, v46, v56
	global_store_dword v[72:73], v74, off
	v_mul_f32_e32 v71, v47, v56
	v_cvt_pk_fp8_f32 v74, v57, v71
	v_mul_f32_e32 v57, v44, v56
	v_mul_f32_e32 v71, v45, v56
	v_cvt_pk_fp8_f32 v74, v57, v71 op_sel:[0,0,1]
	v_mul_f32_e32 v57, v42, v56
	v_mul_f32_e32 v71, v43, v56
	global_store_dword v[72:73], v74, off offset:256
	v_cvt_pk_fp8_f32 v74, v57, v71
	v_mul_f32_e32 v57, v40, v56
	v_mul_f32_e32 v71, v41, v56
	v_cvt_pk_fp8_f32 v74, v57, v71 op_sel:[0,0,1]
	v_mul_f32_e32 v57, v48, v56
	v_mul_f32_e32 v71, v49, v56
	global_store_dword v[72:73], v74, off offset:512
	v_cvt_pk_fp8_f32 v74, v57, v71
	v_mul_f32_e32 v57, v50, v56
	v_mul_f32_e32 v71, v51, v56
	v_cvt_pk_fp8_f32 v74, v57, v71 op_sel:[0,0,1]
	global_store_dword v[72:73], v74, off offset:768
	s_and_saveexec_b64 s[8:9], s[4:5]
	s_cbranch_execz .LBB0_1765
	v_cndmask_b32_e64 v57, 0, v70, s[6:7]
	v_lshl_add_u64 v[70:71], s[10:11], 0, v[28:29]
	global_store_dword v[70:71], v57, off

; template <int PH, bool PRB = false>
; __device__ __forceinline__ void run_phase(int layer, LAS unsigned char* lds, const int wv_) {
;     ...
;             for (int q = 0; q < 2; ++q) { const int r = r0 + q * NGW; if (r < S) {
;                 float4 v[4]; float ss = 0.f;
; #pragma unroll
;                 for (int j = 0; j < 4; ++j) {
;                     typedef float f2_ __attribute__((ext_vector_type(2)));
;                     const u32x2 c = cc[q][j]; const f2_ a0 = __builtin_amdgcn_cvt_pk_f32_fp8((int)aa[q][j], false), a1 = __builtin_amdgcn_cvt_pk_f32_fp8((int)aa[q][j], true), b0 = __builtin_amdgcn_cvt_pk_f32_fp8((int)bb[q][j], false), b1 = __builtin_amdgcn_cvt_pk_f32_fp8((int)bb[q][j], true);
;                     constexpr float iy = 1.0f / pg8::YS8_SCALE;
;                     v[j].x = __uint_as_float(c.x << 16) + (a0[0] + b0[0]) * iy; v[j].y = __uint_as_float(c.x & 0xffff0000u) + (a0[1] + b0[1]) * iy;
;                     v[j].z = __uint_as_float(c.y << 16) + (a1[0] + b1[0]) * iy; v[j].w = __uint_as_float(c.y & 0xffff0000u) + (a1[1] + b1[1]) * iy;
;                     ss += v[j].x * v[j].x + v[j].y * v[j].y + v[j].z * v[j].z + v[j].w * v[j].w;
;                 }
;                 ss = wave_sum(ss);
;                 if (layer == DEPTH - 1) {
;                     const float rs = rsqrtf(ss * (1.0f / D) + 1e-6f); float4* o4 = (float4*)(p.out + (size_t)r * D);
; #pragma unroll
;                     for (int j = 0; j < 4; ++j) { const float4 gg = gfin[j]; float4 o; o.x = v[j].x * rs * gg.x; o.y = v[j].y * rs * gg.y; o.z = v[j].z * rs * gg.z; o.w = v[j].w * rs * gg.w; o4[lane + 64 * j] = o; }
;                 } else {
;                     rms_row_bf16(v, 1.0f, nullptr, hbo + (size_t)r * D, lane);
;                     if (!PRB) {
;                         const float rs8 = rsqrtf(ss * (1.0f / D) + 1e-6f); unsigned char* h8 = ws + WS_H + 32 * MiB + (size_t)r * D;
; #pragma unroll
;                         for (int j = 0; j < 4; ++j) { int w = __builtin_amdgcn_cvt_pk_fp8_f32(v[j].x * rs8, v[j].y * rs8, 0, false); w = __builtin_amdgcn_cvt_pk_fp8_f32(v[j].z * rs8, v[j].w * rs8, w, true); ((int*)h8)[lane + 64 * j] = w; }
;                     }
;                     if (lane < 16) sso[(size_t)r * 16 + lane] = lane == 0 ? ss : 0.f;
;                     if (lane == 0 && !PRB) ((float*)(ws + WS_MISC + MISC_RSROW))[r] = rsqrtf(ss * (1.0f / D) + 1e-6f);
.LBB0_1771:
	v_cvt_pk_f32_fp8_e32 v[40:41], v66
	v_cvt_pk_f32_fp8_sdwa v[42:43], v66 src0_sel:WORD_1
	v_cvt_pk_f32_fp8_e32 v[44:45], v67
	v_cvt_pk_f32_fp8_sdwa v[46:47], v67 src0_sel:WORD_1
	v_lshlrev_b32_e32 v48, 16, v38
	v_and_b32_e32 v49, 0xffff0000, v38
	v_pk_add_f32 v[40:41], v[40:41], v[44:45]
	v_lshlrev_b32_e32 v38, 16, v39
	v_and_b32_e32 v39, 0xffff0000, v39
	v_pk_add_f32 v[42:43], v[42:43], v[46:47]
	v_cvt_pk_f32_fp8_sdwa v[44:45], v62 src0_sel:WORD_1
	v_cvt_pk_f32_fp8_sdwa v[52:53], v63 src0_sel:WORD_1
	v_pk_fma_f32 v[38:39], v[42:43], 0.5, v[38:39] op_sel_hi:[1,0,1]
	v_cvt_pk_f32_fp8_e32 v[42:43], v62
	v_cvt_pk_f32_fp8_e32 v[46:47], v63
	v_lshlrev_b32_e32 v54, 16, v36
	v_and_b32_e32 v55, 0xffff0000, v36
	v_lshlrev_b32_e32 v36, 16, v37
	v_and_b32_e32 v37, 0xffff0000, v37
	v_pk_add_f32 v[44:45], v[44:45], v[52:53]
	v_pk_add_f32 v[42:43], v[42:43], v[46:47]
	v_pk_fma_f32 v[36:37], v[44:45], 0.5, v[36:37] op_sel_hi:[1,0,1]
	v_cvt_pk_f32_fp8_e32 v[44:45], v60
	v_cvt_pk_f32_fp8_sdwa v[46:47], v60 src0_sel:WORD_1
	v_cvt_pk_f32_fp8_e32 v[56:57], v61
	v_cvt_pk_f32_fp8_sdwa v[60:61], v61 src0_sel:WORD_1
	v_lshlrev_b32_e32 v62, 16, v34
	v_and_b32_e32 v63, 0xffff0000, v34
	v_lshlrev_b32_e32 v34, 16, v35
	v_and_b32_e32 v35, 0xffff0000, v35
	v_pk_add_f32 v[46:47], v[46:47], v[60:61]
	v_pk_add_f32 v[44:45], v[44:45], v[56:57]
	v_pk_fma_f32 v[34:35], v[46:47], 0.5, v[34:35] op_sel_hi:[1,0,1]
	v_cvt_pk_f32_fp8_e32 v[46:47], v59
	v_cvt_pk_f32_fp8_e32 v[66:67], v58
	v_pk_fma_f32 v[40:41], v[40:41], 0.5, v[48:49] op_sel_hi:[1,0,1]
	v_pk_fma_f32 v[42:43], v[42:43], 0.5, v[54:55] op_sel_hi:[1,0,1]
	v_pk_fma_f32 v[44:45], v[44:45], 0.5, v[62:63] op_sel_hi:[1,0,1]
	v_cvt_pk_f32_fp8_sdwa v[62:63], v59 src0_sel:WORD_1
	v_cvt_pk_f32_fp8_sdwa v[58:59], v58 src0_sel:WORD_1
	v_pk_mul_f32 v[48:49], v[40:41], v[40:41]
	v_pk_mul_f32 v[52:53], v[42:43], v[42:43]
	v_pk_mul_f32 v[50:51], v[38:39], v[38:39]
	v_pk_mul_f32 v[54:55], v[36:37], v[36:37]
	v_pk_mul_f32 v[56:57], v[44:45], v[44:45]
	v_add_f32_e32 v52, v52, v53
	v_add_f32_e32 v48, v48, v49
	v_pk_mul_f32 v[60:61], v[34:35], v[34:35]
	v_lshlrev_b32_e32 v68, 16, v32
	v_and_b32_e32 v69, 0xffff0000, v32
	v_pk_add_f32 v[46:47], v[46:47], v[66:67]
	v_add_f32_e32 v52, v52, v54
	v_add_f32_e32 v48, v48, v50
	v_add_f32_e32 v49, v56, v57
	v_pk_fma_f32 v[46:47], v[46:47], 0.5, v[68:69] op_sel_hi:[1,0,1]
	v_lshlrev_b32_e32 v32, 16, v33
	v_and_b32_e32 v33, 0xffff0000, v33
	v_pk_add_f32 v[58:59], v[62:63], v[58:59]
	v_add_f32_e32 v52, v55, v52
	v_add_f32_e32 v48, v51, v48
	v_add_f32_e32 v49, v49, v60
	v_pk_fma_f32 v[32:33], v[58:59], 0.5, v[32:33] op_sel_hi:[1,0,1]
	v_pk_mul_f32 v[58:59], v[46:47], v[46:47]
	v_add_f32_e32 v48, v48, v52
	v_add_f32_e32 v49, v61, v49
	v_pk_mul_f32 v[62:63], v[32:33], v[32:33]
	v_add_f32_e32 v48, v48, v49
	v_add_f32_e32 v49, v58, v59
	v_add_f32_e32 v49, v49, v62
	v_add_f32_e32 v49, v63, v49
	v_add_f32_e32 v48, v48, v49
	s_nop 1
	s_mov_b64 s[18:19], -1
	s_andn2_b64 vcc, exec, s[0:1]
	s_waitcnt lgkmcnt(0)
	v_add_f32_dpp v48, v48, v48 quad_perm:[1,0,3,2] row_mask:0xf bank_mask:0xf
	s_nop 1
	s_waitcnt lgkmcnt(0)
	v_add_f32_dpp v48, v48, v48 quad_perm:[2,3,0,1] row_mask:0xf bank_mask:0xf
	s_nop 1
	s_waitcnt lgkmcnt(0)
	v_add_f32_dpp v48, v48, v48 row_half_mirror row_mask:0xf bank_mask:0xf
	s_nop 1
	s_waitcnt lgkmcnt(0)
	v_add_f32_dpp v48, v48, v48 row_mirror row_mask:0xf bank_mask:0xf
	v_mov_b32_e32 v49, v48
	s_nop 1
	v_permlane16_swap_b32_e32 v48, v49
	s_waitcnt lgkmcnt(0)
	v_add_f32_e32 v48, v48, v49
	v_mov_b32_e32 v49, v48
	s_nop 1
	v_permlane32_swap_b32_e32 v48, v49
	v_add_f32_e32 v50, v48, v49
	v_fmamk_f32 v48, v50, 0x3a800000, v218
	v_cmp_gt_f32_e64 s[8:9], s61, v48
	v_mul_f32_e32 v49, 0x4b800000, v48
	s_cbranch_vccnz .LBB0_1777
	v_lshl_add_u64 v[54:55], s[10:11], 0, v[26:27]
	v_add_co_u32_e32 v54, vcc, s29, v54
	v_cndmask_b32_e64 v51, v48, v49, s[8:9]
	v_cvt_pk_bf16_f32 v52, v40, v41
	s_nop 0
	v_addc_co_u32_e32 v55, vcc, 0, v55, vcc
	v_rsq_f32_e32 v51, v51
	v_cvt_pk_bf16_f32 v53, v38, v39
	global_store_dwordx2 v[54:55], v[52:53], off
	v_cvt_pk_bf16_f32 v52, v42, v43
	v_cvt_pk_bf16_f32 v53, v36, v37
	global_store_dwordx2 v[54:55], v[52:53], off offset:512
	v_cvt_pk_bf16_f32 v52, v44, v45
	v_cvt_pk_bf16_f32 v53, v34, v35
	global_store_dwordx2 v[54:55], v[52:53], off offset:1024
	v_cvt_pk_bf16_f32 v52, v46, v47
	v_cvt_pk_bf16_f32 v53, v32, v33
	global_store_dwordx2 v[54:55], v[52:53], off offset:1536
	v_mul_f32_e32 v52, 0x45800000, v51
	v_cndmask_b32_e64 v51, v51, v52, s[8:9]
	v_mul_f32_e32 v52, v40, v51
	v_mul_f32_e32 v53, v41, v51
	v_cvt_pk_fp8_f32 v54, v52, v53
	v_mul_f32_e32 v52, v38, v51
	v_mul_f32_e32 v53, v39, v51
	s_mov_b32 s3, 0x2100000
	v_cvt_pk_fp8_f32 v54, v52, v53 op_sel:[0,0,1]
	v_lshl_add_u64 v[52:53], s[10:11], 0, v[24:25]
	v_add_co_u32_e32 v52, vcc, s3, v52
	v_mul_f32_e32 v55, v43, v51
	s_nop 0
	v_addc_co_u32_e32 v53, vcc, 0, v53, vcc
	global_store_dword v[52:53], v54, off
	v_mul_f32_e32 v54, v42, v51
	v_cvt_pk_fp8_f32 v56, v54, v55
	v_mul_f32_e32 v54, v36, v51
	v_mul_f32_e32 v55, v37, v51
	v_cvt_pk_fp8_f32 v56, v54, v55 op_sel:[0,0,1]
	v_mul_f32_e32 v54, v44, v51
	v_mul_f32_e32 v55, v45, v51
	global_store_dword v[52:53], v56, off offset:256
	v_cvt_pk_fp8_f32 v56, v54, v55
	v_mul_f32_e32 v54, v34, v51
	v_mul_f32_e32 v55, v35, v51
	v_cvt_pk_fp8_f32 v56, v54, v55 op_sel:[0,0,1]
	v_mul_f32_e32 v54, v46, v51
	v_mul_f32_e32 v55, v47, v51
	global_store_dword v[52:53], v56, off offset:512
	v_cvt_pk_fp8_f32 v56, v54, v55
	v_mul_f32_e32 v54, v32, v51
	v_mul_f32_e32 v55, v33, v51
	v_cvt_pk_fp8_f32 v56, v54, v55 op_sel:[0,0,1]
	global_store_dword v[52:53], v56, off offset:768
	s_and_saveexec_b64 s[8:9], s[4:5]
	s_cbranch_execz .LBB0_1774
	v_cndmask_b32_e64 v50, 0, v50, s[6:7]
	v_lshl_add_u64 v[52:53], s[10:11], 0, v[22:23]
	global_store_dword v[52:53], v50, off

; template <int PH, bool PRB = false>
; __device__ __forceinline__ void run_phase(int layer, LAS unsigned char* lds, const int wv_) {
;     ...
;         for (int r0 = gw; r0 < S; r0 += 2 * NGW) {
;             u32x2 cc[2][4]; unsigned aa[2][4], bb[2][4];
; #pragma unroll
;             for (int q = 0; q < 2; ++q) { const int r = r0 + q * NGW < S ? r0 + q * NGW : r0;
;                 const u32x2* hr = (const u32x2*)(hb + (size_t)r * D); const unsigned* y0 = (const unsigned*)((const unsigned char*)ys + (size_t)(2 * r) * D); const unsigned* y1 = (const unsigned*)((const unsigned char*)ys + (size_t)(2 * r + 1) * D);
; #pragma unroll
;                 for (int j = 0; j < 4; ++j) { cc[q][j] = hr[lane + 64 * j]; aa[q][j] = y0[lane + 64 * j]; bb[q][j] = y1[lane + 64 * j]; } }
; #pragma unroll
;             for (int q = 0; q < 2; ++q) { const int r = r0 + q * NGW; if (r < S) {
;                 float4 v[4]; float ss = 0.f;
; #pragma unroll
;                 for (int j = 0; j < 4; ++j) {
;                     typedef float f2_ __attribute__((ext_vector_type(2)));
;                     const u32x2 c = cc[q][j]; const f2_ a0 = __builtin_amdgcn_cvt_pk_f32_fp8((int)aa[q][j], false), a1 = __builtin_amdgcn_cvt_pk_f32_fp8((int)aa[q][j], true), b0 = __builtin_amdgcn_cvt_pk_f32_fp8((int)bb[q][j], false), b1 = __builtin_amdgcn_cvt_pk_f32_fp8((int)bb[q][j], true);
;                     constexpr float iy = 1.0f / pg8::YS8_SCALE;
;                     v[j].x = __uint_as_float(c.x << 16) + (a0[0] + b0[0]) * iy; v[j].y = __uint_as_float(c.x & 0xffff0000u) + (a0[1] + b0[1]) * iy;
;                     v[j].z = __uint_as_float(c.y << 16) + (a1[0] + b1[0]) * iy; v[j].w = __uint_as_float(c.y & 0xffff0000u) + (a1[1] + b1[1]) * iy;
;                     ss += v[j].x * v[j].x + v[j].y * v[j].y + v[j].z * v[j].z + v[j].w * v[j].w;
;                 }
;                 ss = wave_sum(ss);
.LBB0_1844:
	s_add_i32 s3, s90, s2
	s_cmpk_lt_i32 s3, 0x4000
	s_cselect_b64 s[18:19], -1, 0
	v_lshl_add_u64 v[56:57], s[10:11], 0, v[20:21]
	s_and_b64 s[8:9], s[18:19], exec
	s_waitcnt vmcnt(8)
	v_add_co_u32_e32 v32, vcc, s29, v56
	s_cselect_b32 s8, s3, s2
	s_ashr_i32 s13, s12, 31
	v_addc_co_u32_e32 v33, vcc, 0, v57, vcc
	s_lshl_b64 s[20:21], s[12:13], 10
	global_load_dwordx2 v[40:41], v[32:33], off
	global_load_dwordx2 v[42:43], v[32:33], off offset:1024
	global_load_dwordx2 v[50:51], v[32:33], off offset:1536
	global_load_dwordx2 v[44:45], v[32:33], off offset:512
	v_lshl_add_u64 v[32:33], v[18:19], 0, s[20:21]
	s_add_i32 s20, s12, 1
	s_ashr_i32 s21, s20, 31
	global_load_dword v92, v[32:33], off offset:768
	global_load_dword v52, v[32:33], off offset:256
	global_load_dword v72, v[32:33], off offset:512
	s_lshl_b64 s[20:21], s[20:21], 10
	global_load_dword v78, v[32:33], off
	v_lshl_add_u64 v[32:33], v[18:19], 0, s[20:21]
	global_load_dword v82, v[32:33], off
	global_load_dword v86, v[32:33], off offset:256
	global_load_dword v90, v[32:33], off offset:512
	global_load_dword v93, v[32:33], off offset:768
	s_lshl_b32 s20, s8, 1
	s_ashr_i32 s9, s8, 31
	s_ashr_i32 s21, s20, 31
	s_or_b32 s26, s20, 1
	s_lshl_b64 s[8:9], s[8:9], 11
	s_lshl_b64 s[20:21], s[20:21], 10
	s_ashr_i32 s27, s26, 31
	v_lshl_add_u64 v[32:33], v[16:17], 0, s[8:9]
	s_lshl_b64 s[8:9], s[26:27], 10
	v_lshl_add_u64 v[46:47], v[18:19], 0, s[20:21]
	global_load_dwordx2 v[38:39], v[32:33], off
	global_load_dwordx2 v[36:37], v[32:33], off offset:512
	global_load_dwordx2 v[34:35], v[32:33], off offset:1024
	s_nop 0
	global_load_dwordx2 v[32:33], v[32:33], off offset:1536
	v_lshl_add_u64 v[48:49], v[18:19], 0, s[8:9]
	global_load_dword v66, v[46:47], off
	global_load_dword v62, v[46:47], off offset:256
	global_load_dword v60, v[46:47], off offset:512
	global_load_dword v67, v[48:49], off
	global_load_dword v63, v[48:49], off offset:256
	global_load_dword v61, v[48:49], off offset:512
	global_load_dword v58, v[48:49], off offset:768
	global_load_dword v59, v[46:47], off offset:768
	s_mov_b64 s[20:21], -1
	s_and_b64 vcc, exec, s[0:1]
	s_waitcnt vmcnt(23)
	v_lshlrev_b32_e32 v46, 16, v40
	s_waitcnt vmcnt(22)
	v_lshlrev_b32_e32 v68, 16, v42
	v_and_b32_e32 v69, 0xffff0000, v42
	v_lshlrev_b32_e32 v70, 16, v43
	v_and_b32_e32 v71, 0xffff0000, v43
	v_and_b32_e32 v47, 0xffff0000, v40
	s_waitcnt vmcnt(18)
	v_cvt_pk_f32_fp8_e32 v[42:43], v52
	s_waitcnt vmcnt(17)
	v_cvt_pk_f32_fp8_e32 v[54:55], v72
	s_waitcnt vmcnt(15)
	v_cvt_pk_f32_fp8_e32 v[80:81], v82
	v_cvt_pk_f32_fp8_e32 v[76:77], v78
	s_waitcnt vmcnt(14)
	v_cvt_pk_f32_fp8_e32 v[84:85], v86
	v_cvt_pk_f32_fp8_sdwa v[78:79], v78 src0_sel:WORD_1
	v_cvt_pk_f32_fp8_sdwa v[82:83], v82 src0_sel:WORD_1
	s_waitcnt vmcnt(13)
	v_cvt_pk_f32_fp8_e32 v[88:89], v90
	v_cvt_pk_f32_fp8_sdwa v[52:53], v52 src0_sel:WORD_1
	v_cvt_pk_f32_fp8_sdwa v[72:73], v72 src0_sel:WORD_1
	v_cvt_pk_f32_fp8_sdwa v[86:87], v86 src0_sel:WORD_1
	v_cvt_pk_f32_fp8_sdwa v[90:91], v90 src0_sel:WORD_1
	v_lshlrev_b32_e32 v48, 16, v44
	v_and_b32_e32 v49, 0xffff0000, v44
	v_pk_add_f32 v[76:77], v[76:77], v[80:81]
	v_pk_add_f32 v[42:43], v[42:43], v[84:85]
	v_cvt_pk_f32_fp8_e32 v[74:75], v92
	v_pk_add_f32 v[78:79], v[78:79], v[82:83]
	v_pk_add_f32 v[82:83], v[54:55], v[88:89]
	v_pk_fma_f32 v[54:55], v[76:77], 0.5, v[46:47] op_sel_hi:[1,0,1]
	v_pk_fma_f32 v[46:47], v[42:43], 0.5, v[48:49] op_sel_hi:[1,0,1]
	s_waitcnt vmcnt(12)
	v_cvt_pk_f32_fp8_e32 v[48:49], v93
	v_lshlrev_b32_e32 v40, 16, v41
	v_and_b32_e32 v41, 0xffff0000, v41
	v_lshlrev_b32_e32 v44, 16, v45
	v_and_b32_e32 v45, 0xffff0000, v45
	v_pk_add_f32 v[80:81], v[52:53], v[86:87]
	v_pk_add_f32 v[72:73], v[72:73], v[90:91]
	v_pk_fma_f32 v[42:43], v[82:83], 0.5, v[68:69] op_sel_hi:[1,0,1]
	v_cvt_pk_f32_fp8_sdwa v[82:83], v92 src0_sel:WORD_1
	v_cvt_pk_f32_fp8_sdwa v[84:85], v93 src0_sel:WORD_1
	v_pk_fma_f32 v[52:53], v[78:79], 0.5, v[40:41] op_sel_hi:[1,0,1]
	v_pk_fma_f32 v[44:45], v[80:81], 0.5, v[44:45] op_sel_hi:[1,0,1]
	v_pk_fma_f32 v[40:41], v[72:73], 0.5, v[70:71] op_sel_hi:[1,0,1]
	v_pk_mul_f32 v[68:69], v[54:55], v[54:55]
	v_pk_mul_f32 v[72:73], v[46:47], v[46:47]
	v_pk_mul_f32 v[70:71], v[52:53], v[52:53]
	v_pk_mul_f32 v[76:77], v[44:45], v[44:45]
	v_pk_mul_f32 v[78:79], v[42:43], v[42:43]
	v_add_f32_e32 v72, v72, v73
	v_add_f32_e32 v68, v68, v69
	v_pk_mul_f32 v[80:81], v[40:41], v[40:41]
	v_lshlrev_b32_e32 v86, 16, v50
	v_and_b32_e32 v87, 0xffff0000, v50
	v_pk_add_f32 v[48:49], v[74:75], v[48:49]
	v_add_f32_e32 v72, v72, v76
	v_add_f32_e32 v68, v68, v70
	v_add_f32_e32 v69, v78, v79
	v_pk_fma_f32 v[48:49], v[48:49], 0.5, v[86:87] op_sel_hi:[1,0,1]
	v_lshlrev_b32_e32 v50, 16, v51
	v_and_b32_e32 v51, 0xffff0000, v51
	v_pk_add_f32 v[74:75], v[82:83], v[84:85]
	v_add_f32_e32 v72, v77, v72
	v_add_f32_e32 v68, v71, v68
	v_add_f32_e32 v69, v69, v80
	v_pk_fma_f32 v[50:51], v[74:75], 0.5, v[50:51] op_sel_hi:[1,0,1]
	v_pk_mul_f32 v[74:75], v[48:49], v[48:49]
	v_add_f32_e32 v68, v68, v72
	v_add_f32_e32 v69, v81, v69
	v_pk_mul_f32 v[82:83], v[50:51], v[50:51]
	v_add_f32_e32 v68, v68, v69
	v_add_f32_e32 v69, v74, v75
	v_add_f32_e32 v69, v69, v82
	v_add_f32_e32 v69, v83, v69
	v_add_f32_e32 v68, v68, v69
	s_nop 1
	s_waitcnt lgkmcnt(0)
	v_add_f32_dpp v68, v68, v68 quad_perm:[1,0,3,2] row_mask:0xf bank_mask:0xf
	s_nop 1
	s_waitcnt lgkmcnt(0)
	v_add_f32_dpp v68, v68, v68 quad_perm:[2,3,0,1] row_mask:0xf bank_mask:0xf
	s_nop 1
	s_waitcnt lgkmcnt(0)
	v_add_f32_dpp v68, v68, v68 row_half_mirror row_mask:0xf bank_mask:0xf
	s_nop 1
	s_waitcnt lgkmcnt(0)
	v_add_f32_dpp v68, v68, v68 row_mirror row_mask:0xf bank_mask:0xf
	v_mov_b32_e32 v69, v68
	s_nop 1
	v_permlane16_swap_b32_e32 v68, v69
	s_waitcnt lgkmcnt(0)
	v_add_f32_e32 v68, v68, v69
	v_mov_b32_e32 v69, v68
	s_nop 1
	v_permlane32_swap_b32_e32 v68, v69
	v_add_f32_e32 v70, v68, v69
	v_fmamk_f32 v68, v70, 0x3a800000, v218
	v_cmp_gt_f32_e64 s[8:9], s61, v68
	v_mul_f32_e32 v69, 0x4b800000, v68
	s_cbranch_vccz .LBB0_1851
; template <int PH, bool PRB = false>
; __device__ __forceinline__ void run_phase(int layer, LAS unsigned char* lds, const int wv_) {
;     ...
;                     rms_row_bf16(v, 1.0f, nullptr, hbo + (size_t)r * D, lane);
;                     if (!PRB) {
;                         const float rs8 = rsqrtf(ss * (1.0f / D) + 1e-6f); unsigned char* h8 = ws + WS_H + 32 * MiB + (size_t)r * D;
; #pragma unroll
;                         for (int j = 0; j < 4; ++j) { int w = __builtin_amdgcn_cvt_pk_fp8_f32(v[j].x * rs8, v[j].y * rs8, 0, false); w = __builtin_amdgcn_cvt_pk_fp8_f32(v[j].z * rs8, v[j].w * rs8, w, true); ((int*)h8)[lane + 64 * j] = w; }
;                     }
;                     if (lane < 16) sso[(size_t)r * 16 + lane] = lane == 0 ? ss : 0.f;
;                     if (lane == 0 && !PRB) ((float*)(ws + WS_MISC + MISC_RSROW))[r] = rsqrtf(ss * (1.0f / D) + 1e-6f);
	s_mov_b64 s[20:21], 0x4100000
	v_lshl_add_u64 v[72:73], v[56:57], 0, s[20:21]
	s_mov_b64 s[20:21], 0x4100600
	v_lshl_add_u64 v[74:75], v[56:57], 0, s[20:21]
	s_mov_b64 s[20:21], 0x4100400
	v_lshl_add_u64 v[76:77], v[56:57], 0, s[20:21]
	s_mov_b64 s[20:21], 0x4100200
	v_lshl_add_u64 v[56:57], v[56:57], 0, s[20:21]
	v_cvt_pk_bf16_f32 v78, v54, v55
	v_cvt_pk_bf16_f32 v79, v52, v53
	global_store_dwordx2 v[72:73], v[78:79], off
	v_cvt_pk_bf16_f32 v72, v46, v47
	v_cvt_pk_bf16_f32 v73, v44, v45
	global_store_dwordx2 v[56:57], v[72:73], off
	v_cvt_pk_bf16_f32 v56, v42, v43
	v_cvt_pk_bf16_f32 v57, v40, v41
	global_store_dwordx2 v[76:77], v[56:57], off
	v_cvt_pk_bf16_f32 v56, v48, v49
	v_cvt_pk_bf16_f32 v57, v50, v51
	global_store_dwordx2 v[74:75], v[56:57], off
	v_cndmask_b32_e64 v56, v68, v69, s[8:9]
	v_rsq_f32_e32 v56, v56
	v_lshl_add_u64 v[72:73], s[10:11], 0, v[30:31]
	s_mov_b32 s3, 0x2100000
	v_mul_f32_e32 v57, 0x45800000, v56
	v_cndmask_b32_e64 v56, v56, v57, s[8:9]
	v_mul_f32_e32 v57, v54, v56
	v_mul_f32_e32 v71, v55, v56
	v_cvt_pk_fp8_f32 v74, v57, v71
	v_mul_f32_e32 v57, v52, v56
	v_mul_f32_e32 v71, v53, v56
	v_add_co_u32_e32 v72, vcc, s3, v72
	v_cvt_pk_fp8_f32 v74, v57, v71 op_sel:[0,0,1]
	s_nop 0
	v_addc_co_u32_e32 v73, vcc, 0, v73, vcc
	v_mul_f32_e32 v57, v46, v56
	global_store_dword v[72:73], v74, off
	v_mul_f32_e32 v71, v47, v56
	v_cvt_pk_fp8_f32 v74, v57, v71
	v_mul_f32_e32 v57, v44, v56
	v_mul_f32_e32 v71, v45, v56
	v_cvt_pk_fp8_f32 v74, v57, v71 op_sel:[0,0,1]
	v_mul_f32_e32 v57, v42, v56
	v_mul_f32_e32 v71, v43, v56
	global_store_dword v[72:73], v74, off offset:256
	v_cvt_pk_fp8_f32 v74, v57, v71
	v_mul_f32_e32 v57, v40, v56
	v_mul_f32_e32 v71, v41, v56
	v_cvt_pk_fp8_f32 v74, v57, v71 op_sel:[0,0,1]
	v_mul_f32_e32 v57, v48, v56
	v_mul_f32_e32 v71, v49, v56
	global_store_dword v[72:73], v74, off offset:512
	v_cvt_pk_fp8_f32 v74, v57, v71
	v_mul_f32_e32 v57, v50, v56
	v_mul_f32_e32 v71, v51, v56
	v_cvt_pk_fp8_f32 v74, v57, v71 op_sel:[0,0,1]
	global_store_dword v[72:73], v74, off offset:768
	s_and_saveexec_b64 s[8:9], s[4:5]
	s_cbranch_execz .LBB0_1847
	v_cndmask_b32_e64 v57, 0, v70, s[6:7]
	v_lshl_add_u64 v[70:71], s[10:11], 0, v[28:29]
	global_store_dword v[70:71], v57, off

; template <int PH, bool PRB = false>
; __device__ __forceinline__ void run_phase(int layer, LAS unsigned char* lds, const int wv_) {
;     ...
;             for (int q = 0; q < 2; ++q) { const int r = r0 + q * NGW; if (r < S) {
;                 float4 v[4]; float ss = 0.f;
; #pragma unroll
;                 for (int j = 0; j < 4; ++j) {
;                     typedef float f2_ __attribute__((ext_vector_type(2)));
;                     const u32x2 c = cc[q][j]; const f2_ a0 = __builtin_amdgcn_cvt_pk_f32_fp8((int)aa[q][j], false), a1 = __builtin_amdgcn_cvt_pk_f32_fp8((int)aa[q][j], true), b0 = __builtin_amdgcn_cvt_pk_f32_fp8((int)bb[q][j], false), b1 = __builtin_amdgcn_cvt_pk_f32_fp8((int)bb[q][j], true);
;                     constexpr float iy = 1.0f / pg8::YS8_SCALE;
;                     v[j].x = __uint_as_float(c.x << 16) + (a0[0] + b0[0]) * iy; v[j].y = __uint_as_float(c.x & 0xffff0000u) + (a0[1] + b0[1]) * iy;
;                     v[j].z = __uint_as_float(c.y << 16) + (a1[0] + b1[0]) * iy; v[j].w = __uint_as_float(c.y & 0xffff0000u) + (a1[1] + b1[1]) * iy;
;                     ss += v[j].x * v[j].x + v[j].y * v[j].y + v[j].z * v[j].z + v[j].w * v[j].w;
;                 }
;                 ss = wave_sum(ss);
;                 if (layer == DEPTH - 1) {
;                     const float rs = rsqrtf(ss * (1.0f / D) + 1e-6f); float4* o4 = (float4*)(p.out + (size_t)r * D);
; #pragma unroll
;                     for (int j = 0; j < 4; ++j) { const float4 gg = gfin[j]; float4 o; o.x = v[j].x * rs * gg.x; o.y = v[j].y * rs * gg.y; o.z = v[j].z * rs * gg.z; o.w = v[j].w * rs * gg.w; o4[lane + 64 * j] = o; }
;                 } else {
;                     rms_row_bf16(v, 1.0f, nullptr, hbo + (size_t)r * D, lane);
;                     if (!PRB) {
;                         const float rs8 = rsqrtf(ss * (1.0f / D) + 1e-6f); unsigned char* h8 = ws + WS_H + 32 * MiB + (size_t)r * D;
; #pragma unroll
;                         for (int j = 0; j < 4; ++j) { int w = __builtin_amdgcn_cvt_pk_fp8_f32(v[j].x * rs8, v[j].y * rs8, 0, false); w = __builtin_amdgcn_cvt_pk_fp8_f32(v[j].z * rs8, v[j].w * rs8, w, true); ((int*)h8)[lane + 64 * j] = w; }
;                     }
;                     if (lane < 16) sso[(size_t)r * 16 + lane] = lane == 0 ? ss : 0.f;
;                     if (lane == 0 && !PRB) ((float*)(ws + WS_MISC + MISC_RSROW))[r] = rsqrtf(ss * (1.0f / D) + 1e-6f);
.LBB0_1853:
	s_waitcnt vmcnt(7)
	v_cvt_pk_f32_fp8_e32 v[40:41], v66
	v_cvt_pk_f32_fp8_sdwa v[42:43], v66 src0_sel:WORD_1
	s_waitcnt vmcnt(4)
	v_cvt_pk_f32_fp8_e32 v[44:45], v67
	v_cvt_pk_f32_fp8_sdwa v[46:47], v67 src0_sel:WORD_1
	v_lshlrev_b32_e32 v48, 16, v38
	v_and_b32_e32 v49, 0xffff0000, v38
	v_pk_add_f32 v[40:41], v[40:41], v[44:45]
	v_lshlrev_b32_e32 v38, 16, v39
	v_and_b32_e32 v39, 0xffff0000, v39
	v_pk_add_f32 v[42:43], v[42:43], v[46:47]
	v_cvt_pk_f32_fp8_sdwa v[44:45], v62 src0_sel:WORD_1
	s_waitcnt vmcnt(3)
	v_cvt_pk_f32_fp8_sdwa v[52:53], v63 src0_sel:WORD_1
	v_pk_fma_f32 v[38:39], v[42:43], 0.5, v[38:39] op_sel_hi:[1,0,1]
	v_cvt_pk_f32_fp8_e32 v[42:43], v62
	v_cvt_pk_f32_fp8_e32 v[46:47], v63
	v_lshlrev_b32_e32 v54, 16, v36
	v_and_b32_e32 v55, 0xffff0000, v36
	v_lshlrev_b32_e32 v36, 16, v37
	v_and_b32_e32 v37, 0xffff0000, v37
	v_pk_add_f32 v[44:45], v[44:45], v[52:53]
	v_pk_add_f32 v[42:43], v[42:43], v[46:47]
	v_pk_fma_f32 v[36:37], v[44:45], 0.5, v[36:37] op_sel_hi:[1,0,1]
	v_cvt_pk_f32_fp8_e32 v[44:45], v60
	v_cvt_pk_f32_fp8_sdwa v[46:47], v60 src0_sel:WORD_1
	s_waitcnt vmcnt(2)
	v_cvt_pk_f32_fp8_e32 v[56:57], v61
	v_cvt_pk_f32_fp8_sdwa v[60:61], v61 src0_sel:WORD_1
	v_lshlrev_b32_e32 v62, 16, v34
	v_and_b32_e32 v63, 0xffff0000, v34
	v_lshlrev_b32_e32 v34, 16, v35
	v_and_b32_e32 v35, 0xffff0000, v35
	v_pk_add_f32 v[46:47], v[46:47], v[60:61]
	v_pk_add_f32 v[44:45], v[44:45], v[56:57]
	v_pk_fma_f32 v[34:35], v[46:47], 0.5, v[34:35] op_sel_hi:[1,0,1]
	s_waitcnt vmcnt(0)
	v_cvt_pk_f32_fp8_e32 v[46:47], v59
	v_cvt_pk_f32_fp8_e32 v[66:67], v58
	v_pk_fma_f32 v[40:41], v[40:41], 0.5, v[48:49] op_sel_hi:[1,0,1]
	v_pk_fma_f32 v[42:43], v[42:43], 0.5, v[54:55] op_sel_hi:[1,0,1]
	v_pk_fma_f32 v[44:45], v[44:45], 0.5, v[62:63] op_sel_hi:[1,0,1]
	v_cvt_pk_f32_fp8_sdwa v[62:63], v59 src0_sel:WORD_1
	v_cvt_pk_f32_fp8_sdwa v[58:59], v58 src0_sel:WORD_1
	v_pk_mul_f32 v[48:49], v[40:41], v[40:41]
	v_pk_mul_f32 v[52:53], v[42:43], v[42:43]
	v_pk_mul_f32 v[50:51], v[38:39], v[38:39]
	v_pk_mul_f32 v[54:55], v[36:37], v[36:37]
	v_pk_mul_f32 v[56:57], v[44:45], v[44:45]
	v_add_f32_e32 v52, v52, v53
	v_add_f32_e32 v48, v48, v49
	v_pk_mul_f32 v[60:61], v[34:35], v[34:35]
	v_lshlrev_b32_e32 v68, 16, v32
	v_and_b32_e32 v69, 0xffff0000, v32
	v_pk_add_f32 v[46:47], v[46:47], v[66:67]
	v_add_f32_e32 v52, v52, v54
	v_add_f32_e32 v48, v48, v50
	v_add_f32_e32 v49, v56, v57
	v_pk_fma_f32 v[46:47], v[46:47], 0.5, v[68:69] op_sel_hi:[1,0,1]
	v_lshlrev_b32_e32 v32, 16, v33
	v_and_b32_e32 v33, 0xffff0000, v33
	v_pk_add_f32 v[58:59], v[62:63], v[58:59]
	v_add_f32_e32 v52, v55, v52
	v_add_f32_e32 v48, v51, v48
	v_add_f32_e32 v49, v49, v60
	v_pk_fma_f32 v[32:33], v[58:59], 0.5, v[32:33] op_sel_hi:[1,0,1]
	v_pk_mul_f32 v[58:59], v[46:47], v[46:47]
	v_add_f32_e32 v48, v48, v52
	v_add_f32_e32 v49, v61, v49
	v_pk_mul_f32 v[62:63], v[32:33], v[32:33]
	v_add_f32_e32 v48, v48, v49
	v_add_f32_e32 v49, v58, v59
	v_add_f32_e32 v49, v49, v62
	v_add_f32_e32 v49, v63, v49
	v_add_f32_e32 v48, v48, v49
	s_nop 1
	s_mov_b64 s[18:19], -1
	s_andn2_b64 vcc, exec, s[0:1]
	s_waitcnt lgkmcnt(0)
	v_add_f32_dpp v48, v48, v48 quad_perm:[1,0,3,2] row_mask:0xf bank_mask:0xf
	s_nop 1
	s_waitcnt lgkmcnt(0)
	v_add_f32_dpp v48, v48, v48 quad_perm:[2,3,0,1] row_mask:0xf bank_mask:0xf
	s_nop 1
	s_waitcnt lgkmcnt(0)
	v_add_f32_dpp v48, v48, v48 row_half_mirror row_mask:0xf bank_mask:0xf
	s_nop 1
	s_waitcnt lgkmcnt(0)
	v_add_f32_dpp v48, v48, v48 row_mirror row_mask:0xf bank_mask:0xf
	v_mov_b32_e32 v49, v48
	s_nop 1
	v_permlane16_swap_b32_e32 v48, v49
	s_waitcnt lgkmcnt(0)
	v_add_f32_e32 v48, v48, v49
	v_mov_b32_e32 v49, v48
	s_nop 1
	v_permlane32_swap_b32_e32 v48, v49
	v_add_f32_e32 v50, v48, v49
	v_fmamk_f32 v48, v50, 0x3a800000, v218
	v_cmp_gt_f32_e64 s[8:9], s61, v48
	v_mul_f32_e32 v49, 0x4b800000, v48
	s_cbranch_vccnz .LBB0_1859
	v_lshl_add_u64 v[54:55], s[10:11], 0, v[26:27]
	v_add_co_u32_e32 v54, vcc, s29, v54
	v_cndmask_b32_e64 v51, v48, v49, s[8:9]
	v_cvt_pk_bf16_f32 v52, v40, v41
	s_nop 0
	v_addc_co_u32_e32 v55, vcc, 0, v55, vcc
	v_rsq_f32_e32 v51, v51
	v_cvt_pk_bf16_f32 v53, v38, v39
	global_store_dwordx2 v[54:55], v[52:53], off
	v_cvt_pk_bf16_f32 v52, v42, v43
	v_cvt_pk_bf16_f32 v53, v36, v37
	global_store_dwordx2 v[54:55], v[52:53], off offset:512
	v_cvt_pk_bf16_f32 v52, v44, v45
	v_cvt_pk_bf16_f32 v53, v34, v35
	global_store_dwordx2 v[54:55], v[52:53], off offset:1024
	v_cvt_pk_bf16_f32 v52, v46, v47
	v_cvt_pk_bf16_f32 v53, v32, v33
	global_store_dwordx2 v[54:55], v[52:53], off offset:1536
	v_mul_f32_e32 v52, 0x45800000, v51
	v_cndmask_b32_e64 v51, v51, v52, s[8:9]
	v_mul_f32_e32 v52, v40, v51
	v_mul_f32_e32 v53, v41, v51
	v_cvt_pk_fp8_f32 v54, v52, v53
	v_mul_f32_e32 v52, v38, v51
	v_mul_f32_e32 v53, v39, v51
	s_mov_b32 s3, 0x2100000
	v_cvt_pk_fp8_f32 v54, v52, v53 op_sel:[0,0,1]
	v_lshl_add_u64 v[52:53], s[10:11], 0, v[24:25]
	v_add_co_u32_e32 v52, vcc, s3, v52
	v_mul_f32_e32 v55, v43, v51
	s_nop 0
	v_addc_co_u32_e32 v53, vcc, 0, v53, vcc
	global_store_dword v[52:53], v54, off
	v_mul_f32_e32 v54, v42, v51
	v_cvt_pk_fp8_f32 v56, v54, v55
	v_mul_f32_e32 v54, v36, v51
	v_mul_f32_e32 v55, v37, v51
	v_cvt_pk_fp8_f32 v56, v54, v55 op_sel:[0,0,1]
	v_mul_f32_e32 v54, v44, v51
	v_mul_f32_e32 v55, v45, v51
	global_store_dword v[52:53], v56, off offset:256
	v_cvt_pk_fp8_f32 v56, v54, v55
	v_mul_f32_e32 v54, v34, v51
	v_mul_f32_e32 v55, v35, v51
	v_cvt_pk_fp8_f32 v56, v54, v55 op_sel:[0,0,1]
	v_mul_f32_e32 v54, v46, v51
	v_mul_f32_e32 v55, v47, v51
	global_store_dword v[52:53], v56, off offset:512
	v_cvt_pk_fp8_f32 v56, v54, v55
	v_mul_f32_e32 v54, v32, v51
	v_mul_f32_e32 v55, v33, v51
	v_cvt_pk_fp8_f32 v56, v54, v55 op_sel:[0,0,1]
	global_store_dword v[52:53], v56, off offset:768
	s_and_saveexec_b64 s[8:9], s[4:5]
	s_cbranch_execz .LBB0_1856
	v_cndmask_b32_e64 v50, 0, v50, s[6:7]
	v_lshl_add_u64 v[52:53], s[10:11], 0, v[22:23]
	global_store_dword v[52:53], v50, off
